# attention unit output stores as 16-byte stores after permlane32_swap lane exchange (MLA/SB/SWA/diff); claim tickets collected late; diff gain vectors + pmax table + MLAUP rope rows + layer-0 x convers
# speedup vs baseline: 1.0615x; 1.0150x over previous
; #define GAS __attribute__((address_space(1)))
; __device__ __forceinline__ unsigned cvt_pk_bf16(float lo, float hi) { f32x2 v = {lo, hi}; bf16x2_t b = __builtin_convertvector(v, bf16x2_t); return __builtin_bit_cast(unsigned, b); }
; __device__ __forceinline__ unsigned pk_fp8x4(float a, float b, float c_, float d) { int p = __builtin_amdgcn_cvt_pk_fp8_f32(a, b, 0, false); p = __builtin_amdgcn_cvt_pk_fp8_f32(c_, d, p, true); return (unsigned)p; }
; __device__ __forceinline__ void phase_conv(LAS unsigned char* lds, int wv, int l) {
;     ...
;         const float* x = a->in[0]; bf16_t* XB = (bf16_t*)(F.ws + WS_XB);
;         for (size_t i = (size_t)gw * 64 + F.lane; i < (size_t)M * D / 8; i += (size_t)NGW * 64) { const f32x4 v0 = *(const f32x4*)(x + i * 8), v1 = *(const f32x4*)(x + i * 8 + 4);
;             *(GAS u32x4*)(XB + i * 8) = (u32x4){cvt_pk_bf16(v0[0], v0[1]), cvt_pk_bf16(v0[2], v0[3]), cvt_pk_bf16(v1[0], v1[1]), cvt_pk_bf16(v1[2], v1[3])};
;             *(GAS u32x2*)((unsigned char*)(F.ws + WS_XB8) + i * 8) = (u32x2){pk_fp8x4(v0[0], v0[1], v0[2], v0[3]), pk_fp8x4(v1[0], v1[1], v1[2], v1[3])}; }
.Lxb_batch:
	s_lshl_b64 s[2:3], s[14:15], 3
	s_sub_u32 s2, s2, s14
	s_subb_u32 s3, s3, s15
	v_lshl_add_u64 v[96:97], v[0:1], 0, s[2:3]
	s_mov_b64 s[2:3], 0x1fffff
	v_cmp_ge_u64_e32 vcc, s[2:3], v[96:97]
	s_nop 1
	s_cmp_eq_u64 vcc, exec
	s_cbranch_scc0 .Lxb_rest
	v_mov_b64_e32 v[96:97], v[6:7]
	global_load_dwordx4 v[36:39], v[96:97], off
	global_load_dwordx4 v[32:35], v[96:97], off offset:-16
	v_lshl_add_u64 v[96:97], v[96:97], 0, s[38:39]
	global_load_dwordx4 v[44:47], v[96:97], off
	global_load_dwordx4 v[40:43], v[96:97], off offset:-16
	v_lshl_add_u64 v[96:97], v[96:97], 0, s[38:39]
	global_load_dwordx4 v[52:55], v[96:97], off
	global_load_dwordx4 v[48:51], v[96:97], off offset:-16
	v_lshl_add_u64 v[96:97], v[96:97], 0, s[38:39]
	global_load_dwordx4 v[60:63], v[96:97], off
	global_load_dwordx4 v[56:59], v[96:97], off offset:-16
	v_lshl_add_u64 v[96:97], v[96:97], 0, s[38:39]
	global_load_dwordx4 v[68:71], v[96:97], off
	global_load_dwordx4 v[64:67], v[96:97], off offset:-16
	v_lshl_add_u64 v[96:97], v[96:97], 0, s[38:39]
	global_load_dwordx4 v[76:79], v[96:97], off
	global_load_dwordx4 v[72:75], v[96:97], off offset:-16
	v_lshl_add_u64 v[96:97], v[96:97], 0, s[38:39]
	global_load_dwordx4 v[84:87], v[96:97], off
	global_load_dwordx4 v[80:83], v[96:97], off offset:-16
	v_lshl_add_u64 v[96:97], v[96:97], 0, s[38:39]
	global_load_dwordx4 v[92:95], v[96:97], off
	global_load_dwordx4 v[88:91], v[96:97], off offset:-16
	v_lshl_add_u64 v[96:97], v[96:97], 0, s[38:39]
	v_mov_b64_e32 v[6:7], v[96:97]
	s_waitcnt vmcnt(14)
	v_cvt_pk_bf16_f32 v98, v32, v33
	v_cvt_pk_bf16_f32 v99, v34, v35
	v_cvt_pk_bf16_f32 v100, v36, v37
	v_cvt_pk_bf16_f32 v101, v38, v39
	global_store_dwordx4 v[4:5], v[98:101], off
	v_lshl_add_u64 v[4:5], v[4:5], 0, s[34:35]
	v_mov_b32_e32 v102, v31
	v_mov_b32_e32 v103, v31
	v_cvt_pk_fp8_f32 v102, v32, v33
	v_cvt_pk_fp8_f32 v103, v36, v37
	s_nop 0
	v_cvt_pk_fp8_f32 v102, v34, v35 op_sel:[0,0,1]
	v_cvt_pk_fp8_f32 v103, v38, v39 op_sel:[0,0,1]
	s_nop 0
	global_store_dwordx2 v[2:3], v[102:103], off
	v_lshl_add_u64 v[2:3], v[2:3], 0, s[16:17]
	s_waitcnt vmcnt(14)
	v_cvt_pk_bf16_f32 v98, v40, v41
	v_cvt_pk_bf16_f32 v99, v42, v43
	v_cvt_pk_bf16_f32 v100, v44, v45
	v_cvt_pk_bf16_f32 v101, v46, v47
	global_store_dwordx4 v[4:5], v[98:101], off
	v_lshl_add_u64 v[4:5], v[4:5], 0, s[34:35]
	v_mov_b32_e32 v102, v31
	v_mov_b32_e32 v103, v31
	v_cvt_pk_fp8_f32 v102, v40, v41
	v_cvt_pk_fp8_f32 v103, v44, v45
	s_nop 0
	v_cvt_pk_fp8_f32 v102, v42, v43 op_sel:[0,0,1]
	v_cvt_pk_fp8_f32 v103, v46, v47 op_sel:[0,0,1]
	s_nop 0
	global_store_dwordx2 v[2:3], v[102:103], off
	v_lshl_add_u64 v[2:3], v[2:3], 0, s[16:17]
	s_waitcnt vmcnt(14)
	v_cvt_pk_bf16_f32 v98, v48, v49
	v_cvt_pk_bf16_f32 v99, v50, v51
	v_cvt_pk_bf16_f32 v100, v52, v53
	v_cvt_pk_bf16_f32 v101, v54, v55
	global_store_dwordx4 v[4:5], v[98:101], off
	v_lshl_add_u64 v[4:5], v[4:5], 0, s[34:35]
	v_mov_b32_e32 v102, v31
	v_mov_b32_e32 v103, v31
	v_cvt_pk_fp8_f32 v102, v48, v49
	v_cvt_pk_fp8_f32 v103, v52, v53
	s_nop 0
	v_cvt_pk_fp8_f32 v102, v50, v51 op_sel:[0,0,1]
	v_cvt_pk_fp8_f32 v103, v54, v55 op_sel:[0,0,1]
	s_nop 0
	global_store_dwordx2 v[2:3], v[102:103], off
	v_lshl_add_u64 v[2:3], v[2:3], 0, s[16:17]
	s_waitcnt vmcnt(14)
	v_cvt_pk_bf16_f32 v98, v56, v57
	v_cvt_pk_bf16_f32 v99, v58, v59
	v_cvt_pk_bf16_f32 v100, v60, v61
	v_cvt_pk_bf16_f32 v101, v62, v63
	global_store_dwordx4 v[4:5], v[98:101], off
	v_lshl_add_u64 v[4:5], v[4:5], 0, s[34:35]
	v_mov_b32_e32 v102, v31
	v_mov_b32_e32 v103, v31
	v_cvt_pk_fp8_f32 v102, v56, v57
	v_cvt_pk_fp8_f32 v103, v60, v61
	s_nop 0
	v_cvt_pk_fp8_f32 v102, v58, v59 op_sel:[0,0,1]
	v_cvt_pk_fp8_f32 v103, v62, v63 op_sel:[0,0,1]
	s_nop 0
	global_store_dwordx2 v[2:3], v[102:103], off
	v_lshl_add_u64 v[2:3], v[2:3], 0, s[16:17]
	s_waitcnt vmcnt(14)
	v_cvt_pk_bf16_f32 v98, v64, v65
	v_cvt_pk_bf16_f32 v99, v66, v67
	v_cvt_pk_bf16_f32 v100, v68, v69
	v_cvt_pk_bf16_f32 v101, v70, v71
	global_store_dwordx4 v[4:5], v[98:101], off
	v_lshl_add_u64 v[4:5], v[4:5], 0, s[34:35]
	v_mov_b32_e32 v102, v31
	v_mov_b32_e32 v103, v31
	v_cvt_pk_fp8_f32 v102, v64, v65
	v_cvt_pk_fp8_f32 v103, v68, v69
	s_nop 0
	v_cvt_pk_fp8_f32 v102, v66, v67 op_sel:[0,0,1]
	v_cvt_pk_fp8_f32 v103, v70, v71 op_sel:[0,0,1]
	s_nop 0
	global_store_dwordx2 v[2:3], v[102:103], off
	v_lshl_add_u64 v[2:3], v[2:3], 0, s[16:17]
	s_waitcnt vmcnt(14)
	v_cvt_pk_bf16_f32 v98, v72, v73
	v_cvt_pk_bf16_f32 v99, v74, v75
	v_cvt_pk_bf16_f32 v100, v76, v77
	v_cvt_pk_bf16_f32 v101, v78, v79
	global_store_dwordx4 v[4:5], v[98:101], off
	v_lshl_add_u64 v[4:5], v[4:5], 0, s[34:35]
	v_mov_b32_e32 v102, v31
	v_mov_b32_e32 v103, v31
	v_cvt_pk_fp8_f32 v102, v72, v73
	v_cvt_pk_fp8_f32 v103, v76, v77
	s_nop 0
	v_cvt_pk_fp8_f32 v102, v74, v75 op_sel:[0,0,1]
	v_cvt_pk_fp8_f32 v103, v78, v79 op_sel:[0,0,1]
	s_nop 0
	global_store_dwordx2 v[2:3], v[102:103], off
	v_lshl_add_u64 v[2:3], v[2:3], 0, s[16:17]
	s_waitcnt vmcnt(14)
	v_cvt_pk_bf16_f32 v98, v80, v81
	v_cvt_pk_bf16_f32 v99, v82, v83
	v_cvt_pk_bf16_f32 v100, v84, v85
	v_cvt_pk_bf16_f32 v101, v86, v87
	global_store_dwordx4 v[4:5], v[98:101], off
	v_lshl_add_u64 v[4:5], v[4:5], 0, s[34:35]
	v_mov_b32_e32 v102, v31
	v_mov_b32_e32 v103, v31
	v_cvt_pk_fp8_f32 v102, v80, v81
	v_cvt_pk_fp8_f32 v103, v84, v85
	s_nop 0
	v_cvt_pk_fp8_f32 v102, v82, v83 op_sel:[0,0,1]
	v_cvt_pk_fp8_f32 v103, v86, v87 op_sel:[0,0,1]
	s_nop 0
	global_store_dwordx2 v[2:3], v[102:103], off
	v_lshl_add_u64 v[2:3], v[2:3], 0, s[16:17]
	s_waitcnt vmcnt(14)
	v_cvt_pk_bf16_f32 v98, v88, v89
	v_cvt_pk_bf16_f32 v99, v90, v91
	v_cvt_pk_bf16_f32 v100, v92, v93
	v_cvt_pk_bf16_f32 v101, v94, v95
	global_store_dwordx4 v[4:5], v[98:101], off
	v_lshl_add_u64 v[4:5], v[4:5], 0, s[34:35]
	v_mov_b32_e32 v102, v31
	v_mov_b32_e32 v103, v31
	v_cvt_pk_fp8_f32 v102, v88, v89
	v_cvt_pk_fp8_f32 v103, v92, v93
	s_nop 0
	v_cvt_pk_fp8_f32 v102, v90, v91 op_sel:[0,0,1]
	v_cvt_pk_fp8_f32 v103, v94, v95 op_sel:[0,0,1]
	s_nop 0
	global_store_dwordx2 v[2:3], v[102:103], off
	v_lshl_add_u64 v[2:3], v[2:3], 0, s[16:17]
	s_lshl_b64 s[2:3], s[14:15], 3
	v_lshl_add_u64 v[0:1], v[0:1], 0, s[2:3]
	s_branch .Lxb_batch
.Lxb_rest:
	s_mov_b64 s[2:3], 0x200000
	v_cmp_gt_u64_e32 vcc, s[2:3], v[0:1]
	s_nop 1
	s_and_b64 exec, exec, vcc
	s_cbranch_execz .LBB0_215

; __device__ __forceinline__ unsigned cvt_pk_bf16(float lo, float hi) { f32x2 v = {lo, hi}; bf16x2_t b = __builtin_convertvector(v, bf16x2_t); return __builtin_bit_cast(unsigned, b); }
;     __device__ __forceinline__ void operator()(const f32x4 (&acc)[2][2][4][2], const u32x2 (&pf)[8], const g8::Unit& u, int wr, int wc, int fr, int fq) const {
;     ...
;                 if (u.pn == 1) {
;                     const float rq = __builtin_amdgcn_rsqf(sq.x * (1.f / 256.f) + 1e-6f) * SCALE_A;
;                     const float* cp = cs + ((size_t)(row % S) * 16 + 4 * fq) * 2;
;                     const f32x4 c0 = *(const f32x4*)cp, c1 = *(const f32x4*)(cp + 4);
;                     const float cc[4] = {c0[0], c0[2], c1[0], c1[2]}, sn[4] = {c0[1], c0[3], c1[1], c1[3]};
;                     {   const f32x4 t1 = acc[ai][0][m][0] * rq, t2 = acc[ai][0][m][1] * rq;
;                         float o1[4], o2[4];
; #pragma unroll
;                         for (int j = 0; j < 4; ++j) { o1[j] = t1[j] * cc[j] - t2[j] * sn[j]; o2[j] = t1[j] * sn[j] + t2[j] * cc[j]; }
;                         bf16_t* qp = QA + (size_t)row * 384 + wc * 96 + 64 + 4 * fq;
;                         *(u32x2*)qp = (u32x2){cvt_pk_bf16(o1[0], o1[1]), cvt_pk_bf16(o1[2], o1[3])};
;                         *(u32x2*)(qp + 16) = (u32x2){cvt_pk_bf16(o2[0], o2[1]), cvt_pk_bf16(o2[2], o2[3])}; }
;                     {   const bf16_t* hp = H + (size_t)row * HP + C_KR + 4 * fq;
;                         const u32x2 a = *(const u32x2*)hp, b = *(const u32x2*)(hp + 16);
;                         const float t1[4] = {__uint_as_float(a.x << 16), __uint_as_float(a.x & 0xffff0000u), __uint_as_float(a.y << 16), __uint_as_float(a.y & 0xffff0000u)};
;                         const float t2[4] = {__uint_as_float(b.x << 16), __uint_as_float(b.x & 0xffff0000u), __uint_as_float(b.y << 16), __uint_as_float(b.y & 0xffff0000u)};
;                         float o1[4], o2[4];
; #pragma unroll
;                         for (int j = 0; j < 4; ++j) { o1[j] = t1[j] * cc[j] - t2[j] * sn[j]; o2[j] = t1[j] * sn[j] + t2[j] * cc[j]; }
;                         bf16_t* kp = KA + (size_t)row * 384 + wc * 96 + 64 + 4 * fq;
;                         *(u32x2*)kp = (u32x2){cvt_pk_bf16(o1[0], o1[1]), cvt_pk_bf16(o1[2], o1[3])};
;                         *(u32x2*)(kp + 16) = (u32x2){cvt_pk_bf16(o2[0], o2[1]), cvt_pk_bf16(o2[2], o2[3])}; }
.LBB0_563:
	s_cmp_eq_u32 s67, 1
	s_mov_b64 s[14:15], -1
	s_cbranch_scc0 .LBB0_565
	v_lshlrev_b32_e32 v198, 1, v5
	v_mov_b32_e32 v199, v31
	v_mov_b32_e32 v4, v164
	v_ashrrev_i32_e32 v196, 31, v4
	v_lshrrev_b32_e32 v196, 19, v196
	v_add_u32_e32 v196, v4, v196
	v_and_b32_e32 v196, 0xffffe000, v196
	v_sub_u32_e32 v196, v4, v196
	v_ashrrev_i32_e32 v197, 31, v196
	v_lshlrev_b64 v[196:197], 7, v[196:197]
	v_lshl_add_u64 v[196:197], s[46:47], 0, v[196:197]
	v_lshl_add_u64 v[196:197], v[196:197], 0, v[30:31]
	global_load_dwordx4 v[206:209], v[196:197], off offset:16
	global_load_dwordx4 v[210:213], v[196:197], off
	v_mov_b64_e32 v[196:197], s[44:45]
	v_mad_i64_i32 v[196:197], s[14:15], v4, s33, v[196:197]
	v_lshl_add_u64 v[196:197], v[196:197], 0, v[198:199]
	global_load_dwordx2 v[214:215], v[196:197], off offset:768
	global_load_dwordx2 v[216:217], v[196:197], off offset:800
	v_add_u32_e32 v4, 0x10, v164
	v_ashrrev_i32_e32 v196, 31, v4
	v_lshrrev_b32_e32 v196, 19, v196
	v_add_u32_e32 v196, v4, v196
	v_and_b32_e32 v196, 0xffffe000, v196
	v_sub_u32_e32 v196, v4, v196
	v_ashrrev_i32_e32 v197, 31, v196
	v_lshlrev_b64 v[196:197], 7, v[196:197]
	v_lshl_add_u64 v[196:197], s[46:47], 0, v[196:197]
	v_lshl_add_u64 v[196:197], v[196:197], 0, v[30:31]
	global_load_dwordx4 v[218:221], v[196:197], off offset:16
	global_load_dwordx4 v[222:225], v[196:197], off
	v_mov_b64_e32 v[196:197], s[44:45]
	v_mad_i64_i32 v[196:197], s[14:15], v4, s33, v[196:197]
	v_lshl_add_u64 v[196:197], v[196:197], 0, v[198:199]
	global_load_dwordx2 v[226:227], v[196:197], off offset:768
	global_load_dwordx2 v[228:229], v[196:197], off offset:800
	v_add_u32_e32 v4, 0x20, v164
	v_ashrrev_i32_e32 v196, 31, v4
	v_lshrrev_b32_e32 v196, 19, v196
	v_add_u32_e32 v196, v4, v196
	v_and_b32_e32 v196, 0xffffe000, v196
	v_sub_u32_e32 v196, v4, v196
	v_ashrrev_i32_e32 v197, 31, v196
	v_lshlrev_b64 v[196:197], 7, v[196:197]
	v_lshl_add_u64 v[196:197], s[46:47], 0, v[196:197]
	v_lshl_add_u64 v[196:197], v[196:197], 0, v[30:31]
	global_load_dwordx4 v[230:233], v[196:197], off offset:16
	global_load_dwordx4 v[234:237], v[196:197], off
	v_mov_b64_e32 v[196:197], s[44:45]
	v_mad_i64_i32 v[196:197], s[14:15], v4, s33, v[196:197]
	v_lshl_add_u64 v[196:197], v[196:197], 0, v[198:199]
	global_load_dwordx2 v[238:239], v[196:197], off offset:768
	global_load_dwordx2 v[240:241], v[196:197], off offset:800
	v_add_u32_e32 v4, 0x30, v164
	v_ashrrev_i32_e32 v196, 31, v4
	v_lshrrev_b32_e32 v196, 19, v196
	v_add_u32_e32 v196, v4, v196
	v_and_b32_e32 v196, 0xffffe000, v196
	v_sub_u32_e32 v196, v4, v196
	v_ashrrev_i32_e32 v197, 31, v196
	v_lshlrev_b64 v[196:197], 7, v[196:197]
	v_lshl_add_u64 v[196:197], s[46:47], 0, v[196:197]
	v_lshl_add_u64 v[196:197], v[196:197], 0, v[30:31]
	global_load_dwordx4 v[242:245], v[196:197], off offset:16
	global_load_dwordx4 v[188:191], v[196:197], off
	v_mov_b64_e32 v[196:197], s[44:45]
	v_mad_i64_i32 v[196:197], s[14:15], v4, s33, v[196:197]
	v_lshl_add_u64 v[196:197], v[196:197], 0, v[198:199]
	global_load_dwordx2 v[192:193], v[196:197], off offset:768
	global_load_dwordx2 v[194:195], v[196:197], off offset:800
	v_fmamk_f32 v132, v176, 0x3b800000, v246
	v_rsq_f32_e32 v132, v132
	v_lshlrev_b32_e32 v186, 1, v5
	v_mov_b32_e32 v187, v31
	v_mul_f32_e32 v150, 0x3e16c740, v132
	v_ashrrev_i32_e32 v132, 31, v164
	v_lshrrev_b32_e32 v132, 19, v132
	v_add_u32_e32 v132, v164, v132
	v_and_b32_e32 v132, 0xffffe000, v132
	v_sub_u32_e32 v132, v164, v132
	v_ashrrev_i32_e32 v133, 31, v132
	v_lshlrev_b64 v[132:133], 7, v[132:133]
	v_lshl_add_u64 v[132:133], s[46:47], 0, v[132:133]
	v_lshl_add_u64 v[136:137], v[132:133], 0, v[30:31]
	s_waitcnt vmcnt(14)
	v_mov_b64_e32 v[132:133], v[206:207]
	v_mov_b64_e32 v[134:135], v[208:209]
	v_mov_b64_e32 v[136:137], v[210:211]
	v_mov_b64_e32 v[138:139], v[212:213]
	v_pk_mul_f32 v[154:155], v[150:151], v[124:125] op_sel_hi:[0,1]
	v_pk_mul_f32 v[152:153], v[150:151], v[128:129] op_sel_hi:[0,1]
	v_pk_mul_f32 v[184:185], v[150:151], v[126:127] op_sel_hi:[0,1]
	v_mov_b32_e32 v178, v137
	v_mov_b32_e32 v137, v138
	v_mov_b32_e32 v179, v139
	v_pk_mul_f32 v[138:139], v[154:155], v[136:137]
	s_nop 0
	v_pk_fma_f32 v[180:181], v[152:153], v[178:179], v[138:139]
	v_pk_mul_f32 v[138:139], v[154:155], v[178:179]
	v_pk_mul_f32 v[154:155], v[150:151], v[130:131] op_sel_hi:[0,1]
	v_pk_fma_f32 v[152:153], v[152:153], v[136:137], v[138:139] neg_lo:[0,0,1] neg_hi:[0,0,1]
	v_mov_b32_e32 v138, v133
	v_mov_b32_e32 v139, v135
	v_mov_b32_e32 v133, v134
	v_pk_mul_f32 v[134:135], v[184:185], v[132:133]
	v_pk_mul_f32 v[184:185], v[184:185], v[138:139]
	v_pk_fma_f32 v[134:135], v[154:155], v[138:139], v[134:135]
	v_pk_fma_f32 v[154:155], v[154:155], v[132:133], v[184:185] neg_lo:[0,0,1] neg_hi:[0,0,1]
	v_mov_b64_e32 v[184:185], s[54:55]
	v_mad_i64_i32 v[184:185], s[14:15], v164, s0, v[184:185]
	v_lshl_add_u64 v[184:185], v[184:185], 0, v[186:187]
	v_cvt_pk_bf16_f32 v152, v152, v153
	v_cvt_pk_bf16_f32 v153, v154, v155
	global_store_dwordx2 v[184:185], v[152:153], off offset:128
	v_cvt_pk_bf16_f32 v153, v134, v135
	v_mov_b64_e32 v[134:135], s[44:45]
	v_cvt_pk_bf16_f32 v152, v180, v181
	v_mad_i64_i32 v[134:135], s[14:15], v164, s33, v[134:135]
	global_store_dwordx2 v[184:185], v[152:153], off offset:160
	v_lshl_add_u64 v[134:135], v[134:135], 0, v[186:187]
	s_waitcnt vmcnt(14)
	v_mov_b64_e32 v[152:153], v[214:215]
	v_mov_b64_e32 v[134:135], v[216:217]
	v_lshlrev_b32_e32 v154, 16, v152
	v_lshlrev_b32_e32 v180, 16, v134
	v_and_b32_e32 v181, 0xffff0000, v134
	v_and_b32_e32 v155, 0xffff0000, v152
	v_pk_mul_f32 v[184:185], v[136:137], v[180:181]
	v_lshlrev_b32_e32 v134, 16, v135
	v_pk_fma_f32 v[184:185], v[178:179], v[154:155], v[184:185]
	v_pk_mul_f32 v[178:179], v[178:179], v[180:181]
	v_and_b32_e32 v135, 0xffff0000, v135
	v_pk_fma_f32 v[136:137], v[136:137], v[154:155], v[178:179] neg_lo:[0,0,1] neg_hi:[0,0,1]
	v_lshlrev_b32_e32 v152, 16, v153
	v_and_b32_e32 v153, 0xffff0000, v153
	v_pk_mul_f32 v[154:155], v[132:133], v[134:135]
	v_pk_mul_f32 v[134:135], v[138:139], v[134:135]
	v_pk_fma_f32 v[154:155], v[138:139], v[152:153], v[154:155]
	v_pk_fma_f32 v[132:133], v[132:133], v[152:153], v[134:135] neg_lo:[0,0,1] neg_hi:[0,0,1]
	v_mov_b64_e32 v[134:135], s[56:57]
	v_mad_i64_i32 v[134:135], s[14:15], v164, s0, v[134:135]
	v_lshl_add_u64 v[134:135], v[134:135], 0, v[186:187]
	v_cvt_pk_bf16_f32 v136, v136, v137
	v_cvt_pk_bf16_f32 v137, v132, v133
	v_cvt_pk_bf16_f32 v132, v184, v185
	v_cvt_pk_bf16_f32 v133, v154, v155
	global_store_dwordx2 v[134:135], v[136:137], off offset:128
	global_store_dwordx2 v[134:135], v[132:133], off offset:160
	s_mov_b64 s[14:15], 0

; __device__ __forceinline__ unsigned cvt_pk_bf16(float lo, float hi) { f32x2 v = {lo, hi}; bf16x2_t b = __builtin_convertvector(v, bf16x2_t); return __builtin_bit_cast(unsigned, b); }
;     __device__ __forceinline__ void operator()(const f32x4 (&acc)[2][2][4][2], const u32x2 (&pf)[8], const g8::Unit& u, int wr, int wc, int fr, int fq) const {
;     ...
;                 if (u.pn == 1) {
;                     const float rq = __builtin_amdgcn_rsqf(sq.x * (1.f / 256.f) + 1e-6f) * SCALE_A;
;                     const float* cp = cs + ((size_t)(row % S) * 16 + 4 * fq) * 2;
;                     const f32x4 c0 = *(const f32x4*)cp, c1 = *(const f32x4*)(cp + 4);
;                     const float cc[4] = {c0[0], c0[2], c1[0], c1[2]}, sn[4] = {c0[1], c0[3], c1[1], c1[3]};
;                     {   const f32x4 t1 = acc[ai][0][m][0] * rq, t2 = acc[ai][0][m][1] * rq;
;                         float o1[4], o2[4];
; #pragma unroll
;                         for (int j = 0; j < 4; ++j) { o1[j] = t1[j] * cc[j] - t2[j] * sn[j]; o2[j] = t1[j] * sn[j] + t2[j] * cc[j]; }
;                         bf16_t* qp = QA + (size_t)row * 384 + wc * 96 + 64 + 4 * fq;
;                         *(u32x2*)qp = (u32x2){cvt_pk_bf16(o1[0], o1[1]), cvt_pk_bf16(o1[2], o1[3])};
;                         *(u32x2*)(qp + 16) = (u32x2){cvt_pk_bf16(o2[0], o2[1]), cvt_pk_bf16(o2[2], o2[3])}; }
;                     {   const bf16_t* hp = H + (size_t)row * HP + C_KR + 4 * fq;
;                         const u32x2 a = *(const u32x2*)hp, b = *(const u32x2*)(hp + 16);
;                         const float t1[4] = {__uint_as_float(a.x << 16), __uint_as_float(a.x & 0xffff0000u), __uint_as_float(a.y << 16), __uint_as_float(a.y & 0xffff0000u)};
;                         const float t2[4] = {__uint_as_float(b.x << 16), __uint_as_float(b.x & 0xffff0000u), __uint_as_float(b.y << 16), __uint_as_float(b.y & 0xffff0000u)};
;                         float o1[4], o2[4];
; #pragma unroll
;                         for (int j = 0; j < 4; ++j) { o1[j] = t1[j] * cc[j] - t2[j] * sn[j]; o2[j] = t1[j] * sn[j] + t2[j] * cc[j]; }
;                         bf16_t* kp = KA + (size_t)row * 384 + wc * 96 + 64 + 4 * fq;
;                         *(u32x2*)kp = (u32x2){cvt_pk_bf16(o1[0], o1[1]), cvt_pk_bf16(o1[2], o1[3])};
;                         *(u32x2*)(kp + 16) = (u32x2){cvt_pk_bf16(o2[0], o2[1]), cvt_pk_bf16(o2[2], o2[3])}; }
.LBB0_568:
	s_cmp_eq_u32 s67, 1
	s_mov_b64 s[14:15], -1
	s_cbranch_scc0 .LBB0_570
	v_fmamk_f32 v116, v174, 0x3b800000, v246
	v_rsq_f32_e32 v116, v116
	v_lshlrev_b32_e32 v136, 1, v5
	v_mov_b32_e32 v137, v31
	v_mul_f32_e32 v128, 0x3e16c740, v116
	v_ashrrev_i32_e32 v116, 31, v124
	v_lshrrev_b32_e32 v116, 19, v116
	v_add_u32_e32 v116, v124, v116
	v_and_b32_e32 v116, 0xffffe000, v116
	v_sub_u32_e32 v116, v124, v116
	v_ashrrev_i32_e32 v117, 31, v116
	v_lshlrev_b64 v[116:117], 7, v[116:117]
	v_lshl_add_u64 v[116:117], s[46:47], 0, v[116:117]
	v_lshl_add_u64 v[120:121], v[116:117], 0, v[30:31]
	s_waitcnt vmcnt(14)
	v_mov_b64_e32 v[116:117], v[218:219]
	v_mov_b64_e32 v[118:119], v[220:221]
	v_mov_b64_e32 v[120:121], v[222:223]
	v_mov_b64_e32 v[122:123], v[224:225]
	v_pk_mul_f32 v[132:133], v[128:129], v[108:109] op_sel_hi:[0,1]
	v_pk_mul_f32 v[130:131], v[128:129], v[112:113] op_sel_hi:[0,1]
	v_mov_b32_e32 v126, v121
	v_mov_b32_e32 v121, v122
	v_mov_b32_e32 v127, v123
	v_pk_mul_f32 v[122:123], v[132:133], v[120:121]
	s_nop 0
	v_pk_fma_f32 v[134:135], v[130:131], v[126:127], v[122:123]
	v_pk_mul_f32 v[122:123], v[132:133], v[126:127]
	v_pk_mul_f32 v[132:133], v[128:129], v[114:115] op_sel_hi:[0,1]
	v_pk_fma_f32 v[130:131], v[130:131], v[120:121], v[122:123] neg_lo:[0,0,1] neg_hi:[0,0,1]
	v_pk_mul_f32 v[128:129], v[128:129], v[110:111] op_sel_hi:[0,1]
	v_mov_b32_e32 v122, v117
	v_mov_b32_e32 v123, v119
	v_mov_b32_e32 v117, v118
	v_pk_mul_f32 v[118:119], v[128:129], v[116:117]
	v_pk_mul_f32 v[128:129], v[128:129], v[122:123]
	v_pk_fma_f32 v[118:119], v[132:133], v[122:123], v[118:119]
	v_pk_fma_f32 v[128:129], v[132:133], v[116:117], v[128:129] neg_lo:[0,0,1] neg_hi:[0,0,1]
	v_mov_b64_e32 v[132:133], s[54:55]
	v_mad_i64_i32 v[132:133], s[14:15], v124, s0, v[132:133]
	v_cvt_pk_bf16_f32 v130, v130, v131
	v_cvt_pk_bf16_f32 v131, v128, v129
	v_cvt_pk_bf16_f32 v129, v118, v119
	v_mov_b64_e32 v[118:119], s[44:45]
	v_lshl_add_u64 v[132:133], v[132:133], 0, v[136:137]
	v_cvt_pk_bf16_f32 v128, v134, v135
	v_mad_i64_i32 v[118:119], s[14:15], v124, s33, v[118:119]
	global_store_dwordx2 v[132:133], v[130:131], off offset:128
	global_store_dwordx2 v[132:133], v[128:129], off offset:160
	v_lshl_add_u64 v[118:119], v[118:119], 0, v[136:137]
	s_waitcnt vmcnt(14)
	v_mov_b64_e32 v[128:129], v[226:227]
	v_mov_b64_e32 v[118:119], v[228:229]
	v_lshlrev_b32_e32 v130, 16, v128
	v_lshlrev_b32_e32 v132, 16, v118
	v_and_b32_e32 v133, 0xffff0000, v118
	v_and_b32_e32 v131, 0xffff0000, v128
	v_pk_mul_f32 v[134:135], v[120:121], v[132:133]
	v_lshlrev_b32_e32 v118, 16, v119
	v_pk_fma_f32 v[134:135], v[126:127], v[130:131], v[134:135]
	v_pk_mul_f32 v[126:127], v[126:127], v[132:133]
	v_and_b32_e32 v119, 0xffff0000, v119
	v_pk_fma_f32 v[120:121], v[120:121], v[130:131], v[126:127] neg_lo:[0,0,1] neg_hi:[0,0,1]
	v_lshlrev_b32_e32 v126, 16, v129
	v_and_b32_e32 v127, 0xffff0000, v129
	v_pk_mul_f32 v[128:129], v[116:117], v[118:119]
	v_pk_mul_f32 v[118:119], v[122:123], v[118:119]
	v_pk_fma_f32 v[128:129], v[122:123], v[126:127], v[128:129]
	v_pk_fma_f32 v[116:117], v[116:117], v[126:127], v[118:119] neg_lo:[0,0,1] neg_hi:[0,0,1]
	v_mov_b64_e32 v[118:119], s[56:57]
	v_mad_i64_i32 v[118:119], s[14:15], v124, s0, v[118:119]
	v_lshl_add_u64 v[118:119], v[118:119], 0, v[136:137]
	v_cvt_pk_bf16_f32 v120, v120, v121
	v_cvt_pk_bf16_f32 v121, v116, v117
	v_cvt_pk_bf16_f32 v116, v134, v135
	v_cvt_pk_bf16_f32 v117, v128, v129
	global_store_dwordx2 v[118:119], v[120:121], off offset:128
	global_store_dwordx2 v[118:119], v[116:117], off offset:160
	s_mov_b64 s[14:15], 0

; __device__ __forceinline__ unsigned cvt_pk_bf16(float lo, float hi) { f32x2 v = {lo, hi}; bf16x2_t b = __builtin_convertvector(v, bf16x2_t); return __builtin_bit_cast(unsigned, b); }
;     __device__ __forceinline__ void operator()(const f32x4 (&acc)[2][2][4][2], const u32x2 (&pf)[8], const g8::Unit& u, int wr, int wc, int fr, int fq) const {
;     ...
;                 if (u.pn == 1) {
;                     const float rq = __builtin_amdgcn_rsqf(sq.x * (1.f / 256.f) + 1e-6f) * SCALE_A;
;                     const float* cp = cs + ((size_t)(row % S) * 16 + 4 * fq) * 2;
;                     const f32x4 c0 = *(const f32x4*)cp, c1 = *(const f32x4*)(cp + 4);
;                     const float cc[4] = {c0[0], c0[2], c1[0], c1[2]}, sn[4] = {c0[1], c0[3], c1[1], c1[3]};
;                     {   const f32x4 t1 = acc[ai][0][m][0] * rq, t2 = acc[ai][0][m][1] * rq;
;                         float o1[4], o2[4];
; #pragma unroll
;                         for (int j = 0; j < 4; ++j) { o1[j] = t1[j] * cc[j] - t2[j] * sn[j]; o2[j] = t1[j] * sn[j] + t2[j] * cc[j]; }
;                         bf16_t* qp = QA + (size_t)row * 384 + wc * 96 + 64 + 4 * fq;
;                         *(u32x2*)qp = (u32x2){cvt_pk_bf16(o1[0], o1[1]), cvt_pk_bf16(o1[2], o1[3])};
;                         *(u32x2*)(qp + 16) = (u32x2){cvt_pk_bf16(o2[0], o2[1]), cvt_pk_bf16(o2[2], o2[3])}; }
;                     {   const bf16_t* hp = H + (size_t)row * HP + C_KR + 4 * fq;
;                         const u32x2 a = *(const u32x2*)hp, b = *(const u32x2*)(hp + 16);
;                         const float t1[4] = {__uint_as_float(a.x << 16), __uint_as_float(a.x & 0xffff0000u), __uint_as_float(a.y << 16), __uint_as_float(a.y & 0xffff0000u)};
;                         const float t2[4] = {__uint_as_float(b.x << 16), __uint_as_float(b.x & 0xffff0000u), __uint_as_float(b.y << 16), __uint_as_float(b.y & 0xffff0000u)};
;                         float o1[4], o2[4];
; #pragma unroll
;                         for (int j = 0; j < 4; ++j) { o1[j] = t1[j] * cc[j] - t2[j] * sn[j]; o2[j] = t1[j] * sn[j] + t2[j] * cc[j]; }
;                         bf16_t* kp = KA + (size_t)row * 384 + wc * 96 + 64 + 4 * fq;
;                         *(u32x2*)kp = (u32x2){cvt_pk_bf16(o1[0], o1[1]), cvt_pk_bf16(o1[2], o1[3])};
;                         *(u32x2*)(kp + 16) = (u32x2){cvt_pk_bf16(o2[0], o2[1]), cvt_pk_bf16(o2[2], o2[3])}; }
.LBB0_595:
	s_cmp_eq_u32 s67, 1
	s_mov_b64 s[14:15], -1
	s_cbranch_scc0 .LBB0_597
	v_fmamk_f32 v100, v172, 0x3b800000, v246
	v_rsq_f32_e32 v100, v100
	v_lshlrev_b32_e32 v120, 1, v5
	v_mov_b32_e32 v121, v31
	v_mul_f32_e32 v112, 0x3e16c740, v100
	v_ashrrev_i32_e32 v100, 31, v108
	v_lshrrev_b32_e32 v100, 19, v100
	v_add_u32_e32 v100, v108, v100
	v_and_b32_e32 v100, 0xffffe000, v100
	v_sub_u32_e32 v100, v108, v100
	v_ashrrev_i32_e32 v101, 31, v100
	v_lshlrev_b64 v[100:101], 7, v[100:101]
	v_lshl_add_u64 v[100:101], s[46:47], 0, v[100:101]
	v_lshl_add_u64 v[104:105], v[100:101], 0, v[30:31]
	s_waitcnt vmcnt(14)
	v_mov_b64_e32 v[100:101], v[230:231]
	v_mov_b64_e32 v[102:103], v[232:233]
	v_mov_b64_e32 v[104:105], v[234:235]
	v_mov_b64_e32 v[106:107], v[236:237]
	v_pk_mul_f32 v[116:117], v[112:113], v[92:93] op_sel_hi:[0,1]
	v_pk_mul_f32 v[114:115], v[112:113], v[96:97] op_sel_hi:[0,1]
	v_mov_b32_e32 v110, v105
	v_mov_b32_e32 v105, v106
	v_mov_b32_e32 v111, v107
	v_pk_mul_f32 v[106:107], v[116:117], v[104:105]
	s_nop 0
	v_pk_fma_f32 v[118:119], v[114:115], v[110:111], v[106:107]
	v_pk_mul_f32 v[106:107], v[116:117], v[110:111]
	v_pk_mul_f32 v[116:117], v[112:113], v[98:99] op_sel_hi:[0,1]
	v_pk_fma_f32 v[114:115], v[114:115], v[104:105], v[106:107] neg_lo:[0,0,1] neg_hi:[0,0,1]
	v_pk_mul_f32 v[112:113], v[112:113], v[94:95] op_sel_hi:[0,1]
	v_mov_b32_e32 v106, v101
	v_mov_b32_e32 v107, v103
	v_mov_b32_e32 v101, v102
	v_pk_mul_f32 v[102:103], v[112:113], v[100:101]
	v_pk_mul_f32 v[112:113], v[112:113], v[106:107]
	v_pk_fma_f32 v[102:103], v[116:117], v[106:107], v[102:103]
	v_pk_fma_f32 v[112:113], v[116:117], v[100:101], v[112:113] neg_lo:[0,0,1] neg_hi:[0,0,1]
	v_mov_b64_e32 v[116:117], s[54:55]
	v_mad_i64_i32 v[116:117], s[14:15], v108, s0, v[116:117]
	v_cvt_pk_bf16_f32 v114, v114, v115
	v_cvt_pk_bf16_f32 v115, v112, v113
	v_cvt_pk_bf16_f32 v113, v102, v103
	v_mov_b64_e32 v[102:103], s[44:45]
	v_lshl_add_u64 v[116:117], v[116:117], 0, v[120:121]
	v_cvt_pk_bf16_f32 v112, v118, v119
	v_mad_i64_i32 v[102:103], s[14:15], v108, s33, v[102:103]
	global_store_dwordx2 v[116:117], v[114:115], off offset:128
	global_store_dwordx2 v[116:117], v[112:113], off offset:160
	v_lshl_add_u64 v[102:103], v[102:103], 0, v[120:121]
	s_waitcnt vmcnt(14)
	v_mov_b64_e32 v[112:113], v[238:239]
	v_mov_b64_e32 v[102:103], v[240:241]
	v_lshlrev_b32_e32 v114, 16, v112
	v_lshlrev_b32_e32 v116, 16, v102
	v_and_b32_e32 v117, 0xffff0000, v102
	v_and_b32_e32 v115, 0xffff0000, v112
	v_pk_mul_f32 v[118:119], v[104:105], v[116:117]
	v_lshlrev_b32_e32 v102, 16, v103
	v_pk_fma_f32 v[118:119], v[110:111], v[114:115], v[118:119]
	v_pk_mul_f32 v[110:111], v[110:111], v[116:117]
	v_and_b32_e32 v103, 0xffff0000, v103
	v_pk_fma_f32 v[104:105], v[104:105], v[114:115], v[110:111] neg_lo:[0,0,1] neg_hi:[0,0,1]
	v_lshlrev_b32_e32 v110, 16, v113
	v_and_b32_e32 v111, 0xffff0000, v113
	v_pk_mul_f32 v[112:113], v[100:101], v[102:103]
	v_pk_mul_f32 v[102:103], v[106:107], v[102:103]
	v_pk_fma_f32 v[112:113], v[106:107], v[110:111], v[112:113]
	v_pk_fma_f32 v[100:101], v[100:101], v[110:111], v[102:103] neg_lo:[0,0,1] neg_hi:[0,0,1]
	v_mov_b64_e32 v[102:103], s[56:57]
	v_mad_i64_i32 v[102:103], s[14:15], v108, s0, v[102:103]
	v_lshl_add_u64 v[102:103], v[102:103], 0, v[120:121]
	v_cvt_pk_bf16_f32 v104, v104, v105
	v_cvt_pk_bf16_f32 v105, v100, v101
	v_cvt_pk_bf16_f32 v100, v118, v119
	v_cvt_pk_bf16_f32 v101, v112, v113
	global_store_dwordx2 v[102:103], v[104:105], off offset:128
	global_store_dwordx2 v[102:103], v[100:101], off offset:160
	s_mov_b64 s[14:15], 0

; __device__ __forceinline__ unsigned cvt_pk_bf16(float lo, float hi) { f32x2 v = {lo, hi}; bf16x2_t b = __builtin_convertvector(v, bf16x2_t); return __builtin_bit_cast(unsigned, b); }
;     __device__ __forceinline__ void operator()(const f32x4 (&acc)[2][2][4][2], const u32x2 (&pf)[8], const g8::Unit& u, int wr, int wc, int fr, int fq) const {
;     ...
;                 if (u.pn == 1) {
;                     const float rq = __builtin_amdgcn_rsqf(sq.x * (1.f / 256.f) + 1e-6f) * SCALE_A;
;                     const float* cp = cs + ((size_t)(row % S) * 16 + 4 * fq) * 2;
;                     const f32x4 c0 = *(const f32x4*)cp, c1 = *(const f32x4*)(cp + 4);
;                     const float cc[4] = {c0[0], c0[2], c1[0], c1[2]}, sn[4] = {c0[1], c0[3], c1[1], c1[3]};
;                     {   const f32x4 t1 = acc[ai][0][m][0] * rq, t2 = acc[ai][0][m][1] * rq;
;                         float o1[4], o2[4];
; #pragma unroll
;                         for (int j = 0; j < 4; ++j) { o1[j] = t1[j] * cc[j] - t2[j] * sn[j]; o2[j] = t1[j] * sn[j] + t2[j] * cc[j]; }
;                         bf16_t* qp = QA + (size_t)row * 384 + wc * 96 + 64 + 4 * fq;
;                         *(u32x2*)qp = (u32x2){cvt_pk_bf16(o1[0], o1[1]), cvt_pk_bf16(o1[2], o1[3])};
;                         *(u32x2*)(qp + 16) = (u32x2){cvt_pk_bf16(o2[0], o2[1]), cvt_pk_bf16(o2[2], o2[3])}; }
;                     {   const bf16_t* hp = H + (size_t)row * HP + C_KR + 4 * fq;
;                         const u32x2 a = *(const u32x2*)hp, b = *(const u32x2*)(hp + 16);
;                         const float t1[4] = {__uint_as_float(a.x << 16), __uint_as_float(a.x & 0xffff0000u), __uint_as_float(a.y << 16), __uint_as_float(a.y & 0xffff0000u)};
;                         const float t2[4] = {__uint_as_float(b.x << 16), __uint_as_float(b.x & 0xffff0000u), __uint_as_float(b.y << 16), __uint_as_float(b.y & 0xffff0000u)};
;                         float o1[4], o2[4];
; #pragma unroll
;                         for (int j = 0; j < 4; ++j) { o1[j] = t1[j] * cc[j] - t2[j] * sn[j]; o2[j] = t1[j] * sn[j] + t2[j] * cc[j]; }
;                         bf16_t* kp = KA + (size_t)row * 384 + wc * 96 + 64 + 4 * fq;
;                         *(u32x2*)kp = (u32x2){cvt_pk_bf16(o1[0], o1[1]), cvt_pk_bf16(o1[2], o1[3])};
;                         *(u32x2*)(kp + 16) = (u32x2){cvt_pk_bf16(o2[0], o2[1]), cvt_pk_bf16(o2[2], o2[3])}; }
.LBB0_622:
	s_cmp_eq_u32 s67, 1
	s_mov_b64 s[14:15], -1
	s_cbranch_scc0 .LBB0_624
	v_fmamk_f32 v84, v170, 0x3b800000, v246
	v_rsq_f32_e32 v84, v84
	v_lshlrev_b32_e32 v104, 1, v5
	v_mov_b32_e32 v105, v31
	v_mul_f32_e32 v96, 0x3e16c740, v84
	v_ashrrev_i32_e32 v84, 31, v92
	v_lshrrev_b32_e32 v84, 19, v84
	v_add_u32_e32 v84, v92, v84
	v_and_b32_e32 v84, 0xffffe000, v84
	v_sub_u32_e32 v84, v92, v84
	v_ashrrev_i32_e32 v85, 31, v84
	v_lshlrev_b64 v[84:85], 7, v[84:85]
	v_lshl_add_u64 v[84:85], s[46:47], 0, v[84:85]
	v_lshl_add_u64 v[88:89], v[84:85], 0, v[30:31]
	s_waitcnt vmcnt(14)
	v_mov_b64_e32 v[84:85], v[242:243]
	v_mov_b64_e32 v[86:87], v[244:245]
	v_mov_b64_e32 v[88:89], v[188:189]
	v_mov_b64_e32 v[90:91], v[190:191]
	v_pk_mul_f32 v[100:101], v[96:97], v[76:77] op_sel_hi:[0,1]
	v_pk_mul_f32 v[98:99], v[96:97], v[80:81] op_sel_hi:[0,1]
	v_mov_b32_e32 v94, v89
	v_mov_b32_e32 v89, v90
	v_mov_b32_e32 v95, v91
	v_pk_mul_f32 v[90:91], v[100:101], v[88:89]
	s_nop 0
	v_pk_fma_f32 v[102:103], v[98:99], v[94:95], v[90:91]
	v_pk_mul_f32 v[90:91], v[100:101], v[94:95]
	v_pk_mul_f32 v[100:101], v[96:97], v[82:83] op_sel_hi:[0,1]
	v_pk_fma_f32 v[98:99], v[98:99], v[88:89], v[90:91] neg_lo:[0,0,1] neg_hi:[0,0,1]
	v_pk_mul_f32 v[96:97], v[96:97], v[78:79] op_sel_hi:[0,1]
	v_mov_b32_e32 v90, v85
	v_mov_b32_e32 v91, v87
	v_mov_b32_e32 v85, v86
	v_pk_mul_f32 v[86:87], v[96:97], v[84:85]
	v_pk_mul_f32 v[96:97], v[96:97], v[90:91]
	v_pk_fma_f32 v[86:87], v[100:101], v[90:91], v[86:87]
	v_pk_fma_f32 v[96:97], v[100:101], v[84:85], v[96:97] neg_lo:[0,0,1] neg_hi:[0,0,1]
	v_mov_b64_e32 v[100:101], s[54:55]
	v_mad_i64_i32 v[100:101], s[14:15], v92, s0, v[100:101]
	v_cvt_pk_bf16_f32 v98, v98, v99
	v_cvt_pk_bf16_f32 v99, v96, v97
	v_cvt_pk_bf16_f32 v97, v86, v87
	v_mov_b64_e32 v[86:87], s[44:45]
	v_lshl_add_u64 v[100:101], v[100:101], 0, v[104:105]
	v_cvt_pk_bf16_f32 v96, v102, v103
	v_mad_i64_i32 v[86:87], s[14:15], v92, s33, v[86:87]
	global_store_dwordx2 v[100:101], v[98:99], off offset:128
	global_store_dwordx2 v[100:101], v[96:97], off offset:160
	v_lshl_add_u64 v[86:87], v[86:87], 0, v[104:105]
	s_waitcnt vmcnt(14)
	v_mov_b64_e32 v[96:97], v[192:193]
	v_mov_b64_e32 v[86:87], v[194:195]
	v_lshlrev_b32_e32 v98, 16, v96
	v_lshlrev_b32_e32 v100, 16, v86
	v_and_b32_e32 v101, 0xffff0000, v86
	v_and_b32_e32 v99, 0xffff0000, v96
	v_pk_mul_f32 v[102:103], v[88:89], v[100:101]
	v_lshlrev_b32_e32 v86, 16, v87
	v_pk_fma_f32 v[102:103], v[94:95], v[98:99], v[102:103]
	v_pk_mul_f32 v[94:95], v[94:95], v[100:101]
	v_and_b32_e32 v87, 0xffff0000, v87
	v_pk_fma_f32 v[88:89], v[88:89], v[98:99], v[94:95] neg_lo:[0,0,1] neg_hi:[0,0,1]
	v_lshlrev_b32_e32 v94, 16, v97
	v_and_b32_e32 v95, 0xffff0000, v97
	v_pk_mul_f32 v[96:97], v[84:85], v[86:87]
	v_pk_mul_f32 v[86:87], v[90:91], v[86:87]
	v_pk_fma_f32 v[96:97], v[90:91], v[94:95], v[96:97]
	v_pk_fma_f32 v[84:85], v[84:85], v[94:95], v[86:87] neg_lo:[0,0,1] neg_hi:[0,0,1]
	v_mov_b64_e32 v[86:87], s[56:57]
	v_mad_i64_i32 v[86:87], s[14:15], v92, s0, v[86:87]
	v_lshl_add_u64 v[86:87], v[86:87], 0, v[104:105]
	v_cvt_pk_bf16_f32 v88, v88, v89
	v_cvt_pk_bf16_f32 v89, v84, v85
	v_cvt_pk_bf16_f32 v84, v102, v103
	v_cvt_pk_bf16_f32 v85, v96, v97
	global_store_dwordx2 v[86:87], v[88:89], off offset:128
	global_store_dwordx2 v[86:87], v[84:85], off offset:160
	s_mov_b64 s[14:15], 0

; __device__ __forceinline__ unsigned cvt_pk_bf16(float lo, float hi) { f32x2 v = {lo, hi}; bf16x2_t b = __builtin_convertvector(v, bf16x2_t); return __builtin_bit_cast(unsigned, b); }
;     __device__ __forceinline__ void operator()(const f32x4 (&acc)[2][2][4][2], const u32x2 (&pf)[8], const g8::Unit& u, int wr, int wc, int fr, int fq) const {
;     ...
;                 if (u.pn == 1) {
;                     const float rq = __builtin_amdgcn_rsqf(sq.x * (1.f / 256.f) + 1e-6f) * SCALE_A;
;                     const float* cp = cs + ((size_t)(row % S) * 16 + 4 * fq) * 2;
;                     const f32x4 c0 = *(const f32x4*)cp, c1 = *(const f32x4*)(cp + 4);
;                     const float cc[4] = {c0[0], c0[2], c1[0], c1[2]}, sn[4] = {c0[1], c0[3], c1[1], c1[3]};
;                     {   const f32x4 t1 = acc[ai][0][m][0] * rq, t2 = acc[ai][0][m][1] * rq;
;                         float o1[4], o2[4];
; #pragma unroll
;                         for (int j = 0; j < 4; ++j) { o1[j] = t1[j] * cc[j] - t2[j] * sn[j]; o2[j] = t1[j] * sn[j] + t2[j] * cc[j]; }
;                         bf16_t* qp = QA + (size_t)row * 384 + wc * 96 + 64 + 4 * fq;
;                         *(u32x2*)qp = (u32x2){cvt_pk_bf16(o1[0], o1[1]), cvt_pk_bf16(o1[2], o1[3])};
;                         *(u32x2*)(qp + 16) = (u32x2){cvt_pk_bf16(o2[0], o2[1]), cvt_pk_bf16(o2[2], o2[3])}; }
;                     {   const bf16_t* hp = H + (size_t)row * HP + C_KR + 4 * fq;
;                         const u32x2 a = *(const u32x2*)hp, b = *(const u32x2*)(hp + 16);
;                         const float t1[4] = {__uint_as_float(a.x << 16), __uint_as_float(a.x & 0xffff0000u), __uint_as_float(a.y << 16), __uint_as_float(a.y & 0xffff0000u)};
;                         const float t2[4] = {__uint_as_float(b.x << 16), __uint_as_float(b.x & 0xffff0000u), __uint_as_float(b.y << 16), __uint_as_float(b.y & 0xffff0000u)};
;                         float o1[4], o2[4];
; #pragma unroll
;                         for (int j = 0; j < 4; ++j) { o1[j] = t1[j] * cc[j] - t2[j] * sn[j]; o2[j] = t1[j] * sn[j] + t2[j] * cc[j]; }
;                         bf16_t* kp = KA + (size_t)row * 384 + wc * 96 + 64 + 4 * fq;
;                         *(u32x2*)kp = (u32x2){cvt_pk_bf16(o1[0], o1[1]), cvt_pk_bf16(o1[2], o1[3])};
;                         *(u32x2*)(kp + 16) = (u32x2){cvt_pk_bf16(o2[0], o2[1]), cvt_pk_bf16(o2[2], o2[3])}; }
.LBB0_649:
	s_cmp_eq_u32 s67, 1
	s_mov_b64 s[14:15], -1
	s_cbranch_scc0 .LBB0_651
	v_lshlrev_b32_e32 v198, 1, v5
	v_mov_b32_e32 v199, v31
	v_add_u32_e32 v4, 0x80, v164
	v_ashrrev_i32_e32 v196, 31, v4
	v_lshrrev_b32_e32 v196, 19, v196
	v_add_u32_e32 v196, v4, v196
	v_and_b32_e32 v196, 0xffffe000, v196
	v_sub_u32_e32 v196, v4, v196
	v_ashrrev_i32_e32 v197, 31, v196
	v_lshlrev_b64 v[196:197], 7, v[196:197]
	v_lshl_add_u64 v[196:197], s[46:47], 0, v[196:197]
	v_lshl_add_u64 v[196:197], v[196:197], 0, v[30:31]
	global_load_dwordx4 v[206:209], v[196:197], off offset:16
	global_load_dwordx4 v[210:213], v[196:197], off
	v_mov_b64_e32 v[196:197], s[44:45]
	v_mad_i64_i32 v[196:197], s[14:15], v4, s33, v[196:197]
	v_lshl_add_u64 v[196:197], v[196:197], 0, v[198:199]
	global_load_dwordx2 v[214:215], v[196:197], off offset:768
	global_load_dwordx2 v[216:217], v[196:197], off offset:800
	v_add_u32_e32 v4, 0x90, v164
	v_ashrrev_i32_e32 v196, 31, v4
	v_lshrrev_b32_e32 v196, 19, v196
	v_add_u32_e32 v196, v4, v196
	v_and_b32_e32 v196, 0xffffe000, v196
	v_sub_u32_e32 v196, v4, v196
	v_ashrrev_i32_e32 v197, 31, v196
	v_lshlrev_b64 v[196:197], 7, v[196:197]
	v_lshl_add_u64 v[196:197], s[46:47], 0, v[196:197]
	v_lshl_add_u64 v[196:197], v[196:197], 0, v[30:31]
	global_load_dwordx4 v[218:221], v[196:197], off offset:16
	global_load_dwordx4 v[222:225], v[196:197], off
	v_mov_b64_e32 v[196:197], s[44:45]
	v_mad_i64_i32 v[196:197], s[14:15], v4, s33, v[196:197]
	v_lshl_add_u64 v[196:197], v[196:197], 0, v[198:199]
	global_load_dwordx2 v[226:227], v[196:197], off offset:768
	global_load_dwordx2 v[228:229], v[196:197], off offset:800
	v_add_u32_e32 v4, 0xa0, v164
	v_ashrrev_i32_e32 v196, 31, v4
	v_lshrrev_b32_e32 v196, 19, v196
	v_add_u32_e32 v196, v4, v196
	v_and_b32_e32 v196, 0xffffe000, v196
	v_sub_u32_e32 v196, v4, v196
	v_ashrrev_i32_e32 v197, 31, v196
	v_lshlrev_b64 v[196:197], 7, v[196:197]
	v_lshl_add_u64 v[196:197], s[46:47], 0, v[196:197]
	v_lshl_add_u64 v[196:197], v[196:197], 0, v[30:31]
	global_load_dwordx4 v[230:233], v[196:197], off offset:16
	global_load_dwordx4 v[234:237], v[196:197], off
	v_mov_b64_e32 v[196:197], s[44:45]
	v_mad_i64_i32 v[196:197], s[14:15], v4, s33, v[196:197]
	v_lshl_add_u64 v[196:197], v[196:197], 0, v[198:199]
	global_load_dwordx2 v[238:239], v[196:197], off offset:768
	global_load_dwordx2 v[240:241], v[196:197], off offset:800
	v_add_u32_e32 v4, 0xb0, v164
	v_ashrrev_i32_e32 v196, 31, v4
	v_lshrrev_b32_e32 v196, 19, v196
	v_add_u32_e32 v196, v4, v196
	v_and_b32_e32 v196, 0xffffe000, v196
	v_sub_u32_e32 v196, v4, v196
	v_ashrrev_i32_e32 v197, 31, v196
	v_lshlrev_b64 v[196:197], 7, v[196:197]
	v_lshl_add_u64 v[196:197], s[46:47], 0, v[196:197]
	v_lshl_add_u64 v[196:197], v[196:197], 0, v[30:31]
	global_load_dwordx4 v[242:245], v[196:197], off offset:16
	global_load_dwordx4 v[188:191], v[196:197], off
	v_mov_b64_e32 v[196:197], s[44:45]
	v_mad_i64_i32 v[196:197], s[14:15], v4, s33, v[196:197]
	v_lshl_add_u64 v[196:197], v[196:197], 0, v[198:199]
	global_load_dwordx2 v[192:193], v[196:197], off offset:768
	global_load_dwordx2 v[194:195], v[196:197], off offset:800
	v_fmamk_f32 v68, v168, 0x3b800000, v246
	v_rsq_f32_e32 v68, v68
	v_lshlrev_b32_e32 v88, 1, v5
	v_mov_b32_e32 v89, v31
	v_mul_f32_e32 v80, 0x3e16c740, v68
	v_ashrrev_i32_e32 v68, 31, v76
	v_lshrrev_b32_e32 v68, 19, v68
	v_add_u32_e32 v68, v76, v68
	v_and_b32_e32 v68, 0xffffe000, v68
	v_sub_u32_e32 v68, v76, v68
	v_ashrrev_i32_e32 v69, 31, v68
	v_lshlrev_b64 v[68:69], 7, v[68:69]
	v_lshl_add_u64 v[68:69], s[46:47], 0, v[68:69]
	v_lshl_add_u64 v[72:73], v[68:69], 0, v[30:31]
	s_waitcnt vmcnt(14)
	v_mov_b64_e32 v[68:69], v[206:207]
	v_mov_b64_e32 v[70:71], v[208:209]
	v_mov_b64_e32 v[72:73], v[210:211]
	v_mov_b64_e32 v[74:75], v[212:213]
	v_pk_mul_f32 v[84:85], v[80:81], v[60:61] op_sel_hi:[0,1]
	v_pk_mul_f32 v[82:83], v[80:81], v[64:65] op_sel_hi:[0,1]
	v_mov_b32_e32 v78, v73
	v_mov_b32_e32 v73, v74
	v_mov_b32_e32 v79, v75
	v_pk_mul_f32 v[74:75], v[84:85], v[72:73]
	s_nop 0
	v_pk_fma_f32 v[86:87], v[82:83], v[78:79], v[74:75]
	v_pk_mul_f32 v[74:75], v[84:85], v[78:79]
	v_pk_mul_f32 v[84:85], v[80:81], v[66:67] op_sel_hi:[0,1]
	v_pk_fma_f32 v[82:83], v[82:83], v[72:73], v[74:75] neg_lo:[0,0,1] neg_hi:[0,0,1]
	v_pk_mul_f32 v[80:81], v[80:81], v[62:63] op_sel_hi:[0,1]
	v_mov_b32_e32 v74, v69
	v_mov_b32_e32 v75, v71
	v_mov_b32_e32 v69, v70
	v_pk_mul_f32 v[70:71], v[80:81], v[68:69]
	v_pk_mul_f32 v[80:81], v[80:81], v[74:75]
	v_pk_fma_f32 v[70:71], v[84:85], v[74:75], v[70:71]
	v_pk_fma_f32 v[80:81], v[84:85], v[68:69], v[80:81] neg_lo:[0,0,1] neg_hi:[0,0,1]
	v_mov_b64_e32 v[84:85], s[54:55]
	v_mad_i64_i32 v[84:85], s[14:15], v76, s0, v[84:85]
	v_cvt_pk_bf16_f32 v82, v82, v83
	v_cvt_pk_bf16_f32 v83, v80, v81
	v_cvt_pk_bf16_f32 v81, v70, v71
	v_mov_b64_e32 v[70:71], s[44:45]
	v_lshl_add_u64 v[84:85], v[84:85], 0, v[88:89]
	v_cvt_pk_bf16_f32 v80, v86, v87
	v_mad_i64_i32 v[70:71], s[14:15], v76, s33, v[70:71]
	global_store_dwordx2 v[84:85], v[82:83], off offset:128
	global_store_dwordx2 v[84:85], v[80:81], off offset:160
	v_lshl_add_u64 v[70:71], v[70:71], 0, v[88:89]
	s_waitcnt vmcnt(14)
	v_mov_b64_e32 v[80:81], v[214:215]
	v_mov_b64_e32 v[70:71], v[216:217]
	v_lshlrev_b32_e32 v82, 16, v80
	v_lshlrev_b32_e32 v84, 16, v70
	v_and_b32_e32 v85, 0xffff0000, v70
	v_and_b32_e32 v83, 0xffff0000, v80
	v_pk_mul_f32 v[86:87], v[72:73], v[84:85]
	v_lshlrev_b32_e32 v70, 16, v71
	v_pk_fma_f32 v[86:87], v[78:79], v[82:83], v[86:87]
	v_pk_mul_f32 v[78:79], v[78:79], v[84:85]
	v_and_b32_e32 v71, 0xffff0000, v71
	v_pk_fma_f32 v[72:73], v[72:73], v[82:83], v[78:79] neg_lo:[0,0,1] neg_hi:[0,0,1]
	v_lshlrev_b32_e32 v78, 16, v81
	v_and_b32_e32 v79, 0xffff0000, v81
	v_pk_mul_f32 v[80:81], v[68:69], v[70:71]
	v_pk_mul_f32 v[70:71], v[74:75], v[70:71]
	v_pk_fma_f32 v[80:81], v[74:75], v[78:79], v[80:81]
	v_pk_fma_f32 v[68:69], v[68:69], v[78:79], v[70:71] neg_lo:[0,0,1] neg_hi:[0,0,1]
	v_mov_b64_e32 v[70:71], s[56:57]
	v_mad_i64_i32 v[70:71], s[14:15], v76, s0, v[70:71]
	v_lshl_add_u64 v[70:71], v[70:71], 0, v[88:89]
	v_cvt_pk_bf16_f32 v72, v72, v73
	v_cvt_pk_bf16_f32 v73, v68, v69
	v_cvt_pk_bf16_f32 v68, v86, v87
	v_cvt_pk_bf16_f32 v69, v80, v81
	global_store_dwordx2 v[70:71], v[72:73], off offset:128
	global_store_dwordx2 v[70:71], v[68:69], off offset:160
	s_mov_b64 s[14:15], 0

; __device__ __forceinline__ unsigned cvt_pk_bf16(float lo, float hi) { f32x2 v = {lo, hi}; bf16x2_t b = __builtin_convertvector(v, bf16x2_t); return __builtin_bit_cast(unsigned, b); }
;     __device__ __forceinline__ void operator()(const f32x4 (&acc)[2][2][4][2], const u32x2 (&pf)[8], const g8::Unit& u, int wr, int wc, int fr, int fq) const {
;     ...
;                 if (u.pn == 1) {
;                     const float rq = __builtin_amdgcn_rsqf(sq.x * (1.f / 256.f) + 1e-6f) * SCALE_A;
;                     const float* cp = cs + ((size_t)(row % S) * 16 + 4 * fq) * 2;
;                     const f32x4 c0 = *(const f32x4*)cp, c1 = *(const f32x4*)(cp + 4);
;                     const float cc[4] = {c0[0], c0[2], c1[0], c1[2]}, sn[4] = {c0[1], c0[3], c1[1], c1[3]};
;                     {   const f32x4 t1 = acc[ai][0][m][0] * rq, t2 = acc[ai][0][m][1] * rq;
;                         float o1[4], o2[4];
; #pragma unroll
;                         for (int j = 0; j < 4; ++j) { o1[j] = t1[j] * cc[j] - t2[j] * sn[j]; o2[j] = t1[j] * sn[j] + t2[j] * cc[j]; }
;                         bf16_t* qp = QA + (size_t)row * 384 + wc * 96 + 64 + 4 * fq;
;                         *(u32x2*)qp = (u32x2){cvt_pk_bf16(o1[0], o1[1]), cvt_pk_bf16(o1[2], o1[3])};
;                         *(u32x2*)(qp + 16) = (u32x2){cvt_pk_bf16(o2[0], o2[1]), cvt_pk_bf16(o2[2], o2[3])}; }
;                     {   const bf16_t* hp = H + (size_t)row * HP + C_KR + 4 * fq;
;                         const u32x2 a = *(const u32x2*)hp, b = *(const u32x2*)(hp + 16);
;                         const float t1[4] = {__uint_as_float(a.x << 16), __uint_as_float(a.x & 0xffff0000u), __uint_as_float(a.y << 16), __uint_as_float(a.y & 0xffff0000u)};
;                         const float t2[4] = {__uint_as_float(b.x << 16), __uint_as_float(b.x & 0xffff0000u), __uint_as_float(b.y << 16), __uint_as_float(b.y & 0xffff0000u)};
;                         float o1[4], o2[4];
; #pragma unroll
;                         for (int j = 0; j < 4; ++j) { o1[j] = t1[j] * cc[j] - t2[j] * sn[j]; o2[j] = t1[j] * sn[j] + t2[j] * cc[j]; }
;                         bf16_t* kp = KA + (size_t)row * 384 + wc * 96 + 64 + 4 * fq;
;                         *(u32x2*)kp = (u32x2){cvt_pk_bf16(o1[0], o1[1]), cvt_pk_bf16(o1[2], o1[3])};
;                         *(u32x2*)(kp + 16) = (u32x2){cvt_pk_bf16(o2[0], o2[1]), cvt_pk_bf16(o2[2], o2[3])}; }
.LBB0_676:
	s_cmp_eq_u32 s67, 1
	s_mov_b64 s[14:15], -1
	s_cbranch_scc0 .LBB0_678
	v_fmamk_f32 v52, v166, 0x3b800000, v246
	v_rsq_f32_e32 v52, v52
	v_lshlrev_b32_e32 v72, 1, v5
	v_mov_b32_e32 v73, v31
	v_mul_f32_e32 v64, 0x3e16c740, v52
	v_ashrrev_i32_e32 v52, 31, v60
	v_lshrrev_b32_e32 v52, 19, v52
	v_add_u32_e32 v52, v60, v52
	v_and_b32_e32 v52, 0xffffe000, v52
	v_sub_u32_e32 v52, v60, v52
	v_ashrrev_i32_e32 v53, 31, v52
	v_lshlrev_b64 v[52:53], 7, v[52:53]
	v_lshl_add_u64 v[52:53], s[46:47], 0, v[52:53]
	v_lshl_add_u64 v[56:57], v[52:53], 0, v[30:31]
	s_waitcnt vmcnt(14)
	v_mov_b64_e32 v[52:53], v[218:219]
	v_mov_b64_e32 v[54:55], v[220:221]
	v_mov_b64_e32 v[56:57], v[222:223]
	v_mov_b64_e32 v[58:59], v[224:225]
	v_pk_mul_f32 v[68:69], v[64:65], v[44:45] op_sel_hi:[0,1]
	v_pk_mul_f32 v[66:67], v[64:65], v[48:49] op_sel_hi:[0,1]
	v_mov_b32_e32 v62, v57
	v_mov_b32_e32 v57, v58
	v_mov_b32_e32 v63, v59
	v_pk_mul_f32 v[58:59], v[68:69], v[56:57]
	s_nop 0
	v_pk_fma_f32 v[70:71], v[66:67], v[62:63], v[58:59]
	v_pk_mul_f32 v[58:59], v[68:69], v[62:63]
	v_pk_mul_f32 v[68:69], v[64:65], v[50:51] op_sel_hi:[0,1]
	v_pk_fma_f32 v[66:67], v[66:67], v[56:57], v[58:59] neg_lo:[0,0,1] neg_hi:[0,0,1]
	v_pk_mul_f32 v[64:65], v[64:65], v[46:47] op_sel_hi:[0,1]
	v_mov_b32_e32 v58, v53
	v_mov_b32_e32 v59, v55
	v_mov_b32_e32 v53, v54
	v_pk_mul_f32 v[54:55], v[64:65], v[52:53]
	v_pk_mul_f32 v[64:65], v[64:65], v[58:59]
	v_pk_fma_f32 v[54:55], v[68:69], v[58:59], v[54:55]
	v_pk_fma_f32 v[64:65], v[68:69], v[52:53], v[64:65] neg_lo:[0,0,1] neg_hi:[0,0,1]
	v_mov_b64_e32 v[68:69], s[54:55]
	v_mad_i64_i32 v[68:69], s[14:15], v60, s0, v[68:69]
	v_cvt_pk_bf16_f32 v66, v66, v67
	v_cvt_pk_bf16_f32 v67, v64, v65
	v_cvt_pk_bf16_f32 v65, v54, v55
	v_mov_b64_e32 v[54:55], s[44:45]
	v_lshl_add_u64 v[68:69], v[68:69], 0, v[72:73]
	v_cvt_pk_bf16_f32 v64, v70, v71
	v_mad_i64_i32 v[54:55], s[14:15], v60, s33, v[54:55]
	global_store_dwordx2 v[68:69], v[66:67], off offset:128
	global_store_dwordx2 v[68:69], v[64:65], off offset:160
	v_lshl_add_u64 v[54:55], v[54:55], 0, v[72:73]
	s_waitcnt vmcnt(14)
	v_mov_b64_e32 v[64:65], v[226:227]
	v_mov_b64_e32 v[54:55], v[228:229]
	v_lshlrev_b32_e32 v66, 16, v64
	v_lshlrev_b32_e32 v68, 16, v54
	v_and_b32_e32 v69, 0xffff0000, v54
	v_and_b32_e32 v67, 0xffff0000, v64
	v_pk_mul_f32 v[70:71], v[56:57], v[68:69]
	v_lshlrev_b32_e32 v54, 16, v55
	v_pk_fma_f32 v[70:71], v[62:63], v[66:67], v[70:71]
	v_pk_mul_f32 v[62:63], v[62:63], v[68:69]
	v_and_b32_e32 v55, 0xffff0000, v55
	v_pk_fma_f32 v[56:57], v[56:57], v[66:67], v[62:63] neg_lo:[0,0,1] neg_hi:[0,0,1]
	v_lshlrev_b32_e32 v62, 16, v65
	v_and_b32_e32 v63, 0xffff0000, v65
	v_pk_mul_f32 v[64:65], v[52:53], v[54:55]
	v_pk_mul_f32 v[54:55], v[58:59], v[54:55]
	v_pk_fma_f32 v[64:65], v[58:59], v[62:63], v[64:65]
	v_pk_fma_f32 v[52:53], v[52:53], v[62:63], v[54:55] neg_lo:[0,0,1] neg_hi:[0,0,1]
	v_mov_b64_e32 v[54:55], s[56:57]
	v_mad_i64_i32 v[54:55], s[14:15], v60, s0, v[54:55]
	v_lshl_add_u64 v[54:55], v[54:55], 0, v[72:73]
	v_cvt_pk_bf16_f32 v56, v56, v57
	v_cvt_pk_bf16_f32 v57, v52, v53
	v_cvt_pk_bf16_f32 v52, v70, v71
	v_cvt_pk_bf16_f32 v53, v64, v65
	global_store_dwordx2 v[54:55], v[56:57], off offset:128
	global_store_dwordx2 v[54:55], v[52:53], off offset:160
	s_mov_b64 s[14:15], 0

; __device__ __forceinline__ unsigned cvt_pk_bf16(float lo, float hi) { f32x2 v = {lo, hi}; bf16x2_t b = __builtin_convertvector(v, bf16x2_t); return __builtin_bit_cast(unsigned, b); }
;     __device__ __forceinline__ void operator()(const f32x4 (&acc)[2][2][4][2], const u32x2 (&pf)[8], const g8::Unit& u, int wr, int wc, int fr, int fq) const {
;     ...
;                 if (u.pn == 1) {
;                     const float rq = __builtin_amdgcn_rsqf(sq.x * (1.f / 256.f) + 1e-6f) * SCALE_A;
;                     const float* cp = cs + ((size_t)(row % S) * 16 + 4 * fq) * 2;
;                     const f32x4 c0 = *(const f32x4*)cp, c1 = *(const f32x4*)(cp + 4);
;                     const float cc[4] = {c0[0], c0[2], c1[0], c1[2]}, sn[4] = {c0[1], c0[3], c1[1], c1[3]};
;                     {   const f32x4 t1 = acc[ai][0][m][0] * rq, t2 = acc[ai][0][m][1] * rq;
;                         float o1[4], o2[4];
; #pragma unroll
;                         for (int j = 0; j < 4; ++j) { o1[j] = t1[j] * cc[j] - t2[j] * sn[j]; o2[j] = t1[j] * sn[j] + t2[j] * cc[j]; }
;                         bf16_t* qp = QA + (size_t)row * 384 + wc * 96 + 64 + 4 * fq;
;                         *(u32x2*)qp = (u32x2){cvt_pk_bf16(o1[0], o1[1]), cvt_pk_bf16(o1[2], o1[3])};
;                         *(u32x2*)(qp + 16) = (u32x2){cvt_pk_bf16(o2[0], o2[1]), cvt_pk_bf16(o2[2], o2[3])}; }
;                     {   const bf16_t* hp = H + (size_t)row * HP + C_KR + 4 * fq;
;                         const u32x2 a = *(const u32x2*)hp, b = *(const u32x2*)(hp + 16);
;                         const float t1[4] = {__uint_as_float(a.x << 16), __uint_as_float(a.x & 0xffff0000u), __uint_as_float(a.y << 16), __uint_as_float(a.y & 0xffff0000u)};
;                         const float t2[4] = {__uint_as_float(b.x << 16), __uint_as_float(b.x & 0xffff0000u), __uint_as_float(b.y << 16), __uint_as_float(b.y & 0xffff0000u)};
;                         float o1[4], o2[4];
; #pragma unroll
;                         for (int j = 0; j < 4; ++j) { o1[j] = t1[j] * cc[j] - t2[j] * sn[j]; o2[j] = t1[j] * sn[j] + t2[j] * cc[j]; }
;                         bf16_t* kp = KA + (size_t)row * 384 + wc * 96 + 64 + 4 * fq;
;                         *(u32x2*)kp = (u32x2){cvt_pk_bf16(o1[0], o1[1]), cvt_pk_bf16(o1[2], o1[3])};
;                         *(u32x2*)(kp + 16) = (u32x2){cvt_pk_bf16(o2[0], o2[1]), cvt_pk_bf16(o2[2], o2[3])}; }
.LBB0_703:
	s_cmp_eq_u32 s67, 1
	s_mov_b64 s[14:15], -1
	s_cbranch_scc0 .LBB0_705
	v_fmamk_f32 v36, v162, 0x3b800000, v246
	v_rsq_f32_e32 v36, v36
	v_lshlrev_b32_e32 v56, 1, v5
	v_mov_b32_e32 v57, v31
	v_mul_f32_e32 v48, 0x3e16c740, v36
	v_ashrrev_i32_e32 v36, 31, v44
	v_lshrrev_b32_e32 v36, 19, v36
	v_add_u32_e32 v36, v44, v36
	v_and_b32_e32 v36, 0xffffe000, v36
	v_sub_u32_e32 v36, v44, v36
	v_ashrrev_i32_e32 v37, 31, v36
	v_lshlrev_b64 v[36:37], 7, v[36:37]
	v_lshl_add_u64 v[36:37], s[46:47], 0, v[36:37]
	v_lshl_add_u64 v[40:41], v[36:37], 0, v[30:31]
	s_waitcnt vmcnt(14)
	v_mov_b64_e32 v[36:37], v[230:231]
	v_mov_b64_e32 v[38:39], v[232:233]
	v_mov_b64_e32 v[40:41], v[234:235]
	v_mov_b64_e32 v[42:43], v[236:237]
	v_pk_mul_f32 v[52:53], v[48:49], v[26:27] op_sel_hi:[0,1]
	v_pk_mul_f32 v[50:51], v[48:49], v[32:33] op_sel_hi:[0,1]
	v_mov_b32_e32 v46, v41
	v_mov_b32_e32 v41, v42
	v_mov_b32_e32 v47, v43
	v_pk_mul_f32 v[42:43], v[52:53], v[40:41]
	s_nop 0
	v_pk_fma_f32 v[54:55], v[50:51], v[46:47], v[42:43]
	v_pk_mul_f32 v[42:43], v[52:53], v[46:47]
	v_pk_mul_f32 v[52:53], v[48:49], v[34:35] op_sel_hi:[0,1]
	v_pk_fma_f32 v[50:51], v[50:51], v[40:41], v[42:43] neg_lo:[0,0,1] neg_hi:[0,0,1]
	v_pk_mul_f32 v[48:49], v[48:49], v[28:29] op_sel_hi:[0,1]
	v_mov_b32_e32 v42, v37
	v_mov_b32_e32 v43, v39
	v_mov_b32_e32 v37, v38
	v_pk_mul_f32 v[38:39], v[48:49], v[36:37]
	v_pk_mul_f32 v[48:49], v[48:49], v[42:43]
	v_pk_fma_f32 v[38:39], v[52:53], v[42:43], v[38:39]
	v_pk_fma_f32 v[48:49], v[52:53], v[36:37], v[48:49] neg_lo:[0,0,1] neg_hi:[0,0,1]
	v_mov_b64_e32 v[52:53], s[54:55]
	v_mad_i64_i32 v[52:53], s[14:15], v44, s0, v[52:53]
	v_cvt_pk_bf16_f32 v50, v50, v51
	v_cvt_pk_bf16_f32 v51, v48, v49
	v_cvt_pk_bf16_f32 v49, v38, v39
	v_mov_b64_e32 v[38:39], s[44:45]
	v_lshl_add_u64 v[52:53], v[52:53], 0, v[56:57]
	v_cvt_pk_bf16_f32 v48, v54, v55
	v_mad_i64_i32 v[38:39], s[14:15], v44, s33, v[38:39]
	global_store_dwordx2 v[52:53], v[50:51], off offset:128
	global_store_dwordx2 v[52:53], v[48:49], off offset:160
	v_lshl_add_u64 v[38:39], v[38:39], 0, v[56:57]
	s_waitcnt vmcnt(14)
	v_mov_b64_e32 v[48:49], v[238:239]
	v_mov_b64_e32 v[38:39], v[240:241]
	v_lshlrev_b32_e32 v50, 16, v48
	v_lshlrev_b32_e32 v52, 16, v38
	v_and_b32_e32 v53, 0xffff0000, v38
	v_and_b32_e32 v51, 0xffff0000, v48
	v_pk_mul_f32 v[54:55], v[40:41], v[52:53]
	v_lshlrev_b32_e32 v38, 16, v39
	v_pk_fma_f32 v[54:55], v[46:47], v[50:51], v[54:55]
	v_pk_mul_f32 v[46:47], v[46:47], v[52:53]
	v_and_b32_e32 v39, 0xffff0000, v39
	v_pk_fma_f32 v[40:41], v[40:41], v[50:51], v[46:47] neg_lo:[0,0,1] neg_hi:[0,0,1]
	v_lshlrev_b32_e32 v46, 16, v49
	v_and_b32_e32 v47, 0xffff0000, v49
	v_pk_mul_f32 v[48:49], v[36:37], v[38:39]
	v_pk_mul_f32 v[38:39], v[42:43], v[38:39]
	v_pk_fma_f32 v[48:49], v[42:43], v[46:47], v[48:49]
	v_pk_fma_f32 v[36:37], v[36:37], v[46:47], v[38:39] neg_lo:[0,0,1] neg_hi:[0,0,1]
	v_mov_b64_e32 v[38:39], s[56:57]
	v_mad_i64_i32 v[38:39], s[14:15], v44, s0, v[38:39]
	v_lshl_add_u64 v[38:39], v[38:39], 0, v[56:57]
	v_cvt_pk_bf16_f32 v40, v40, v41
	v_cvt_pk_bf16_f32 v41, v36, v37
	v_cvt_pk_bf16_f32 v36, v54, v55
	v_cvt_pk_bf16_f32 v37, v48, v49
	global_store_dwordx2 v[38:39], v[40:41], off offset:128
	global_store_dwordx2 v[38:39], v[36:37], off offset:160
	s_mov_b64 s[14:15], 0

; __device__ __forceinline__ unsigned cvt_pk_bf16(float lo, float hi) { f32x2 v = {lo, hi}; bf16x2_t b = __builtin_convertvector(v, bf16x2_t); return __builtin_bit_cast(unsigned, b); }
;     __device__ __forceinline__ void operator()(const f32x4 (&acc)[2][2][4][2], const u32x2 (&pf)[8], const g8::Unit& u, int wr, int wc, int fr, int fq) const {
;     ...
;                 if (u.pn == 1) {
;                     const float rq = __builtin_amdgcn_rsqf(sq.x * (1.f / 256.f) + 1e-6f) * SCALE_A;
;                     const float* cp = cs + ((size_t)(row % S) * 16 + 4 * fq) * 2;
;                     const f32x4 c0 = *(const f32x4*)cp, c1 = *(const f32x4*)(cp + 4);
;                     const float cc[4] = {c0[0], c0[2], c1[0], c1[2]}, sn[4] = {c0[1], c0[3], c1[1], c1[3]};
;                     {   const f32x4 t1 = acc[ai][0][m][0] * rq, t2 = acc[ai][0][m][1] * rq;
;                         float o1[4], o2[4];
; #pragma unroll
;                         for (int j = 0; j < 4; ++j) { o1[j] = t1[j] * cc[j] - t2[j] * sn[j]; o2[j] = t1[j] * sn[j] + t2[j] * cc[j]; }
;                         bf16_t* qp = QA + (size_t)row * 384 + wc * 96 + 64 + 4 * fq;
;                         *(u32x2*)qp = (u32x2){cvt_pk_bf16(o1[0], o1[1]), cvt_pk_bf16(o1[2], o1[3])};
;                         *(u32x2*)(qp + 16) = (u32x2){cvt_pk_bf16(o2[0], o2[1]), cvt_pk_bf16(o2[2], o2[3])}; }
;                     {   const bf16_t* hp = H + (size_t)row * HP + C_KR + 4 * fq;
;                         const u32x2 a = *(const u32x2*)hp, b = *(const u32x2*)(hp + 16);
;                         const float t1[4] = {__uint_as_float(a.x << 16), __uint_as_float(a.x & 0xffff0000u), __uint_as_float(a.y << 16), __uint_as_float(a.y & 0xffff0000u)};
;                         const float t2[4] = {__uint_as_float(b.x << 16), __uint_as_float(b.x & 0xffff0000u), __uint_as_float(b.y << 16), __uint_as_float(b.y & 0xffff0000u)};
;                         float o1[4], o2[4];
; #pragma unroll
;                         for (int j = 0; j < 4; ++j) { o1[j] = t1[j] * cc[j] - t2[j] * sn[j]; o2[j] = t1[j] * sn[j] + t2[j] * cc[j]; }
;                         bf16_t* kp = KA + (size_t)row * 384 + wc * 96 + 64 + 4 * fq;
;                         *(u32x2*)kp = (u32x2){cvt_pk_bf16(o1[0], o1[1]), cvt_pk_bf16(o1[2], o1[3])};
;                         *(u32x2*)(kp + 16) = (u32x2){cvt_pk_bf16(o2[0], o2[1]), cvt_pk_bf16(o2[2], o2[3])}; }
.LBB0_730:
	s_cmp_eq_u32 s67, 1
	s_mov_b64 s[14:15], -1
	s_cbranch_scc0 .LBB0_732
	v_fmamk_f32 v18, v160, 0x3b800000, v246
	v_rsq_f32_e32 v18, v18
	v_lshlrev_b32_e32 v40, 1, v5
	v_mov_b32_e32 v41, v31
	v_mul_f32_e32 v32, 0x3e16c740, v18
	v_ashrrev_i32_e32 v18, 31, v26
	v_lshrrev_b32_e32 v18, 19, v18
	v_add_u32_e32 v18, v26, v18
	v_and_b32_e32 v18, 0xffffe000, v18
	v_sub_u32_e32 v18, v26, v18
	v_ashrrev_i32_e32 v19, 31, v18
	v_lshlrev_b64 v[18:19], 7, v[18:19]
	v_lshl_add_u64 v[18:19], s[46:47], 0, v[18:19]
	v_lshl_add_u64 v[22:23], v[18:19], 0, v[30:31]
	s_waitcnt vmcnt(14)
	v_mov_b64_e32 v[18:19], v[242:243]
	v_mov_b64_e32 v[20:21], v[244:245]
	v_mov_b64_e32 v[22:23], v[188:189]
	v_mov_b64_e32 v[24:25], v[190:191]
	v_pk_mul_f32 v[36:37], v[32:33], v[10:11] op_sel_hi:[0,1]
	v_pk_mul_f32 v[34:35], v[32:33], v[14:15] op_sel_hi:[0,1]
	v_mov_b32_e32 v28, v23
	v_mov_b32_e32 v23, v24
	v_mov_b32_e32 v29, v25
	v_pk_mul_f32 v[24:25], v[36:37], v[22:23]
	s_nop 0
	v_pk_fma_f32 v[38:39], v[34:35], v[28:29], v[24:25]
	v_pk_mul_f32 v[24:25], v[36:37], v[28:29]
	v_pk_mul_f32 v[36:37], v[32:33], v[16:17] op_sel_hi:[0,1]
	v_pk_fma_f32 v[34:35], v[34:35], v[22:23], v[24:25] neg_lo:[0,0,1] neg_hi:[0,0,1]
	v_pk_mul_f32 v[32:33], v[32:33], v[12:13] op_sel_hi:[0,1]
	v_mov_b32_e32 v24, v19
	v_mov_b32_e32 v25, v21
	v_mov_b32_e32 v19, v20
	v_pk_mul_f32 v[20:21], v[32:33], v[18:19]
	v_pk_mul_f32 v[32:33], v[32:33], v[24:25]
	v_pk_fma_f32 v[20:21], v[36:37], v[24:25], v[20:21]
	v_pk_fma_f32 v[32:33], v[36:37], v[18:19], v[32:33] neg_lo:[0,0,1] neg_hi:[0,0,1]
	v_mov_b64_e32 v[36:37], s[54:55]
	v_mad_i64_i32 v[36:37], s[14:15], v26, s0, v[36:37]
	v_cvt_pk_bf16_f32 v34, v34, v35
	v_cvt_pk_bf16_f32 v35, v32, v33
	v_cvt_pk_bf16_f32 v33, v20, v21
	v_mov_b64_e32 v[20:21], s[44:45]
	v_lshl_add_u64 v[36:37], v[36:37], 0, v[40:41]
	v_cvt_pk_bf16_f32 v32, v38, v39
	v_mad_i64_i32 v[20:21], s[14:15], v26, s33, v[20:21]
	global_store_dwordx2 v[36:37], v[34:35], off offset:128
	global_store_dwordx2 v[36:37], v[32:33], off offset:160
	v_lshl_add_u64 v[20:21], v[20:21], 0, v[40:41]
	s_waitcnt vmcnt(14)
	v_mov_b64_e32 v[32:33], v[192:193]
	v_mov_b64_e32 v[20:21], v[194:195]
	v_lshlrev_b32_e32 v34, 16, v32
	v_lshlrev_b32_e32 v36, 16, v20
	v_and_b32_e32 v37, 0xffff0000, v20
	v_and_b32_e32 v35, 0xffff0000, v32
	v_pk_mul_f32 v[38:39], v[22:23], v[36:37]
	v_lshlrev_b32_e32 v20, 16, v21
	v_pk_fma_f32 v[38:39], v[28:29], v[34:35], v[38:39]
	v_pk_mul_f32 v[28:29], v[28:29], v[36:37]
	v_and_b32_e32 v21, 0xffff0000, v21
	v_pk_fma_f32 v[22:23], v[22:23], v[34:35], v[28:29] neg_lo:[0,0,1] neg_hi:[0,0,1]
	v_lshlrev_b32_e32 v28, 16, v33
	v_and_b32_e32 v29, 0xffff0000, v33
	v_pk_mul_f32 v[32:33], v[18:19], v[20:21]
	v_pk_mul_f32 v[20:21], v[24:25], v[20:21]
	v_pk_fma_f32 v[32:33], v[24:25], v[28:29], v[32:33]
	v_pk_fma_f32 v[18:19], v[18:19], v[28:29], v[20:21] neg_lo:[0,0,1] neg_hi:[0,0,1]
	v_mov_b64_e32 v[20:21], s[56:57]
	v_mad_i64_i32 v[20:21], s[14:15], v26, s0, v[20:21]
	v_lshl_add_u64 v[20:21], v[20:21], 0, v[40:41]
	v_cvt_pk_bf16_f32 v22, v22, v23
	v_cvt_pk_bf16_f32 v23, v18, v19
	v_cvt_pk_bf16_f32 v18, v38, v39
	v_cvt_pk_bf16_f32 v19, v32, v33
	global_store_dwordx2 v[20:21], v[22:23], off offset:128
	global_store_dwordx2 v[20:21], v[18:19], off offset:160
	s_mov_b64 s[14:15], 0

; #define LAS __attribute__((address_space(3)))
; __device__ __forceinline__ void lds_barrier() { asm volatile("s_waitcnt lgkmcnt(0)\n\ts_barrier" ::: "memory"); }
; __device__ __forceinline__ int claim_take(LAS unsigned char* lds, int tid, const int* pend) {
;     if (tid == 0) *(volatile LAS int*)(lds + QSLOT) = *pend;
;     lds_barrier();
;     const int v = __builtin_amdgcn_readfirstlane(*(volatile LAS int*)(lds + QSLOT));
;     lds_barrier();
;     return v;
.LBB0_857:
	s_or_b64 exec, exec, s[14:15]
	s_waitcnt vmcnt(0)
	v_readfirstlane_b32 s1, v1
	s_nop 1
	v_add_u32_e32 v164, s1, v0
	v_mov_b32_e32 v192, v164

; #define LAS __attribute__((address_space(3)))
; __device__ __forceinline__ void lds_barrier() { asm volatile("s_waitcnt lgkmcnt(0)\n\ts_barrier" ::: "memory"); }
; __device__ __forceinline__ int claim_take(LAS unsigned char* lds, int tid, const int* pend) {
;     if (tid == 0) *(volatile LAS int*)(lds + QSLOT) = *pend;
;     lds_barrier();
;     const int v = __builtin_amdgcn_readfirstlane(*(volatile LAS int*)(lds + QSLOT));
;     lds_barrier();
;     return v;
.LBB0_859:
	s_waitcnt vmcnt(4)
	ds_write_b32 v247, v192

;     ...
;     if (nctr != nullptr && tid == 0) *pend = (int)__hip_atomic_fetch_add(nctr, 1u, __ATOMIC_RELAXED, __HIP_MEMORY_SCOPE_AGENT);
.LBB0_888:
	v_cmp_eq_u32_e32 vcc, 0, v29
	s_and_saveexec_b64 s[14:15], vcc
	s_cbranch_execz .LBB0_892
	s_mov_b64 s[34:35], exec
	v_mbcnt_lo_u32_b32 v16, s34, 0
	v_mbcnt_hi_u32_b32 v16, s35, v16
	v_cmp_eq_u32_e32 vcc, 0, v16
	s_and_saveexec_b64 s[16:17], vcc
	s_cbranch_execz .LBB0_891
	s_bcnt1_i32_b64 s34, s[34:35]
	v_mov_b32_e32 v17, s34
	global_atomic_add v192, v31, v17, s[52:53] sc0

; __device__ __forceinline__ unsigned cvt_pk_bf16(float lo, float hi) { f32x2 v = {lo, hi}; bf16x2_t b = __builtin_convertvector(v, bf16x2_t); return __builtin_bit_cast(unsigned, b); }
; __device__ __forceinline__ float swapsum(float a) { auto rr = __builtin_amdgcn_permlane32_swap(__float_as_uint(a), __float_as_uint(a), false, false); return __uint_as_float(rr[0]) + __uint_as_float(rr[1]); }
;     ...
;     l = swapsum(l);
;     if (SWA) { const float sk = sink_l2 + (ALIBI ? slope_l2 * (float)(pos[qidx] - pos_ref) : 0.f);
;         const float mnew = fmaxf(m, sk), f = __builtin_amdgcn_exp2f(m - mnew); l = l * f + __builtin_amdgcn_exp2f(sk - mnew);
; #pragma unroll
;         for (int i = 0; i < 16; ++i) { ot[0][i] *= f; ot[1][i] *= f; } }
;     const float inv = 1.f / l;
;     ...
;     else { bf16_t* op = (bf16_t*)outp + (size_t)qidx * opitch + 4 * hf + hsel * 64;
; #pragma unroll
;         for (int db = 0; db < 2; ++db)
; #pragma unroll
;             for (int g = 0; g < 4; ++g) *(u32x2*)(op + 32 * db + 8 * g) = (u32x2){cvt_pk_bf16(ot[db][4 * g] * inv, ot[db][4 * g + 1] * inv), cvt_pk_bf16(ot[db][4 * g + 2] * inv, ot[db][4 * g + 3] * inv)}; }
.LBB0_892:
	s_or_b64 exec, exec, s[14:15]
	s_mulk_i32 s29, 0xa00
	v_mov_b32_e32 v16, v113
	s_add_u32 s14, s13, s29
	s_nop 0
	v_permlane32_swap_b32_e32 v113, v16
	s_addc_u32 s15, s31, 0
	s_lshl_b32 s16, s42, 1
	v_add_f32_e32 v16, v113, v16
	s_add_u32 s14, s14, s16
	v_div_scale_f32 v17, s[16:17], v16, v16, 1.0
	v_rcp_f32_e32 v18, v17
	s_addc_u32 s15, s15, 0
	v_fma_f32 v19, -v17, v18, 1.0
	v_fmac_f32_e32 v18, v19, v18
	v_div_scale_f32 v19, vcc, 1.0, v16, 1.0
	v_mul_f32_e32 v20, v19, v18
	v_fma_f32 v21, -v17, v20, v19
	v_fmac_f32_e32 v20, v21, v18
	v_fma_f32 v17, -v17, v20, v19
	v_div_fmas_f32 v17, v17, v18, v20
	v_mov_b64_e32 v[18:19], s[14:15]
	s_movk_i32 s14, 0xa00
	v_div_fixup_f32 v16, v17, v16, 1.0
	v_mad_i64_i32 v[18:19], s[14:15], v28, s14, v[18:19]
	v_lshlrev_b32_e32 v20, 1, v30
	v_mov_b32_e32 v21, v31
	v_lshl_add_u64 v[18:19], v[18:19], 0, v[20:21]
	v_pk_mul_f32 v[20:21], v[32:33], v[16:17] op_sel_hi:[1,0]
	v_pk_mul_f32 v[22:23], v[34:35], v[16:17] op_sel_hi:[1,0]
	v_pk_mul_f32 v[0:1], v[0:1], v[16:17] op_sel_hi:[1,0]
	v_pk_mul_f32 v[2:3], v[2:3], v[16:17] op_sel_hi:[1,0]
	v_cvt_pk_bf16_f32 v32, v20, v21
	v_cvt_pk_bf16_f32 v33, v22, v23
	v_cvt_pk_bf16_f32 v34, v0, v1
	v_cvt_pk_bf16_f32 v35, v2, v3
	v_pk_mul_f32 v[20:21], v[36:37], v[16:17] op_sel_hi:[1,0]
	v_pk_mul_f32 v[22:23], v[38:39], v[16:17] op_sel_hi:[1,0]
	v_pk_mul_f32 v[0:1], v[4:5], v[16:17] op_sel_hi:[1,0]
	v_pk_mul_f32 v[2:3], v[6:7], v[16:17] op_sel_hi:[1,0]
	v_cvt_pk_bf16_f32 v36, v20, v21
	v_cvt_pk_bf16_f32 v37, v22, v23
	v_cvt_pk_bf16_f32 v38, v0, v1
	v_cvt_pk_bf16_f32 v39, v2, v3
	v_pk_mul_f32 v[20:21], v[40:41], v[16:17] op_sel_hi:[1,0]
	v_pk_mul_f32 v[22:23], v[42:43], v[16:17] op_sel_hi:[1,0]
	v_pk_mul_f32 v[0:1], v[8:9], v[16:17] op_sel_hi:[1,0]
	v_pk_mul_f32 v[2:3], v[10:11], v[16:17] op_sel_hi:[1,0]
	v_cvt_pk_bf16_f32 v40, v20, v21
	v_cvt_pk_bf16_f32 v41, v22, v23
	v_cvt_pk_bf16_f32 v42, v0, v1
	v_cvt_pk_bf16_f32 v43, v2, v3
	v_pk_mul_f32 v[20:21], v[44:45], v[16:17] op_sel_hi:[1,0]
	v_pk_mul_f32 v[22:23], v[46:47], v[16:17] op_sel_hi:[1,0]
	v_pk_mul_f32 v[0:1], v[12:13], v[16:17] op_sel_hi:[1,0]
	v_pk_mul_f32 v[2:3], v[14:15], v[16:17] op_sel_hi:[1,0]
	v_cvt_pk_bf16_f32 v44, v20, v21
	v_cvt_pk_bf16_f32 v45, v22, v23
	v_cvt_pk_bf16_f32 v46, v0, v1
	v_cvt_pk_bf16_f32 v47, v2, v3
	s_nop 1
	v_permlane32_swap_b32_e32 v32, v34
	v_permlane32_swap_b32_e32 v33, v35
	v_permlane32_swap_b32_e32 v36, v38
	v_permlane32_swap_b32_e32 v37, v39
	v_permlane32_swap_b32_e32 v40, v42
	v_permlane32_swap_b32_e32 v41, v43
	v_permlane32_swap_b32_e32 v44, v46
	v_permlane32_swap_b32_e32 v45, v47
	v_mbcnt_lo_u32_b32 v22, -1, 0
	v_mbcnt_hi_u32_b32 v22, -1, v22
	v_lshrrev_b32_e32 v22, 5, v22
	v_mul_u32_u24_e32 v22, 56, v22
	v_add_co_u32_e32 v18, vcc, v18, v22
	s_nop 1
	v_addc_co_u32_e32 v19, vcc, 0, v19, vcc
	global_store_dwordx4 v[18:19], v[32:35], off
	global_store_dwordx4 v[18:19], v[36:39], off offset:16
	global_store_dwordx4 v[18:19], v[40:43], off offset:32
	global_store_dwordx4 v[18:19], v[44:47], off offset:48
	s_andn2_b64 vcc, exec, s[10:11]
	s_cbranch_vccz .LBB0_894

; #define LAS __attribute__((address_space(3)))
; __device__ __forceinline__ void lds_barrier() { asm volatile("s_waitcnt lgkmcnt(0)\n\ts_barrier" ::: "memory"); }
; __device__ __forceinline__ int claim_take(LAS unsigned char* lds, int tid, const int* pend) {
;     if (tid == 0) *(volatile LAS int*)(lds + QSLOT) = *pend;
;     lds_barrier();
;     const int v = __builtin_amdgcn_readfirstlane(*(volatile LAS int*)(lds + QSLOT));
;     lds_barrier();
;     return v;
.LBB0_916:
	s_or_b64 exec, exec, s[16:17]
	s_waitcnt vmcnt(0)
	v_readfirstlane_b32 s1, v1
	s_nop 1
	v_add_u32_e32 v164, s1, v0
	v_mov_b32_e32 v192, v164

; __device__ __forceinline__ int lane_id() { unsigned m = ~0u; asm volatile("" : "+s"(m)); return (int)__builtin_amdgcn_mbcnt_hi(m, __builtin_amdgcn_mbcnt_lo(m, 0u)); }
; __device__ __forceinline__ float swapsum(float a) { auto rr = __builtin_amdgcn_permlane32_swap(__float_as_uint(a), __float_as_uint(a), false, false); return __uint_as_float(rr[0]) + __uint_as_float(rr[1]); }
;     ...
;     const int qmin = q0 + 32 * wq, qidx = qmin + r32, qmax = qmin + 31;
;     int t_lo = 0; if (SWA) { t_lo = q0 - 127; t_lo = (t_lo < 0 ? 0 : t_lo) >> 7; }
;     const int t_hi = (q0 + ((MODE == 3) ? 127 : (MODE == 4) ? 63 : 255)) >> 7;
;     if (MODE == 3 && mp) kmax = kmax1;
;     const int pos_ref = ALIBI ? pos[q0] : 0;
;     bf16x8 qf[NC];
;     { const bf16_t* qr = T.q + (size_t)qidx * T.qp + 8 * hf + (mp + hsel) * DQK;
; #pragma unroll
;       for (int c = 0; c < NC; ++c) qf[c] = *(const bf16x8*)(qr + 16 * c); }
;     f32x16 ot[2];
; #pragma unroll
;     for (int i = 0; i < 16; ++i) { ot[0][i] = 0.f; ot[1][i] = 0.f; }
;     float m = SWA ? -1e30f : 0.f, l = 0.f; bool first = true;
;     u32x4 kreg[NKI], vreg[2]; float breg = 0.f;
;     const int vr = tid >> 3, vc = tid & 7;
;     ...
;     constexpr bool DESC = (MODE == 2 || MODE == 3);
;     float qn = 0.f; bool fin = false; int par = 0;
;     if (DESC) {
; #pragma unroll
;         for (int c = 0; c < NC; ++c)
; #pragma unroll
;             for (int j = 0; j < 8; ++j) { const float v = __uint_as_float(((unsigned)(unsigned short)qf[c][j]) << 16); qn += v * v; }
;         qn = sqrtf(swapsum(qn)) * 1.01f;
;     ...
;         const int idx = at::claim_take(lds, F.tid, &pend); if (idx >= 512) break;
;         const int h = 3 - (idx >> 7), rem = idx & 127, qb = 63 - (rem >> 1), b = rem & 1;
;         const bf16_t* Hb = H + (size_t)b * S * HP;
;         at::Tens T{Hb + C_DFQ + h * 64, Hb + C_DFK + h * 64, Hb + C_DFV + h * 64, HP, HP, HP};
;         const int ki_ = b * 8 + h * 2;
;         const float kmx0 = sqrtf(__uint_as_float((unsigned)__builtin_amdgcn_readlane((int)kmv, ki_))) * 1.01f, kmx1 = sqrtf(__uint_as_float((unsigned)__builtin_amdgcn_readlane((int)kmv, ki_ + 1))) * 1.01f;
;         at::softmax_unit<32, true, 3, false>(lds, wv, lane_id(), T, pos, qb * 128, slopes4[h] * LOG2E, 0.f, O + (size_t)b * S * OP + 1024 + h * 64, OP, kmx0, (const int*)(F.ctl + CW_PMAX), kmx1, lamv, dgain, q1ctr, &pend);
.LBB0_919:
	s_and_saveexec_b64 s[40:41], s[38:39]
	s_waitcnt vmcnt(12)
	ds_write_b32 v247, v192
	s_or_b64 exec, exec, s[40:41]
	s_waitcnt lgkmcnt(0)
	s_barrier
	ds_read_b32 v0, v247
	s_waitcnt lgkmcnt(0)
	s_barrier
	s_waitcnt lgkmcnt(0)
	v_readfirstlane_b32 s21, v0
	s_cmpk_gt_i32 s21, 0x1ff
	s_cselect_b64 s[54:55], -1, 0
	s_and_b64 vcc, exec, s[54:55]
	s_cbranch_vccnz .LBB0_918
	s_ashr_i32 s4, s21, 7
	s_and_b32 s28, s21, 1
	s_sub_i32 s44, 3, s4
	s_mul_i32 s60, s28, 0x2c00000
	s_add_u32 s29, s2, s60
	s_addc_u32 s41, s1, 0
	s_lshl_b32 s4, s44, 6
	s_lshl_b64 s[56:57], s[4:5], 1
	s_add_u32 s40, s29, s56
	s_addc_u32 s41, s41, s57
	s_add_u32 s42, s40, 0x1140
	s_addc_u32 s43, s41, 0
	s_lshl_b32 s4, s28, 3
	s_lshl_b32 s29, s44, 1
	s_add_i32 s58, s29, s4
	s_mov_b32 s4, -1
	s_mov_b32 s45, s5
	v_mbcnt_lo_u32_b32 v0, s4, 0
	v_mbcnt_hi_u32_b32 v141, s4, v0
	s_lshl_b32 s4, s21, 6
	s_and_b32 s29, s4, 0x1f80
	s_or_b32 s59, s58, 1
	s_xor_b32 s4, s29, 0x1f80
	s_lshl_b64 s[44:45], s[44:45], 2
	s_add_u32 s44, s3, s44
	s_addc_u32 s45, s20, s45
	v_readlane_b32 s21, v253, 62
	s_lshl_b32 s63, s4, 2
	v_and_b32_e32 v8, 31, v141
	s_or_b32 s21, s4, s21
	v_mov_b32_e32 v0, s63
	v_or_b32_e32 v109, s21, v8
	v_mbcnt_lo_u32_b32 v194, -1, 0
	v_mbcnt_hi_u32_b32 v194, -1, v194
	v_lshlrev_b32_e32 v194, 2, v194
	v_add_u32_e32 v194, 0x2a00, v194
	global_load_dword v195, v194, s[50:51]
	global_load_dword v194, v194, s[50:51] offset:256
	global_load_dword v142, v0, s[6:7]
	v_mov_b64_e32 v[0:1], s[40:41]
	global_load_dword v11, v31, s[44:45]
	v_ashrrev_i32_e32 v7, 5, v141
	v_mad_u64_u32 v[0:1], s[44:45], v109, s33, v[0:1]
	v_lshlrev_b32_e32 v2, 3, v7
	v_readlane_b32 s44, v254, 56
	v_ashrrev_i32_e32 v3, 31, v2
	v_readlane_b32 s45, v254, 57
	v_lshl_add_u64 v[0:1], v[2:3], 1, v[0:1]
	s_mov_b32 s45, s5
	v_lshl_add_u64 v[0:1], v[0:1], 0, s[44:45]
	global_load_dwordx4 v[16:19], v[0:1], off offset:3904
	global_load_dwordx4 v[20:23], v[0:1], off offset:3936
	s_mov_b32 s62, s44
	v_writelane_b32 v254, s62, 56
	v_mov_b64_e32 v[2:3], s[42:43]
	v_and_b32_e32 v15, 7, v141
	v_writelane_b32 v254, s63, 57
	v_lshlrev_b32_e32 v30, 4, v15
	v_readlane_b32 s44, v254, 53
	v_readlane_b32 s62, v140, s58
	v_readlane_b32 s61, v140, s59
	v_add_u32_e32 v106, s44, v141
	v_ashrrev_i32_e32 v107, 31, v106
	v_add_u32_e32 v12, 0x200, v106
	v_lshrrev_b32_e32 v0, 29, v107
	v_ashrrev_i32_e32 v10, 31, v12
	v_add_u32_e32 v0, v106, v0
	v_lshrrev_b32_e32 v10, 29, v10
	v_ashrrev_i32_e32 v9, 3, v0
	v_and_b32_e32 v0, -8, v0
	v_add_u32_e32 v14, v12, v10
	v_sub_u32_e32 v13, v106, v0
	v_add_u32_e32 v0, s4, v9
	v_ashrrev_i32_e32 v10, 3, v14
	v_and_b32_e32 v14, -8, v14
	v_mad_i64_i32 v[4:5], s[44:45], v0, s33, v[2:3]
	v_lshlrev_b32_e32 v0, 3, v13
	v_sub_u32_e32 v14, v12, v14
	v_add_u32_e32 v12, s4, v10
	v_ashrrev_i32_e32 v1, 31, v0
	s_waitcnt vmcnt(7)
	v_mad_i64_i32 v[24:25], s[44:45], v12, s33, v[2:3]
	v_lshlrev_b32_e32 v2, 3, v14
	v_lshl_add_u64 v[4:5], v[0:1], 1, v[4:5]
	v_ashrrev_i32_e32 v3, 31, v2
	v_ashrrev_i32_e32 v6, 3, v106
	v_lshl_add_u64 v[32:33], v[2:3], 1, v[24:25]
	global_load_dwordx4 v[24:27], v[4:5], off
	global_load_dwordx4 v[94:97], v[32:33], off
	v_lshl_add_u64 v[4:5], s[40:41], 0, v[30:31]
	s_mov_b64 s[40:41], 0x1340
	v_add_u32_e32 v12, s4, v6
	v_lshl_add_u64 v[4:5], v[4:5], 0, s[40:41]
	v_mad_i64_i32 v[32:33], s[40:41], v12, s33, v[4:5]
	v_add_u32_e32 v12, 64, v12
	v_mad_i64_i32 v[34:35], s[40:41], v12, s33, v[4:5]
	global_load_dwordx4 v[98:101], v[32:33], off
	global_load_dwordx4 v[102:105], v[34:35], off
	s_add_u32 s44, s6, s63
	s_movk_i32 s40, 0x80
	s_addc_u32 s45, s7, 0
	v_cmp_gt_i32_e64 s[40:41], s40, v106
	v_mov_b32_e32 v144, 0
	s_waitcnt vmcnt(6)
	v_mul_f32_e32 v143, 0x3fb8aa3b, v11
	s_waitcnt vmcnt(5)
	v_and_b32_e32 v11, 0xffff0000, v16
	v_lshlrev_b32_e32 v12, 16, v16
	v_mul_f32_e32 v11, v11, v11
	v_lshlrev_b32_e32 v32, 16, v17
	v_fmac_f32_e32 v11, v12, v12
	v_and_b32_e32 v33, 0xffff0000, v17
	v_fmac_f32_e32 v11, v32, v32
	v_lshlrev_b32_e32 v34, 16, v18
	v_fmac_f32_e32 v11, v33, v33
	v_and_b32_e32 v35, 0xffff0000, v18
	v_fmac_f32_e32 v11, v34, v34
	v_fmac_f32_e32 v11, v35, v35
	v_lshlrev_b32_e32 v12, 16, v19
	v_fmac_f32_e32 v11, v12, v12
	v_and_b32_e32 v12, 0xffff0000, v19
	v_fmac_f32_e32 v11, v12, v12
	s_waitcnt vmcnt(4)
	v_lshlrev_b32_e32 v12, 16, v20
	v_fmac_f32_e32 v11, v12, v12
	v_and_b32_e32 v12, 0xffff0000, v20
	v_fmac_f32_e32 v11, v12, v12
	v_lshlrev_b32_e32 v12, 16, v21
	v_fmac_f32_e32 v11, v12, v12
	v_and_b32_e32 v12, 0xffff0000, v21
	v_fmac_f32_e32 v11, v12, v12
	v_lshlrev_b32_e32 v12, 16, v22
	v_fmac_f32_e32 v11, v12, v12
	v_and_b32_e32 v12, 0xffff0000, v22
	v_fmac_f32_e32 v11, v12, v12
	v_lshlrev_b32_e32 v12, 16, v23
	v_fmac_f32_e32 v11, v12, v12
	v_and_b32_e32 v12, 0xffff0000, v23
	v_fmac_f32_e32 v11, v12, v12
	v_mov_b32_e32 v12, v11
	s_nop 1
	v_permlane32_swap_b32_e32 v11, v12
	s_and_saveexec_b64 s[58:59], s[40:41]
	s_cbranch_execz .LBB0_924
	v_lshl_add_u64 v[32:33], v[106:107], 2, s[44:45]
	global_load_dword v32, v[32:33], off
	s_waitcnt vmcnt(0)
	v_sub_u32_e32 v32, v32, v142
	v_cvt_f32_i32_e32 v32, v32
	v_mul_f32_e32 v144, v143, v32
.LBB0_924:
	s_or_b64 exec, exec, s[58:59]
	s_movk_i32 s58, 0x90
	v_mul_lo_u32 v145, v9, s58
	v_lshlrev_b32_e32 v146, 4, v13
	v_add_u32_e32 v13, v145, v146
	v_mul_lo_u32 v147, v10, s58
	v_lshlrev_b32_e32 v151, 4, v14
	s_waitcnt vmcnt(3)
	ds_write_b128 v13, v[24:27]
	v_add_u32_e32 v13, v147, v151
	s_movk_i32 s58, 0xc0
	s_waitcnt vmcnt(2)
	ds_write_b128 v13, v[94:97]
	v_mul_lo_u32 v13, v6, s58
	v_lshl_add_u32 v156, v15, 4, v13
	v_mov_b32_e32 v13, 0x15000
	v_lshl_add_u32 v157, v106, 2, v13
	s_waitcnt vmcnt(1)
	ds_write_b128 v156, v[98:101] offset:36864
	s_waitcnt vmcnt(0)
	ds_write_b128 v156, v[102:105] offset:49152
	s_and_saveexec_b64 s[58:59], s[40:41]
	ds_write_b32 v157, v144
	s_or_b64 exec, exec, s[58:59]
	s_cmpk_eq_i32 s29, 0x1f80
	s_cbranch_scc1 .LBB0_930
	s_add_i32 s29, s4, 0xffffff80
	v_add_u32_e32 v13, s29, v9
	v_mov_b64_e32 v[14:15], s[42:43]
	v_mad_i64_i32 v[24:25], s[42:43], v13, s33, v[14:15]
	v_add_u32_e32 v13, s29, v10
	v_mad_i64_i32 v[14:15], s[42:43], v13, s33, v[14:15]
	v_lshl_add_u64 v[24:25], v[0:1], 1, v[24:25]
	v_lshl_add_u64 v[14:15], v[2:3], 1, v[14:15]
	v_add_u32_e32 v13, s29, v6
	global_load_dwordx4 v[24:27], v[24:25], off
	s_nop 0
	global_load_dwordx4 v[94:97], v[14:15], off
	v_mad_i64_i32 v[14:15], s[42:43], v13, s33, v[4:5]
	v_add_u32_e32 v13, 64, v13
	v_mad_i64_i32 v[4:5], s[42:43], v13, s33, v[4:5]
	global_load_dwordx4 v[98:101], v[14:15], off
	global_load_dwordx4 v[102:105], v[4:5], off
	s_and_saveexec_b64 s[42:43], s[40:41]
	s_cbranch_execz .LBB0_929
	v_lshl_add_u64 v[4:5], v[106:107], 2, s[44:45]
	global_load_dword v4, v[4:5], off offset:-512
	s_waitcnt vmcnt(0)
	v_mov_b32_e32 v193, v4
	v_sub_u32_e32 v4, v4, v142
	v_cvt_f32_i32_e32 v4, v4
	v_mul_f32_e32 v144, v143, v4

; #define AT_SUB(sub_, pm_) do { bool want_; AT_WANT(2 * t + (sub_), pm_, want_); \
;         if (want_) { AT_QK(st, t * 128 + (sub_) * 64, b0 * KB2 + (sub_) * 64 * KS, BBASE + b0 * 512 + (sub_) * 256); AT_SMPV(st, VBASE + b0 * VB2 + (sub_) * 64 * VS); } } while (0)
;     ...
;     for (;;) {
;         const bool has_next = DESC ? (t > 0) : (t < t_hi); const int tn = DESC ? t - 1 : t + 1;
;         const bool has_next2 = has_next && (DESC ? (tn > 0) : (tn < t_hi)); const int tn2 = DESC ? tn - 1 : tn + 1;
;         int pm0 = 0, pm1 = 0; if (DESC) { pm0 = pmaxpre[2 * t]; pm1 = pmaxpre[2 * t + 1]; }
;         if (DESC) { AT_SUB(1, pm1); AT_SUB(0, pm0); } else { AT_SUB(0, pm0); AT_SUB(1, pm1); }
.LBB0_931:
	s_lshr_b32 s64, s58, 2
	s_and_b32 s65, s64, 63
	s_add_i32 s69, s65, 1
	v_readlane_b32 s70, v195, s65
	v_readlane_b32 s71, v194, s65
	v_readlane_b32 s65, v195, s69
	v_readlane_b32 s69, v194, s69
	s_nop 1
	s_cmp_lt_u32 s64, 64
	s_cselect_b32 s70, s70, s71
	s_cselect_b32 s65, s65, s69
	v_mov_b32_e32 v30, s70
	v_mov_b32_e32 v32, s65
	s_mov_b32 s68, s44
	s_add_i32 s44, s67, 1
	s_cmp_gt_i32 s44, s66
	s_cselect_b64 s[44:45], -1, 0
	s_or_b64 s[70:71], s[44:45], s[60:61]
	s_or_b64 s[70:71], s[70:71], s[62:63]
	s_and_b64 vcc, exec, s[70:71]
	s_cbranch_vccnz .LBB0_933
	v_sub_u32_e32 v32, v32, v142
	v_cvt_f32_i32_e32 v32, v32
	v_mul_f32_e32 v202, v143, v32
	v_pk_add_f32 v[32:33], v[110:111], v[202:203]
	s_nop 0
	v_cmp_lt_f32_e32 vcc, v32, v33
	s_cmp_eq_u64 vcc, exec
	s_cselect_b64 s[60:61], -1, 0

.LBB0_948:
	v_sub_u32_e32 v30, v30, v142
	v_cvt_f32_i32_e32 v30, v30
	v_mul_f32_e32 v202, v143, v30
	v_pk_add_f32 v[32:33], v[110:111], v[202:203]
	s_nop 0
	v_cmp_lt_f32_e32 vcc, v32, v33
	s_cmp_eq_u64 vcc, exec
	s_cselect_b64 s[60:61], -1, 0
	s_or_b64 s[44:45], s[44:45], s[60:61]
	s_and_b64 vcc, exec, s[44:45]
	s_cbranch_vccnz .LBB0_945
.LBB0_949:
	s_mul_i32 s44, s29, 0x4800
	v_add_u32_e32 v30, s44, v162
	s_lshl_b32 s69, s29, 9
	ds_read_b128 v[32:35], v30
	ds_read_b128 v[36:39], v30 offset:32
	ds_read_b128 v[40:43], v30 offset:4608
	ds_read_b128 v[122:125], v30 offset:4640
	v_add_u32_e32 v30, s69, v159
	v_add_u32_e32 v30, 0x15000, v30
	ds_read_b128 v[62:65], v30
	ds_read_b128 v[66:69], v30 offset:32
	ds_read_b128 v[70:73], v30 offset:64
	ds_read_b128 v[74:77], v30 offset:96
	ds_read_b128 v[126:129], v30 offset:128
	ds_read_b128 v[130:133], v30 offset:160
	ds_read_b128 v[134:137], v30 offset:192
	ds_read_b128 v[152:155], v30 offset:224
	s_waitcnt lgkmcnt(4)
	v_sub_f32_e32 v93, v77, v111
	v_sub_f32_e32 v92, v76, v111
	v_sub_f32_e32 v91, v75, v111
	v_sub_f32_e32 v90, v74, v111
	v_sub_f32_e32 v89, v73, v111
	v_sub_f32_e32 v88, v72, v111
	v_sub_f32_e32 v87, v71, v111
	v_sub_f32_e32 v86, v70, v111
	v_sub_f32_e32 v85, v69, v111
	v_sub_f32_e32 v84, v68, v111
	v_sub_f32_e32 v83, v67, v111
	v_sub_f32_e32 v82, v66, v111
	v_sub_f32_e32 v81, v65, v111
	v_sub_f32_e32 v80, v64, v111
	v_sub_f32_e32 v79, v63, v111
	v_sub_f32_e32 v78, v62, v111
	s_waitcnt lgkmcnt(0)
	v_sub_f32_e32 v77, v155, v111
	v_sub_f32_e32 v76, v154, v111
	v_sub_f32_e32 v75, v153, v111
	v_sub_f32_e32 v74, v152, v111
	v_sub_f32_e32 v73, v137, v111
	v_sub_f32_e32 v72, v136, v111
	v_sub_f32_e32 v71, v135, v111
	v_sub_f32_e32 v70, v134, v111
	v_sub_f32_e32 v69, v133, v111
	v_sub_f32_e32 v68, v132, v111
	v_sub_f32_e32 v67, v131, v111
	v_sub_f32_e32 v66, v130, v111
	v_sub_f32_e32 v65, v129, v111
	v_sub_f32_e32 v64, v128, v111
	v_sub_f32_e32 v63, v127, v111
	v_sub_f32_e32 v62, v126, v111
	v_mfma_f32_32x32x16_bf16 v[78:93], v[32:35], v[16:19], v[78:93]
	s_nop 0
	v_mfma_f32_32x32x16_bf16 v[62:77], v[40:43], v[16:19], v[62:77]
	v_mfma_f32_32x32x16_bf16 v[78:93], v[36:39], v[20:23], v[78:93]
	v_mfma_f32_32x32x16_bf16 v[62:77], v[122:125], v[20:23], v[62:77]
	s_cmp_le_i32 s67, s21
	s_cbranch_scc1 .LBB0_951
	v_add_u32_e32 v30, s67, v108
	v_subrev_u32_e32 v32, 63, v30
	v_cmp_gt_i32_e32 vcc, v32, v109
	s_nop 5
	v_cndmask_b32_e32 v33, v78, v200, vcc
	v_cmp_lt_i32_e32 vcc, v32, v109
	s_nop 1
	v_cndmask_b32_e32 v78, v33, v78, vcc
	v_subrev_u32_e32 v33, 61, v30
	v_cndmask_b32_e32 v79, v200, v79, vcc
	v_cmp_le_i32_e32 vcc, v33, v109
	v_subrev_u32_e32 v33, 60, v30
	s_nop 0
	v_cndmask_b32_e32 v80, v200, v80, vcc
	v_cmp_le_i32_e32 vcc, v33, v109
	v_subrev_u32_e32 v33, 31, v30
	s_nop 0
	v_cndmask_b32_e32 v81, v200, v81, vcc
	v_cmp_le_i32_e32 vcc, v32, v163
	s_nop 1
	v_cndmask_b32_e32 v82, v200, v82, vcc
	v_cmp_le_i32_e32 vcc, v32, v165
	s_nop 1
	v_cndmask_b32_e32 v83, v200, v83, vcc
	v_cmp_le_i32_e32 vcc, v32, v166
	s_nop 1
	v_cndmask_b32_e32 v84, v200, v84, vcc
	v_cmp_le_i32_e32 vcc, v32, v167
	s_nop 1
	v_cndmask_b32_e32 v85, v200, v85, vcc
	v_cmp_le_i32_e32 vcc, v32, v168
	s_nop 1
	v_cndmask_b32_e32 v86, v200, v86, vcc
	v_cmp_le_i32_e32 vcc, v32, v169
	s_nop 1
	v_cndmask_b32_e32 v87, v200, v87, vcc
	v_cmp_le_i32_e32 vcc, v32, v170
	s_nop 1
	v_cndmask_b32_e32 v88, v200, v88, vcc
	v_cmp_le_i32_e32 vcc, v32, v171
	s_nop 1
	v_cndmask_b32_e32 v89, v200, v89, vcc
	v_cmp_le_i32_e32 vcc, v32, v172
	s_nop 1
	v_cndmask_b32_e32 v90, v200, v90, vcc
	v_cmp_le_i32_e32 vcc, v32, v173
	s_nop 1
	v_cndmask_b32_e32 v91, v200, v91, vcc
	v_cmp_le_i32_e32 vcc, v32, v174
	s_nop 1
	v_cndmask_b32_e32 v92, v200, v92, vcc
	v_cmp_le_i32_e32 vcc, v32, v175
	s_nop 1
	v_cndmask_b32_e32 v93, v200, v93, vcc
	v_cmp_le_i32_e32 vcc, v33, v109
	s_nop 1
	v_cndmask_b32_e32 v62, v200, v62, vcc
	v_cmp_lt_i32_e32 vcc, v33, v109
	v_subrev_u32_e32 v33, 29, v30
	v_subrev_u32_e32 v30, 28, v30
	v_cndmask_b32_e32 v63, v200, v63, vcc
	v_cmp_le_i32_e32 vcc, v33, v109
	s_nop 1
	v_cndmask_b32_e32 v64, v200, v64, vcc
	v_cmp_le_i32_e32 vcc, v30, v109
	s_nop 1
	v_cndmask_b32_e32 v65, v200, v65, vcc
	v_cmp_le_i32_e32 vcc, v32, v176
	s_nop 1
	v_cndmask_b32_e32 v66, v200, v66, vcc
	v_cmp_le_i32_e32 vcc, v32, v177
	s_nop 1
	v_cndmask_b32_e32 v67, v200, v67, vcc
	v_cmp_le_i32_e32 vcc, v32, v178
	s_nop 1
	v_cndmask_b32_e32 v68, v200, v68, vcc
	v_cmp_le_i32_e32 vcc, v32, v179
	s_nop 1
	v_cndmask_b32_e32 v69, v200, v69, vcc
	v_cmp_le_i32_e32 vcc, v32, v180
	s_nop 1
	v_cndmask_b32_e32 v70, v200, v70, vcc
	v_cmp_le_i32_e32 vcc, v32, v181
	s_nop 1
	v_cndmask_b32_e32 v71, v200, v71, vcc
	v_cmp_le_i32_e32 vcc, v32, v205
	s_nop 1
	v_cndmask_b32_e32 v72, v200, v72, vcc
	v_cmp_le_i32_e32 vcc, v32, v206
	s_nop 1
	v_cndmask_b32_e32 v73, v200, v73, vcc
	v_cmp_le_i32_e32 vcc, v32, v207
	s_nop 1
	v_cndmask_b32_e32 v74, v200, v74, vcc
	v_cmp_le_i32_e32 vcc, v32, v208
	s_nop 1
	v_cndmask_b32_e32 v75, v200, v75, vcc
	v_cmp_le_i32_e32 vcc, v32, v209
	s_nop 1
	v_cndmask_b32_e32 v76, v200, v76, vcc
	v_cmp_le_i32_e32 vcc, v32, v210
	s_nop 1
	v_cndmask_b32_e32 v77, v200, v77, vcc

;     ...
;         if (has_next) AT_STORE(b1);
;         if (has_next2) AT_LOAD(tn2);
.LBB0_959:
	s_mul_i32 s64, s68, 0x4800
	v_add3_u32 v32, s64, v145, v146
	ds_write_b128 v32, v[24:27]
	v_add3_u32 v32, s64, v147, v151
	s_mul_i32 s64, s68, 0x6000
	ds_write_b128 v32, v[94:97]
	v_add_u32_e32 v32, s64, v156
	ds_write_b128 v32, v[98:101] offset:36864
	ds_write_b128 v32, v[102:105] offset:49152
	s_and_saveexec_b64 s[64:65], s[40:41]
	v_sub_u32_e32 v144, v193, v142
	v_cvt_f32_i32_e32 v144, v144
	v_mul_f32_e32 v144, v143, v144
	v_lshl_add_u32 v32, s68, 9, v157
	ds_write_b32 v32, v144
	s_or_b64 exec, exec, s[64:65]
	v_cmp_gt_i32_e32 vcc, 2, v211
	s_cbranch_vccnz .LBB0_965
.LBB0_962:
	v_lshl_add_u64 v[24:25], s[50:51], 0, v[120:121]
	v_lshl_add_u64 v[32:33], s[50:51], 0, v[118:119]
	global_load_dwordx4 v[24:27], v[24:25], off
	s_nop 0
	global_load_dwordx4 v[94:97], v[32:33], off
	v_lshl_add_u64 v[32:33], s[50:51], 0, v[116:117]
	v_lshl_add_u64 v[34:35], s[50:51], 0, v[114:115]
	global_load_dwordx4 v[98:101], v[32:33], off
	global_load_dwordx4 v[102:105], v[34:35], off
	s_and_saveexec_b64 s[64:65], s[40:41]
	s_cbranch_execz .LBB0_964
	global_load_dword v193, v[112:113], off

; #define LAS __attribute__((address_space(3)))
; __device__ __forceinline__ float swapsum(float a) { auto rr = __builtin_amdgcn_permlane32_swap(__float_as_uint(a), __float_as_uint(a), false, false); return __uint_as_float(rr[0]) + __uint_as_float(rr[1]); }
; __device__ __forceinline__ void lds_barrier() { asm volatile("s_waitcnt lgkmcnt(0)\n\ts_barrier" ::: "memory"); }
;     ...
;     if (nctr != nullptr && tid == 0) *pend = (int)__hip_atomic_fetch_add(nctr, 1u, __ATOMIC_RELAXED, __HIP_MEMORY_SCOPE_AGENT);
;     ...
;     l = swapsum(l);
;     if (SWA) { const float sk = sink_l2 + (ALIBI ? slope_l2 * (float)(pos[qidx] - pos_ref) : 0.f);
;         const float mnew = fmaxf(m, sk), f = __builtin_amdgcn_exp2f(m - mnew); l = l * f + __builtin_amdgcn_exp2f(sk - mnew);
; #pragma unroll
;         for (int i = 0; i < 16; ++i) { ot[0][i] *= f; ot[1][i] *= f; } }
;     const float inv = 1.f / l;
;     if (MODE == 3) {
;         LAS float* xch = (LAS float*)(lds + XCH) + wq * 64 + lane;
;         if (mp) {
; #pragma unroll
;             for (int i = 0; i < 32; ++i) xch[i * 256] = ot[i >> 4][i & 15] * inv; }
;         lds_barrier();
;         if (!mp) {
;             float o[32]; float ss = 0.f;
; #pragma unroll
;             for (int i = 0; i < 32; ++i) { o[i] = ot[i >> 4][i & 15] * inv - lam * xch[i * 256]; ss += o[i] * o[i]; }
.LBB0_967:
	v_cmp_eq_u32_e32 vcc, 0, v106
	s_and_b64 s[42:43], s[16:17], vcc
	s_and_saveexec_b64 s[40:41], s[42:43]
	s_cbranch_execz .LBB0_971
	s_mov_b64 s[44:45], exec
	v_mbcnt_lo_u32_b32 v16, s44, 0
	v_mbcnt_hi_u32_b32 v16, s45, v16
	v_cmp_eq_u32_e32 vcc, 0, v16
	s_and_saveexec_b64 s[42:43], vcc
	s_cbranch_execz .LBB0_970
	s_bcnt1_i32_b64 s4, s[44:45]
	v_mov_b32_e32 v17, s4
	global_atomic_add v192, v31, v17, s[14:15] sc0
.LBB0_970:
	s_or_b64 exec, exec, s[42:43]
.LBB0_971:
	s_or_b64 exec, exec, s[40:41]
	v_mov_b32_e32 v16, v107
	s_nop 1
	v_permlane32_swap_b32_e32 v107, v16
	v_add_f32_e32 v16, v107, v16
	v_div_scale_f32 v17, s[40:41], v16, v16, 1.0
	v_rcp_f32_e32 v18, v17
	v_readlane_b32 s40, v254, 4
	v_readlane_b32 s41, v254, 5
	v_readlane_b32 s4, v254, 14
	v_fma_f32 v19, -v17, v18, 1.0
	v_fmac_f32_e32 v18, v19, v18
	v_div_scale_f32 v19, vcc, 1.0, v16, 1.0
	v_mul_f32_e32 v20, v19, v18
	v_fma_f32 v21, -v17, v20, v19
	v_fmac_f32_e32 v20, v21, v18
	v_fma_f32 v17, -v17, v20, v19
	v_div_fmas_f32 v17, v17, v18, v20
	v_div_fixup_f32 v20, v17, v16, 1.0
	s_andn2_b64 vcc, exec, s[40:41]
	v_lshl_add_u32 v16, v141, 2, s4
	s_cbranch_vccnz .LBB0_973
	v_mul_f32_e32 v17, v46, v20
	v_mul_f32_e32 v18, v47, v20
	ds_write2st64_b32 v16, v17, v18 offset1:4
	v_mul_f32_e32 v17, v48, v20
	v_mul_f32_e32 v18, v49, v20
	ds_write2st64_b32 v16, v17, v18 offset0:8 offset1:12
	v_mul_f32_e32 v17, v50, v20
	v_mul_f32_e32 v18, v51, v20
	ds_write2st64_b32 v16, v17, v18 offset0:16 offset1:20
	v_mul_f32_e32 v17, v52, v20
	v_mul_f32_e32 v18, v53, v20
	ds_write2st64_b32 v16, v17, v18 offset0:24 offset1:28
	v_mul_f32_e32 v17, v54, v20
	v_mul_f32_e32 v18, v55, v20
	ds_write2st64_b32 v16, v17, v18 offset0:32 offset1:36
	v_mul_f32_e32 v17, v56, v20
	v_mul_f32_e32 v18, v57, v20
	ds_write2st64_b32 v16, v17, v18 offset0:40 offset1:44
	v_mul_f32_e32 v17, v58, v20
	v_mul_f32_e32 v18, v59, v20
	ds_write2st64_b32 v16, v17, v18 offset0:48 offset1:52
	v_mul_f32_e32 v17, v60, v20
	v_mul_f32_e32 v18, v61, v20
	ds_write2st64_b32 v16, v17, v18 offset0:56 offset1:60
	v_mul_f32_e32 v17, v0, v20
	v_mul_f32_e32 v18, v1, v20
	ds_write2st64_b32 v16, v17, v18 offset0:64 offset1:68
	v_mul_f32_e32 v17, v2, v20
	v_mul_f32_e32 v18, v3, v20
	ds_write2st64_b32 v16, v17, v18 offset0:72 offset1:76
	v_mul_f32_e32 v17, v4, v20
	v_mul_f32_e32 v18, v5, v20
	ds_write2st64_b32 v16, v17, v18 offset0:80 offset1:84
	v_mul_f32_e32 v17, v6, v20
	v_mul_f32_e32 v18, v7, v20
	ds_write2st64_b32 v16, v17, v18 offset0:88 offset1:92
	v_mul_f32_e32 v17, v8, v20
	v_mul_f32_e32 v18, v9, v20
	ds_write2st64_b32 v16, v17, v18 offset0:96 offset1:100
	v_mul_f32_e32 v17, v10, v20
	v_mul_f32_e32 v18, v11, v20
	ds_write2st64_b32 v16, v17, v18 offset0:104 offset1:108
	v_mul_f32_e32 v17, v12, v20
	v_mul_f32_e32 v18, v13, v20
	ds_write2st64_b32 v16, v17, v18 offset0:112 offset1:116
	v_mul_f32_e32 v17, v14, v20
	v_mul_f32_e32 v18, v15, v20
	ds_write2st64_b32 v16, v17, v18 offset0:120 offset1:124
.LBB0_973:
	s_waitcnt lgkmcnt(0)
	s_barrier
	s_andn2_b64 vcc, exec, s[36:37]
	s_cbranch_vccnz .LBB0_918
	s_waitcnt vmcnt(3)
	ds_read2st64_b32 v[26:27], v16 offset1:4
	ds_read2st64_b32 v[32:33], v16 offset0:8 offset1:12
	ds_read2st64_b32 v[34:35], v16 offset0:16 offset1:20
	ds_read2st64_b32 v[36:37], v16 offset0:24 offset1:28
	ds_read2st64_b32 v[38:39], v16 offset0:32 offset1:36
	ds_read2st64_b32 v[40:41], v16 offset0:40 offset1:44
	ds_read2st64_b32 v[42:43], v16 offset0:48 offset1:52
	ds_read2st64_b32 v[44:45], v16 offset0:56 offset1:60
	ds_read2st64_b32 v[62:63], v16 offset0:64 offset1:68
	ds_read2st64_b32 v[64:65], v16 offset0:72 offset1:76
	ds_read2st64_b32 v[66:67], v16 offset0:80 offset1:84
	ds_read2st64_b32 v[68:69], v16 offset0:88 offset1:92
	ds_read2st64_b32 v[70:71], v16 offset0:96 offset1:100
	ds_read2st64_b32 v[72:73], v16 offset0:104 offset1:108
	ds_read2st64_b32 v[18:19], v16 offset0:112 offset1:116
	ds_read2st64_b32 v[16:17], v16 offset0:120 offset1:124
	s_mulk_i32 s28, 0xa00
	s_add_u32 s4, s13, s28
	s_addc_u32 s21, s31, 0
	s_add_u32 s40, s4, s56
	s_addc_u32 s41, s21, s57
	s_waitcnt lgkmcnt(0)
	v_pk_mul_f32 v[16:17], v[28:29], v[16:17]
	s_movk_i32 s4, 0xa00
	v_pk_fma_f32 v[16:17], v[14:15], v[20:21], v[16:17] op_sel_hi:[1,0,1] neg_lo:[0,0,1] neg_hi:[0,0,1]
	v_mov_b64_e32 v[14:15], s[40:41]
	v_pk_mul_f32 v[18:19], v[28:29], v[18:19]
	v_mad_u64_u32 v[14:15], s[28:29], v109, s4, v[14:15]
	v_ashrrev_i32_e32 v109, 31, v108
	v_pk_fma_f32 v[12:13], v[12:13], v[20:21], v[18:19] op_sel_hi:[1,0,1] neg_lo:[0,0,1] neg_hi:[0,0,1]
	v_lshl_add_u64 v[18:19], v[108:109], 2, s[10:11]
	global_load_dwordx4 v[212:215], v[18:19], off
	global_load_dwordx4 v[216:219], v[18:19], off offset:32
	global_load_dwordx4 v[220:223], v[18:19], off offset:64
	global_load_dwordx4 v[224:227], v[18:19], off offset:96
	global_load_dwordx4 v[228:231], v[18:19], off offset:128
	global_load_dwordx4 v[232:235], v[18:19], off offset:160
	global_load_dwordx4 v[236:239], v[18:19], off offset:192
	global_load_dwordx4 v[240:243], v[18:19], off offset:224
	v_pk_mul_f32 v[26:27], v[28:29], v[26:27]
	v_pk_mul_f32 v[32:33], v[28:29], v[32:33]
	v_pk_fma_f32 v[26:27], v[46:47], v[20:21], v[26:27] op_sel_hi:[1,0,1] neg_lo:[0,0,1] neg_hi:[0,0,1]
	v_pk_fma_f32 v[32:33], v[48:49], v[20:21], v[32:33] op_sel_hi:[1,0,1] neg_lo:[0,0,1] neg_hi:[0,0,1]
	v_mul_f32_e32 v30, v27, v27
	v_pk_fma_f32 v[46:47], v[26:27], v[26:27], v[30:31] op_sel_hi:[1,1,0]
	v_mul_f32_e32 v30, v33, v33
	v_pk_fma_f32 v[46:47], v[32:33], v[32:33], v[46:47]
	v_pk_mul_f32 v[34:35], v[28:29], v[34:35]
	v_pk_add_f32 v[46:47], v[46:47], v[30:31] op_sel_hi:[1,0]
	v_pk_fma_f32 v[34:35], v[50:51], v[20:21], v[34:35] op_sel_hi:[1,0,1] neg_lo:[0,0,1] neg_hi:[0,0,1]
; __device__ __forceinline__ unsigned cvt_pk_bf16(float lo, float hi) { f32x2 v = {lo, hi}; bf16x2_t b = __builtin_convertvector(v, bf16x2_t); return __builtin_bit_cast(unsigned, b); }
; __device__ __forceinline__ float swapsum(float a) { auto rr = __builtin_amdgcn_permlane32_swap(__float_as_uint(a), __float_as_uint(a), false, false); return __uint_as_float(rr[0]) + __uint_as_float(rr[1]); }
;     ...
;             float o[32]; float ss = 0.f;
; #pragma unroll
;             for (int i = 0; i < 32; ++i) { o[i] = ot[i >> 4][i & 15] * inv - lam * xch[i * 256]; ss += o[i] * o[i]; }
;             const float rs = __builtin_amdgcn_rsqf(swapsum(ss) * (1.f / 64.f) + 1e-6f);
;             bf16_t* op = (bf16_t*)outp + (size_t)qidx * opitch + 4 * hf;
; #pragma unroll
;             for (int db = 0; db < 2; ++db)
; #pragma unroll
;                 for (int g = 0; g < 4; ++g) { const f32x4 gn = *(const f32x4*)(gain + 32 * db + 8 * g + 4 * hf); const int i0 = 16 * db + 4 * g;
;                     *(u32x2*)(op + 32 * db + 8 * g) = (u32x2){cvt_pk_bf16(o[i0] * rs * gn[0], o[i0 + 1] * rs * gn[1]), cvt_pk_bf16(o[i0 + 2] * rs * gn[2], o[i0 + 3] * rs * gn[3])}; }
	v_pk_mul_f32 v[36:37], v[28:29], v[36:37]
	v_pk_fma_f32 v[46:47], v[34:35], v[34:35], v[46:47]
	v_mul_f32_e32 v30, v35, v35
	v_pk_fma_f32 v[36:37], v[52:53], v[20:21], v[36:37] op_sel_hi:[1,0,1] neg_lo:[0,0,1] neg_hi:[0,0,1]
	v_pk_add_f32 v[46:47], v[46:47], v[30:31] op_sel_hi:[1,0]
	v_mul_f32_e32 v30, v37, v37
	v_pk_fma_f32 v[46:47], v[36:37], v[36:37], v[46:47]
	v_pk_mul_f32 v[38:39], v[28:29], v[38:39]
	v_pk_add_f32 v[46:47], v[46:47], v[30:31] op_sel_hi:[1,0]
	v_pk_fma_f32 v[38:39], v[54:55], v[20:21], v[38:39] op_sel_hi:[1,0,1] neg_lo:[0,0,1] neg_hi:[0,0,1]
	v_pk_mul_f32 v[40:41], v[28:29], v[40:41]
	v_pk_fma_f32 v[46:47], v[38:39], v[38:39], v[46:47]
	v_mul_f32_e32 v30, v39, v39
	v_pk_fma_f32 v[40:41], v[56:57], v[20:21], v[40:41] op_sel_hi:[1,0,1] neg_lo:[0,0,1] neg_hi:[0,0,1]
	v_pk_add_f32 v[46:47], v[46:47], v[30:31] op_sel_hi:[1,0]
	v_mul_f32_e32 v30, v41, v41
	v_pk_fma_f32 v[46:47], v[40:41], v[40:41], v[46:47]
	v_pk_mul_f32 v[42:43], v[28:29], v[42:43]
	v_pk_add_f32 v[46:47], v[46:47], v[30:31] op_sel_hi:[1,0]
	v_pk_fma_f32 v[42:43], v[58:59], v[20:21], v[42:43] op_sel_hi:[1,0,1] neg_lo:[0,0,1] neg_hi:[0,0,1]
	v_pk_mul_f32 v[44:45], v[28:29], v[44:45]
	v_pk_fma_f32 v[46:47], v[42:43], v[42:43], v[46:47]
	v_mul_f32_e32 v30, v43, v43
	v_pk_fma_f32 v[44:45], v[60:61], v[20:21], v[44:45] op_sel_hi:[1,0,1] neg_lo:[0,0,1] neg_hi:[0,0,1]
	v_pk_add_f32 v[46:47], v[46:47], v[30:31] op_sel_hi:[1,0]
	v_pk_mul_f32 v[48:49], v[28:29], v[64:65]
	v_pk_fma_f32 v[46:47], v[44:45], v[44:45], v[46:47]
	v_mul_f32_e32 v30, v45, v45
	v_pk_fma_f32 v[48:49], v[2:3], v[20:21], v[48:49] op_sel_hi:[1,0,1] neg_lo:[0,0,1] neg_hi:[0,0,1]
	v_pk_mul_f32 v[2:3], v[28:29], v[62:63]
	v_pk_add_f32 v[46:47], v[46:47], v[30:31] op_sel_hi:[1,0]
	v_pk_fma_f32 v[50:51], v[0:1], v[20:21], v[2:3] op_sel_hi:[1,0,1] neg_lo:[0,0,1] neg_hi:[0,0,1]
	v_lshl_add_u64 v[14:15], v[108:109], 1, v[14:15]
	v_pk_fma_f32 v[0:1], v[50:51], v[50:51], v[46:47]
	v_mul_f32_e32 v2, v51, v51
	v_pk_add_f32 v[0:1], v[0:1], v[2:3] op_sel_hi:[1,0]
	v_mul_f32_e32 v2, v49, v49
	v_pk_fma_f32 v[0:1], v[48:49], v[48:49], v[0:1]
	s_nop 0
	v_pk_add_f32 v[0:1], v[0:1], v[2:3] op_sel_hi:[1,0]
	v_pk_mul_f32 v[2:3], v[28:29], v[68:69]
	s_nop 0
	v_pk_fma_f32 v[6:7], v[6:7], v[20:21], v[2:3] op_sel_hi:[1,0,1] neg_lo:[0,0,1] neg_hi:[0,0,1]
	v_pk_mul_f32 v[2:3], v[28:29], v[66:67]
	s_nop 0
	v_pk_fma_f32 v[4:5], v[4:5], v[20:21], v[2:3] op_sel_hi:[1,0,1] neg_lo:[0,0,1] neg_hi:[0,0,1]
	s_nop 0
	v_pk_fma_f32 v[0:1], v[4:5], v[4:5], v[0:1]
	v_mul_f32_e32 v2, v5, v5
	v_pk_add_f32 v[0:1], v[0:1], v[2:3] op_sel_hi:[1,0]
	v_mul_f32_e32 v2, v7, v7
	v_pk_fma_f32 v[0:1], v[6:7], v[6:7], v[0:1]
	s_nop 0
	v_pk_add_f32 v[0:1], v[0:1], v[2:3] op_sel_hi:[1,0]
	v_pk_mul_f32 v[2:3], v[28:29], v[72:73]
	s_nop 0
	v_pk_fma_f32 v[10:11], v[10:11], v[20:21], v[2:3] op_sel_hi:[1,0,1] neg_lo:[0,0,1] neg_hi:[0,0,1]
	v_pk_mul_f32 v[2:3], v[28:29], v[70:71]
	s_nop 0
	v_pk_fma_f32 v[8:9], v[8:9], v[20:21], v[2:3] op_sel_hi:[1,0,1] neg_lo:[0,0,1] neg_hi:[0,0,1]
	s_nop 0
	v_pk_fma_f32 v[0:1], v[8:9], v[8:9], v[0:1]
	v_mul_f32_e32 v2, v9, v9
	v_pk_add_f32 v[0:1], v[0:1], v[2:3] op_sel_hi:[1,0]
	v_mul_f32_e32 v2, v11, v11
	v_pk_fma_f32 v[0:1], v[10:11], v[10:11], v[0:1]
	s_nop 0
	v_pk_add_f32 v[0:1], v[0:1], v[2:3] op_sel_hi:[1,0]
	v_mul_f32_e32 v2, v13, v13
	v_pk_fma_f32 v[0:1], v[12:13], v[12:13], v[0:1]
	s_nop 0
	v_pk_add_f32 v[0:1], v[0:1], v[2:3] op_sel_hi:[1,0]
	v_mul_f32_e32 v2, v17, v17
	v_pk_fma_f32 v[0:1], v[16:17], v[16:17], v[0:1]
	s_nop 0
	v_pk_add_f32 v[0:1], v[0:1], v[2:3] op_sel_hi:[1,0]
	s_nop 0
	v_mov_b32_e32 v1, v0
	s_nop 1
	v_permlane32_swap_b32_e32 v0, v1
	v_add_f32_e32 v0, v0, v1
	v_fmamk_f32 v0, v0, 0x3c800000, v246
	v_rsq_f32_e32 v20, v0
	s_nop 0
	v_pk_mul_f32 v[0:1], v[26:27], v[20:21] op_sel_hi:[1,0]
	v_pk_mul_f32 v[2:3], v[32:33], v[20:21] op_sel_hi:[1,0]
	s_waitcnt vmcnt(7)
	v_pk_mul_f32 v[0:1], v[212:213], v[0:1]
	v_pk_mul_f32 v[2:3], v[214:215], v[2:3]
	v_cvt_pk_bf16_f32 v212, v0, v1
	v_cvt_pk_bf16_f32 v213, v2, v3
	v_pk_mul_f32 v[22:23], v[34:35], v[20:21] op_sel_hi:[1,0]
	v_pk_mul_f32 v[4:5], v[4:5], v[20:21] op_sel_hi:[1,0]
	s_waitcnt vmcnt(6)
	v_pk_mul_f32 v[0:1], v[216:217], v[22:23]
	v_pk_mul_f32 v[22:23], v[36:37], v[20:21] op_sel_hi:[1,0]
	v_cvt_pk_bf16_f32 v216, v0, v1
	v_pk_mul_f32 v[2:3], v[218:219], v[22:23]
	v_pk_mul_f32 v[22:23], v[38:39], v[20:21] op_sel_hi:[1,0]
	v_cvt_pk_bf16_f32 v217, v2, v3
	s_waitcnt vmcnt(5)
	v_pk_mul_f32 v[0:1], v[220:221], v[22:23]
	v_pk_mul_f32 v[22:23], v[40:41], v[20:21] op_sel_hi:[1,0]
	v_cvt_pk_bf16_f32 v220, v0, v1
	v_pk_mul_f32 v[2:3], v[222:223], v[22:23]
	v_pk_mul_f32 v[22:23], v[42:43], v[20:21] op_sel_hi:[1,0]
	v_cvt_pk_bf16_f32 v221, v2, v3
	s_waitcnt vmcnt(4)
	v_pk_mul_f32 v[0:1], v[22:23], v[224:225]
	v_pk_mul_f32 v[22:23], v[44:45], v[20:21] op_sel_hi:[1,0]
	v_cvt_pk_bf16_f32 v224, v0, v1
	v_pk_mul_f32 v[2:3], v[22:23], v[226:227]
	v_pk_mul_f32 v[22:23], v[50:51], v[20:21] op_sel_hi:[1,0]
	v_cvt_pk_bf16_f32 v225, v2, v3
	s_waitcnt vmcnt(3)
	v_pk_mul_f32 v[0:1], v[22:23], v[228:229]
	v_pk_mul_f32 v[22:23], v[48:49], v[20:21] op_sel_hi:[1,0]
	v_cvt_pk_bf16_f32 v214, v0, v1
	v_pk_mul_f32 v[2:3], v[22:23], v[230:231]
	s_nop 0
	v_cvt_pk_bf16_f32 v215, v2, v3
	s_waitcnt vmcnt(2)
	v_pk_mul_f32 v[0:1], v[4:5], v[232:233]
	v_pk_mul_f32 v[4:5], v[6:7], v[20:21] op_sel_hi:[1,0]
	v_cvt_pk_bf16_f32 v218, v0, v1
	v_pk_mul_f32 v[2:3], v[4:5], v[234:235]
	v_pk_mul_f32 v[4:5], v[8:9], v[20:21] op_sel_hi:[1,0]
	v_cvt_pk_bf16_f32 v219, v2, v3
	s_waitcnt vmcnt(1)
	v_pk_mul_f32 v[0:1], v[4:5], v[236:237]
	v_pk_mul_f32 v[4:5], v[10:11], v[20:21] op_sel_hi:[1,0]
	v_cvt_pk_bf16_f32 v222, v0, v1
	v_pk_mul_f32 v[2:3], v[4:5], v[238:239]
	v_pk_mul_f32 v[4:5], v[12:13], v[20:21] op_sel_hi:[1,0]
	v_cvt_pk_bf16_f32 v223, v2, v3
	s_waitcnt vmcnt(0)
	v_pk_mul_f32 v[0:1], v[4:5], v[240:241]
	v_pk_mul_f32 v[4:5], v[16:17], v[20:21] op_sel_hi:[1,0]
	v_cvt_pk_bf16_f32 v226, v0, v1
	v_pk_mul_f32 v[2:3], v[4:5], v[242:243]
	s_nop 0
	v_cvt_pk_bf16_f32 v227, v2, v3
	s_nop 1
	v_permlane32_swap_b32_e32 v212, v214
	v_permlane32_swap_b32_e32 v213, v215
	v_permlane32_swap_b32_e32 v216, v218
	v_permlane32_swap_b32_e32 v217, v219
	v_permlane32_swap_b32_e32 v220, v222
	v_permlane32_swap_b32_e32 v221, v223
	v_permlane32_swap_b32_e32 v224, v226
	v_permlane32_swap_b32_e32 v225, v227
	v_mbcnt_lo_u32_b32 v22, -1, 0
	v_mbcnt_hi_u32_b32 v22, -1, v22
	v_lshrrev_b32_e32 v22, 5, v22
	v_mul_u32_u24_e32 v22, 56, v22
	v_mov_b32_e32 v23, 0
	v_lshl_add_u64 v[14:15], v[22:23], 0, v[14:15]
	global_store_dwordx4 v[14:15], v[212:215], off offset:2048
	global_store_dwordx4 v[14:15], v[216:219], off offset:2064
	global_store_dwordx4 v[14:15], v[220:223], off offset:2080
	global_store_dwordx4 v[14:15], v[224:227], off offset:2096
	s_branch .LBB0_918

; #define LAS __attribute__((address_space(3)))
; __device__ __forceinline__ void lds_barrier() { asm volatile("s_waitcnt lgkmcnt(0)\n\ts_barrier" ::: "memory"); }
; __device__ __forceinline__ int claim_take(LAS unsigned char* lds, int tid, const int* pend) {
;     if (tid == 0) *(volatile LAS int*)(lds + QSLOT) = *pend;
;     lds_barrier();
;     const int v = __builtin_amdgcn_readfirstlane(*(volatile LAS int*)(lds + QSLOT));
;     lds_barrier();
;     return v;
.LBB0_995:
	s_or_b64 exec, exec, s[16:17]
	s_waitcnt vmcnt(0)
	v_readfirstlane_b32 s3, v1
	s_nop 1
	v_add_u32_e32 v164, s3, v0
	v_mov_b32_e32 v192, v164

; __device__ __forceinline__ unsigned cvt_pk_bf16(float lo, float hi) { f32x2 v = {lo, hi}; bf16x2_t b = __builtin_convertvector(v, bf16x2_t); return __builtin_bit_cast(unsigned, b); }
; __device__ __forceinline__ void sb_unit(LAS unsigned char* lds, int wv, int lane, const Tens T, int q0, bf16_t* outp, int opitch, unsigned* nctr, int* pend) {
;     ...
;     if (tid == 0) *pend = (int)__hip_atomic_fetch_add(nctr, 1u, __ATOMIC_RELAXED, __HIP_MEMORY_SCOPE_AGENT);
;     bf16_t* op = outp + (size_t)qidx * opitch + 4 * hf;
; #pragma unroll
;     for (int db = 0; db < 2; ++db)
; #pragma unroll
;         for (int g = 0; g < 4; ++g) *(u32x2*)(op + 32 * db + 8 * g) = (u32x2){cvt_pk_bf16(ot[db][4 * g], ot[db][4 * g + 1]), cvt_pk_bf16(ot[db][4 * g + 2], ot[db][4 * g + 3])};
.LBB0_998:
	s_or_b64 exec, exec, s[16:17]
	s_mulk_i32 s3, 0xa00
	s_add_u32 s3, s13, s3
	s_addc_u32 s17, s31, 0
	s_lshl_b32 s4, s4, 1
	s_add_u32 s16, s3, s4
	s_addc_u32 s17, s17, 0
	v_mov_b64_e32 v[16:17], s[16:17]
	s_movk_i32 s3, 0xa00
	v_mad_i64_i32 v[16:17], s[16:17], v28, s3, v[16:17]
	v_lshlrev_b32_e32 v18, 1, v30
	v_mov_b32_e32 v19, v31
	v_lshl_add_u64 v[16:17], v[16:17], 0, v[18:19]
	v_cvt_pk_bf16_f32 v0, v0, v1
	v_cvt_pk_bf16_f32 v1, v2, v3
	v_cvt_pk_bf16_f32 v4, v4, v5
	v_cvt_pk_bf16_f32 v5, v6, v7
	v_cvt_pk_bf16_f32 v8, v8, v9
	v_cvt_pk_bf16_f32 v9, v10, v11
	v_cvt_pk_bf16_f32 v12, v12, v13
	v_cvt_pk_bf16_f32 v13, v14, v15
	v_cvt_pk_bf16_f32 v2, v32, v33
	v_cvt_pk_bf16_f32 v3, v34, v35
	v_cvt_pk_bf16_f32 v6, v36, v37
	v_cvt_pk_bf16_f32 v7, v38, v39
	v_cvt_pk_bf16_f32 v10, v40, v41
	v_cvt_pk_bf16_f32 v11, v42, v43
	v_cvt_pk_bf16_f32 v14, v44, v45
	v_cvt_pk_bf16_f32 v15, v46, v47
	s_nop 1
	v_permlane32_swap_b32_e32 v0, v2
	v_permlane32_swap_b32_e32 v1, v3
	v_permlane32_swap_b32_e32 v4, v6
	v_permlane32_swap_b32_e32 v5, v7
	v_permlane32_swap_b32_e32 v8, v10
	v_permlane32_swap_b32_e32 v9, v11
	v_permlane32_swap_b32_e32 v12, v14
	v_permlane32_swap_b32_e32 v13, v15
	v_mbcnt_lo_u32_b32 v18, -1, 0
	v_mbcnt_hi_u32_b32 v18, -1, v18
	v_lshrrev_b32_e32 v18, 5, v18
	v_mul_u32_u24_e32 v18, 56, v18
	v_add_co_u32_e32 v16, vcc, v16, v18
	s_nop 1
	v_addc_co_u32_e32 v17, vcc, 0, v17, vcc
	global_store_dwordx4 v[16:17], v[0:3], off offset:512
	global_store_dwordx4 v[16:17], v[4:7], off offset:528
	global_store_dwordx4 v[16:17], v[8:11], off offset:544
	global_store_dwordx4 v[16:17], v[12:15], off offset:560

; #define LAS __attribute__((address_space(3)))
; __device__ __forceinline__ void lds_barrier() { asm volatile("s_waitcnt lgkmcnt(0)\n\ts_barrier" ::: "memory"); }
; #define SB_LOAD(t_) do { const int k0_ = (t_) * 64; kreg = *(const u32x4*)(T.k + (size_t)(k0_ + vr) * T.kp + vc * 8); vreg = *(const u32x4*)(T.v + (size_t)(k0_ + vr) * T.vp + vc * 8); } while (0)
; #define SB_STORE(buf_) do { *(LAS u32x4*)(lds + ((buf_) ? KB1 : KB0) + vr * KS + vc * 16) = kreg; *(LAS u32x4*)(lds + ((buf_) ? VB1 : VB0) + vr * VS + vc * 16) = vreg; } while (0)
; __device__ __forceinline__ int claim_take(LAS unsigned char* lds, int tid, const int* pend) {
;     if (tid == 0) *(volatile LAS int*)(lds + QSLOT) = *pend;
;     lds_barrier();
;     const int v = __builtin_amdgcn_readfirstlane(*(volatile LAS int*)(lds + QSLOT));
;     lds_barrier();
;     return v;
; }
; __device__ __forceinline__ void sb_unit(LAS unsigned char* lds, int wv, int lane, const Tens T, int q0, bf16_t* outp, int opitch, unsigned* nctr, int* pend) {
;     constexpr int KS = 144;
;     const int tid = wv * 64 + lane, r32 = lane & 31, hf = lane >> 5;
;     const int qmin = q0 + 32 * wv, qidx = qmin + r32, qmax = qmin + 31;
;     const int t_hi = (q0 + 255) >> 6;
;     bf16x8 qf[4];
;     { const bf16_t* qr = T.q + (size_t)qidx * T.qp + 8 * hf;
; #pragma unroll
;       for (int c = 0; c < 4; ++c) qf[c] = *(const bf16x8*)(qr + 16 * c); }
;     f32x16 ot[2];
; #pragma unroll
;     for (int i = 0; i < 16; ++i) { ot[0][i] = 0.f; ot[1][i] = 0.f; }
;     float R = 0.f; bool done = false;
;     u32x4 kreg, vreg;
;     const int vr = tid >> 3, vc = tid & 7;
;     ...
;     SB_LOAD(t_hi); SB_STORE(0); __syncthreads();
;     int buf = 0, par = 0;
.LBB0_1000:
	s_and_saveexec_b64 s[14:15], s[38:39]
	s_waitcnt vmcnt(4)
	ds_write_b32 v247, v192
	s_or_b64 exec, exec, s[14:15]
	s_waitcnt lgkmcnt(0)
	s_barrier
	ds_read_b32 v0, v247
	s_waitcnt lgkmcnt(0)
	s_barrier
	s_waitcnt lgkmcnt(0)
	v_readfirstlane_b32 s16, v0
	s_cmpk_gt_i32 s16, 0xff
	s_cselect_b64 s[14:15], -1, 0
	s_and_b64 vcc, exec, s[14:15]
	s_cbranch_vccnz .LBB0_999
	s_lshl_b32 s3, s16, 11
	s_and_b32 s3, s3, 0x2000
	s_mul_i32 s4, s3, 0x1600
	s_add_u32 s17, s2, s4
	s_addc_u32 s20, s1, 0
	s_lshl_b32 s4, s16, 6
	s_and_b32 s4, s4, 0xc0
	s_lshl_b32 s21, s4, 1
	s_add_u32 s28, s17, s21
	s_mov_b32 s17, -1
	s_addc_u32 s29, s20, 0
	s_lshl_b32 s16, s16, 5
	v_mbcnt_lo_u32_b32 v0, s17, 0
	v_mbcnt_hi_u32_b32 v6, s17, v0
	s_and_b32 s16, s16, 0xffffff00
	v_readlane_b32 s17, v254, 17
	s_sub_i32 s21, s17, s16
	v_and_b32_e32 v7, 31, v6
	s_add_i32 s17, s21, 0x1f00
	v_or_b32_e32 v28, s17, v7
	v_mov_b64_e32 v[0:1], s[28:29]
	s_sub_i32 s34, 0x1fff, s16
	v_mad_i64_i32 v[2:3], s[16:17], v28, s33, v[0:1]
	v_lshrrev_b32_e32 v8, 5, v6
	v_readlane_b32 s16, v254, 53
	v_lshlrev_b32_e32 v4, 4, v8
	v_mov_b32_e32 v5, v31
	v_add_u32_e32 v140, s16, v6
	v_lshl_add_u64 v[2:3], v[2:3], 0, v[4:5]
	v_ashrrev_i32_e32 v5, 3, v140
	s_and_b32 s16, s34, 0x7fffffc0
	global_load_dwordx4 v[16:19], v[2:3], off offset:832
	global_load_dwordx4 v[20:23], v[2:3], off offset:864
	global_load_dwordx4 v[24:27], v[2:3], off offset:896
	global_load_dwordx4 v[80:83], v[2:3], off offset:928
	v_and_b32_e32 v2, 7, v6
	v_add_u32_e32 v3, s16, v5
	v_mad_i64_i32 v[0:1], s[16:17], v3, s33, v[0:1]
	v_lshlrev_b32_e32 v2, 4, v2
	v_mov_b32_e32 v3, v31
	v_lshl_add_u64 v[0:1], v[0:1], 0, v[2:3]
	global_load_dwordx4 v[84:87], v[0:1], off offset:1344
	global_load_dwordx4 v[88:91], v[0:1], off offset:1856
	s_movk_i32 s42, 0x90
	v_lshlrev_b32_e32 v30, 2, v8
	v_lshrrev_b32_e32 v0, 2, v6
	v_mad_u64_u32 v[92:93], s[16:17], v5, s42, v[2:3]
	s_waitcnt vmcnt(8)
	v_lshl_add_u64 v[96:97], s[28:29], 0, v[2:3]
	v_and_or_b32 v0, v0, 3, v30
	v_and_b32_e32 v1, 16, v6
	v_lshlrev_b32_e32 v2, 2, v6
	v_mad_u64_u32 v[94:95], s[16:17], v5, 48, v[92:93]
	v_mul_u32_u24_e32 v0, 0xc0, v0
	v_and_or_b32 v1, v2, 12, v1
	v_mov_b32_e32 v14, v31
	v_mov_b32_e32 v15, v31
	s_lshr_b32 s35, s34, 6
	v_cmp_eq_u32_e64 s[40:41], 0, v6
	v_mad_u32_u24 v93, v7, s42, v4
	v_cmp_gt_u32_e64 s[42:43], 32, v6
	v_lshl_or_b32 v95, v1, 1, v0
	v_subrev_u32_e32 v141, 64, v5
	v_mov_b32_e32 v0, v31
	v_mov_b32_e32 v1, v31
	v_mov_b32_e32 v2, v31
	v_mov_b32_e32 v4, v31
	v_mov_b32_e32 v5, v31
	v_mov_b32_e32 v6, v31
	v_mov_b32_e32 v7, v31
	v_mov_b32_e32 v8, v31
	v_mov_b32_e32 v9, v31
	v_mov_b32_e32 v10, v31
	v_mov_b32_e32 v11, v31
	v_mov_b32_e32 v12, v31
	v_mov_b32_e32 v13, v31
	v_mov_b64_e32 v[46:47], v[14:15]
	s_mov_b32 s20, 0
	s_addk_i32 s21, 0x1f1f
	v_mov_b32_e32 v29, v28
	s_and_b32 s28, s34, 0xffffffc0
	s_waitcnt vmcnt(7)
	v_mov_b32_e32 v98, 0
	s_mov_b64 s[16:17], 0
	v_mov_b32_e32 v142, s35
	v_mov_b64_e32 v[44:45], v[12:13]
	v_mov_b64_e32 v[42:43], v[10:11]
	v_mov_b64_e32 v[40:41], v[8:9]
	v_mov_b64_e32 v[38:39], v[6:7]
	v_mov_b64_e32 v[36:37], v[4:5]
	v_mov_b64_e32 v[34:35], v[2:3]
	v_mov_b64_e32 v[32:33], v[0:1]
	s_mov_b32 s29, 0
	s_waitcnt vmcnt(1)
	ds_write_b128 v92, v[84:87]
	s_waitcnt vmcnt(0)
	ds_write_b128 v94, v[88:91] offset:26624
	s_waitcnt lgkmcnt(0)
	s_barrier
	s_branch .LBB0_1005

; __device__ __forceinline__ void sb_unit(LAS unsigned char* lds, int wv, int lane, const Tens T, int q0, bf16_t* outp, int opitch, unsigned* nctr, int* pend) {
;     ...
;     if (tid == 0) *pend = (int)__hip_atomic_fetch_add(nctr, 1u, __ATOMIC_RELAXED, __HIP_MEMORY_SCOPE_AGENT);
.LBB0_1016:
	v_cmp_eq_u32_e32 vcc, 0, v140
	s_and_saveexec_b64 s[16:17], vcc
	s_cbranch_execz .LBB0_998
	s_mov_b64 s[40:41], exec
	v_mbcnt_lo_u32_b32 v16, s40, 0
	v_mbcnt_hi_u32_b32 v16, s41, v16
	v_cmp_eq_u32_e32 vcc, 0, v16
	s_and_saveexec_b64 s[34:35], vcc
	s_cbranch_execz .LBB0_997
	s_bcnt1_i32_b64 s20, s[40:41]
	v_mov_b32_e32 v17, s20
	global_atomic_add v192, v31, v17, s[52:53] offset:768 sc0
	s_branch .LBB0_997

; __device__ __forceinline__ unsigned cvt_pk_bf16(float lo, float hi) { f32x2 v = {lo, hi}; bf16x2_t b = __builtin_convertvector(v, bf16x2_t); return __builtin_bit_cast(unsigned, b); }
; __device__ __forceinline__ float swapsum(float a) { auto rr = __builtin_amdgcn_permlane32_swap(__float_as_uint(a), __float_as_uint(a), false, false); return __uint_as_float(rr[0]) + __uint_as_float(rr[1]); }
;     ...
;     l = swapsum(l);
;     if (SWA) { const float sk = sink_l2 + (ALIBI ? slope_l2 * (float)(pos[qidx] - pos_ref) : 0.f);
;         const float mnew = fmaxf(m, sk), f = __builtin_amdgcn_exp2f(m - mnew); l = l * f + __builtin_amdgcn_exp2f(sk - mnew);
; #pragma unroll
;         for (int i = 0; i < 16; ++i) { ot[0][i] *= f; ot[1][i] *= f; } }
;     const float inv = 1.f / l;
;     ...
;     else { bf16_t* op = (bf16_t*)outp + (size_t)qidx * opitch + 4 * hf + hsel * 64;
; #pragma unroll
;         for (int db = 0; db < 2; ++db)
; #pragma unroll
;             for (int g = 0; g < 4; ++g) *(u32x2*)(op + 32 * db + 8 * g) = (u32x2){cvt_pk_bf16(ot[db][4 * g] * inv, ot[db][4 * g + 1] * inv), cvt_pk_bf16(ot[db][4 * g + 2] * inv, ot[db][4 * g + 3] * inv)}; }
.LBB0_1025:
	s_or_b64 exec, exec, s[40:41]
	v_lshl_add_u64 v[0:1], v[112:113], 2, s[6:7]
	global_load_dword v0, v[0:1], off
	s_mulk_i32 s62, 0xa00
	v_mov_b32_e32 v2, v119
	s_add_u32 s3, s13, s62
	s_nop 0
	v_permlane32_swap_b32_e32 v119, v2
	s_addc_u32 s28, s31, 0
	s_lshl_b32 s20, s21, 1
	s_add_u32 s20, s3, s20
	s_addc_u32 s21, s28, 0
	s_movk_i32 s3, 0xa00
	v_ashrrev_i32_e32 v117, 31, v116
	s_waitcnt vmcnt(0)
	v_sub_u32_e32 v0, v0, v115
	v_cvt_f32_i32_e32 v251, v0
	v_mov_b32_e32 v115, v122
	v_pk_mul_f32 v[0:1], v[114:115], v[250:251]
	s_nop 0
	v_add_f32_e32 v0, v0, v1
	v_max_f32_e32 v1, v172, v172
	v_max_f32_e32 v1, v1, v0
	v_sub_f32_e32 v3, v172, v1
	v_sub_f32_e32 v0, v0, v1
	v_exp_f32_e32 v4, v3
	v_exp_f32_e32 v0, v0
	v_add_f32_e32 v1, v119, v2
	v_fmac_f32_e32 v0, v1, v4
	v_div_scale_f32 v1, s[28:29], v0, v0, 1.0
	v_rcp_f32_e32 v2, v1
	s_nop 0
	v_fma_f32 v3, -v1, v2, 1.0
	v_fmac_f32_e32 v2, v3, v2
	v_div_scale_f32 v3, vcc, 1.0, v0, 1.0
	v_mul_f32_e32 v5, v3, v2
	v_fma_f32 v6, -v1, v5, v3
	v_fmac_f32_e32 v5, v6, v2
	v_fma_f32 v1, -v1, v5, v3
	v_div_fmas_f32 v1, v1, v2, v5
	v_mov_b64_e32 v[2:3], s[20:21]
	v_div_fixup_f32 v0, v1, v0, 1.0
	v_mad_i64_i32 v[2:3], s[20:21], v112, s3, v[2:3]
	v_pk_mul_f32 v[6:7], v[48:49], v[4:5] op_sel_hi:[1,0]
	v_pk_mul_f32 v[8:9], v[50:51], v[4:5] op_sel_hi:[1,0]
	v_lshl_add_u64 v[2:3], v[116:117], 1, v[2:3]
	v_pk_mul_f32 v[6:7], v[6:7], v[0:1] op_sel_hi:[1,0]
	v_pk_mul_f32 v[8:9], v[8:9], v[0:1] op_sel_hi:[1,0]
	v_lshl_add_u64 v[2:3], v[2:3], 0, s[4:5]
	v_cvt_pk_bf16_f32 v48, v6, v7
	v_cvt_pk_bf16_f32 v49, v8, v9
	v_pk_mul_f32 v[6:7], v[52:53], v[4:5] op_sel_hi:[1,0]
	v_pk_mul_f32 v[8:9], v[54:55], v[4:5] op_sel_hi:[1,0]
	v_pk_mul_f32 v[6:7], v[6:7], v[0:1] op_sel_hi:[1,0]
	v_pk_mul_f32 v[8:9], v[8:9], v[0:1] op_sel_hi:[1,0]
	v_cvt_pk_bf16_f32 v52, v6, v7
	v_cvt_pk_bf16_f32 v53, v8, v9
	v_pk_mul_f32 v[6:7], v[56:57], v[4:5] op_sel_hi:[1,0]
	v_pk_mul_f32 v[8:9], v[58:59], v[4:5] op_sel_hi:[1,0]
	v_pk_mul_f32 v[6:7], v[6:7], v[0:1] op_sel_hi:[1,0]
	v_pk_mul_f32 v[8:9], v[8:9], v[0:1] op_sel_hi:[1,0]
	v_cvt_pk_bf16_f32 v56, v6, v7
	v_cvt_pk_bf16_f32 v57, v8, v9
	v_pk_mul_f32 v[6:7], v[60:61], v[4:5] op_sel_hi:[1,0]
	v_pk_mul_f32 v[8:9], v[62:63], v[4:5] op_sel_hi:[1,0]
	v_pk_mul_f32 v[6:7], v[6:7], v[0:1] op_sel_hi:[1,0]
	v_pk_mul_f32 v[8:9], v[8:9], v[0:1] op_sel_hi:[1,0]
	v_cvt_pk_bf16_f32 v60, v6, v7
	v_cvt_pk_bf16_f32 v61, v8, v9
	v_pk_mul_f32 v[6:7], v[32:33], v[4:5] op_sel_hi:[1,0]
	v_pk_mul_f32 v[8:9], v[34:35], v[4:5] op_sel_hi:[1,0]
	v_pk_mul_f32 v[6:7], v[6:7], v[0:1] op_sel_hi:[1,0]
	v_pk_mul_f32 v[8:9], v[8:9], v[0:1] op_sel_hi:[1,0]
	v_cvt_pk_bf16_f32 v50, v6, v7
	v_cvt_pk_bf16_f32 v51, v8, v9
	v_pk_mul_f32 v[6:7], v[36:37], v[4:5] op_sel_hi:[1,0]
	v_pk_mul_f32 v[8:9], v[38:39], v[4:5] op_sel_hi:[1,0]
	v_pk_mul_f32 v[6:7], v[6:7], v[0:1] op_sel_hi:[1,0]
	v_pk_mul_f32 v[8:9], v[8:9], v[0:1] op_sel_hi:[1,0]
	v_cvt_pk_bf16_f32 v54, v6, v7
	v_cvt_pk_bf16_f32 v55, v8, v9
	v_pk_mul_f32 v[6:7], v[40:41], v[4:5] op_sel_hi:[1,0]
	v_pk_mul_f32 v[8:9], v[42:43], v[4:5] op_sel_hi:[1,0]
	v_pk_mul_f32 v[6:7], v[6:7], v[0:1] op_sel_hi:[1,0]
	v_pk_mul_f32 v[8:9], v[8:9], v[0:1] op_sel_hi:[1,0]
	v_cvt_pk_bf16_f32 v58, v6, v7
	v_cvt_pk_bf16_f32 v59, v8, v9
	v_pk_mul_f32 v[6:7], v[44:45], v[4:5] op_sel_hi:[1,0]
	v_pk_mul_f32 v[4:5], v[46:47], v[4:5] op_sel_hi:[1,0]
	v_pk_mul_f32 v[6:7], v[6:7], v[0:1] op_sel_hi:[1,0]
	v_pk_mul_f32 v[0:1], v[4:5], v[0:1] op_sel_hi:[1,0]
	v_cvt_pk_bf16_f32 v62, v6, v7
	v_cvt_pk_bf16_f32 v63, v0, v1
	s_nop 1
	v_permlane32_swap_b32_e32 v48, v50
	v_permlane32_swap_b32_e32 v49, v51
	v_permlane32_swap_b32_e32 v52, v54
	v_permlane32_swap_b32_e32 v53, v55
	v_permlane32_swap_b32_e32 v56, v58
	v_permlane32_swap_b32_e32 v57, v59
	v_permlane32_swap_b32_e32 v60, v62
	v_permlane32_swap_b32_e32 v61, v63
	v_mbcnt_lo_u32_b32 v8, -1, 0
	v_mbcnt_hi_u32_b32 v8, -1, v8
	v_lshrrev_b32_e32 v8, 5, v8
	v_mul_u32_u24_e32 v8, 56, v8
	v_add_co_u32_e32 v2, vcc, v2, v8
	s_nop 1
	v_addc_co_u32_e32 v3, vcc, 0, v3, vcc
	global_store_dwordx4 v[2:3], v[48:51], off offset:1024
	global_store_dwordx4 v[2:3], v[52:55], off offset:1040
	global_store_dwordx4 v[2:3], v[56:59], off offset:1056
	global_store_dwordx4 v[2:3], v[60:63], off offset:1072

; template <int lda, int ldb, class Epi, class Sched>
; __device__ __forceinline__ void gemm_phase(LAS unsigned char* lds, int wid, int lane, const char* baseA, const char* baseB, const Sched& S, const Epi& E) {
;     const int tid = wid * 64 + lane, wr = wid >> 2, wc = wid & 3, fr = lane & 15, fq = lane >> 4;
;     unsigned voffA[2], voffB[2]; int gR[2], gC[2];
; #pragma unroll
;     for (int i = 0; i < 2; ++i) { int R, C; stage_rc(tid * 16 + i * 8192, R, C); const int Rb = Epi::PERM ? ((R & ~31) + perm32(R & 31)) : R;
;         voffA[i] = (unsigned)(R * lda + C) * 2u; voffB[i] = (unsigned)(Rb * ldb + C) * 2u; gR[i] = R; gC[i] = C; }
;     __device__ __forceinline__ void pre(u32x2 (&pf)[8], const g8::Unit& u, int wr, int wc, int ln) const {
;         const int fr = ln & 15, fq = ln >> 4, br = u.tag & 3, row0 = u.pm * 256 + wr * 64 + fr, col0 = u.pn * 256 + (u.tag >> 2) * 128 + wc * 32 + 8 * fq;
; #pragma unroll
;         for (int ai = 0; ai < 2; ++ai)
; #pragma unroll
;             for (int m = 0; m < 4; ++m) pf[ai * 4 + m] = *(const u32x2*)(GT + (size_t)(row0 + ai * 128 + m * 16) * 4096 + br * 1024 + col0);
;     }
.LBB0_1171:
	s_and_b64 vcc, exec, s[38:39]
	s_cbranch_vccnz .LBB0_1214
	v_mbcnt_lo_u32_b32 v0, s2, 0
	v_mbcnt_hi_u32_b32 v1, s2, v0
	v_lshl_add_u32 v2, v1, 4, s27
	v_ashrrev_i32_e32 v0, 31, v2
	v_lshrrev_b32_e32 v0, 22, v0
	v_add_u32_e32 v0, v2, v0
	v_ashrrev_i32_e32 v0, 10, v0
	s_waitcnt vmcnt(0)
	v_mul_i32_i24_e32 v3, 0x400, v0
	v_sub_u32_e32 v3, v2, v3
	v_lshrrev_b32_e32 v4, 4, v3
	v_bitop3_b32 v3, v4, v3, 32 bitop3:0x6c
	v_ashrrev_i32_e32 v5, 31, v3
	v_lshrrev_b32_e32 v5, 26, v5
	v_lshlrev_b32_e32 v4, 3, v0
	v_add_u32_e32 v5, v3, v5
	v_and_b32_e32 v4, -16, v4
	v_ashrrev_i32_e32 v7, 6, v5
	v_and_b32_e32 v5, 0xc0, v5
	v_add_u32_e32 v4, v7, v4
	v_sub_u32_e32 v3, v3, v5
	v_mov_b32_e32 v12, 1
	v_lshlrev_b32_e32 v6, 5, v0
	v_ashrrev_i16_sdwa v3, v12, sext(v3) dst_sel:DWORD dst_unused:UNUSED_PAD src0_sel:DWORD src1_sel:BYTE_0
	v_lshlrev_b32_e32 v5, 1, v4
	v_lshrrev_b32_e32 v9, 2, v4
	v_and_b32_e32 v10, 3, v7
	s_mov_b32 s28, 0xffffe0
	v_and_b32_e32 v6, 32, v6
	v_bfe_i32 v8, v3, 0, 16
	v_and_b32_e32 v5, 24, v5
	v_and_b32_e32 v9, 4, v9
	v_and_or_b32 v10, v4, s28, v10
	s_movk_i32 s21, 0x500
	v_add_u32_e32 v3, v6, v8
	v_or3_b32 v5, v10, v9, v5
	v_mul_lo_u32 v4, v4, s21
	v_add_lshl_u32 v68, v3, v4, 1
	v_mul_u32_u24_e32 v4, 0x500, v5
	v_add_u32_e32 v2, 0x2000, v2
	v_add_lshl_u32 v70, v4, v3, 1
	v_ashrrev_i32_e32 v3, 31, v2
	v_lshrrev_b32_e32 v3, 22, v3
	v_add_u32_e32 v3, v2, v3
	v_ashrrev_i32_e32 v9, 10, v3
	v_mul_i32_i24_e32 v3, 0x400, v9
	v_sub_u32_e32 v2, v2, v3
	v_lshrrev_b32_e32 v3, 4, v2
	v_bitop3_b32 v2, v3, v2, 32 bitop3:0x6c
	v_ashrrev_i32_e32 v4, 31, v2
	v_lshrrev_b32_e32 v4, 26, v4
	v_add_u32_e32 v4, v2, v4
	v_ashrrev_i32_e32 v11, 6, v4
	v_and_b32_e32 v4, 0xffc0, v4
	v_sub_u32_e32 v2, v2, v4
	s_load_dwordx2 s[14:15], s[10:11], 0xf0
	v_lshlrev_b32_e32 v3, 3, v9
	v_lshrrev_b16_e32 v4, 7, v2
	v_and_b32_e32 v3, -16, v3
	v_and_b32_e32 v4, 1, v4
	v_add_u32_e32 v3, v11, v3
	v_lshlrev_b32_e32 v5, 5, v9
	v_add_u16_e32 v2, v2, v4
	v_readlane_b32 s10, v253, 2
	v_and_b32_e32 v10, 32, v5
	v_ashrrev_i16_sdwa v2, v12, sext(v2) dst_sel:DWORD dst_unused:UNUSED_PAD src0_sel:DWORD src1_sel:BYTE_0
	v_lshlrev_b32_e32 v4, 1, v3
	v_lshrrev_b32_e32 v5, 2, v3
	v_and_b32_e32 v13, 3, v11
	v_readlane_b32 s11, v253, 3
	v_bfe_i32 v12, v2, 0, 16
	v_and_b32_e32 v4, 24, v4
	v_and_b32_e32 v5, 4, v5
	v_and_or_b32 v13, v3, s28, v13
	s_load_dword s1, s[10:11], 0x0
	s_waitcnt lgkmcnt(0)
	s_add_u32 s10, s14, 0x16900000
	v_add_u32_e32 v2, v10, v12
	v_or3_b32 v4, v13, v5, v4
	v_mul_lo_u32 v3, v3, s21
	s_addc_u32 s11, s15, 0
	v_add_lshl_u32 v72, v2, v3, 1
	v_mul_u32_u24_e32 v3, 0x500, v4
	s_add_u32 s2, s14, 0x4300000
	v_add_lshl_u32 v74, v3, v2, 1
	v_mov_b32_e32 v2, v31
	v_mov_b32_e32 v3, 0x7f7f7f7f
	s_addc_u32 s3, s15, 0
	s_mov_b32 s21, -1
	s_bitcmp0_b32 s72, 0
	s_mov_b32 s13, 0xdc00000
	s_cselect_b32 s13, s13, 0x22400000
	v_mbcnt_lo_u32_b32 v3, s21, 0
	v_mbcnt_hi_u32_b32 v3, s21, v3
	s_add_u32 s13, s14, s13
	v_and_b32_e32 v4, 3, v3
	v_lshrrev_b32_e32 v3, 2, v3
	v_or_b32_e32 v3, s9, v3
	s_addc_u32 s20, s15, 0
	v_lshl_add_u32 v14, s4, 8, v3
	s_add_u32 s44, s13, s34
	v_ashrrev_i32_e32 v15, 31, v14
	s_addc_u32 s45, s20, s35
	s_lshl_b32 s21, s60, 8
	v_lshlrev_b64 v[16:17], 12, v[14:15]
	v_or_b32_e32 v18, 16, v14
	v_or_b32_e32 v20, 32, v14
	v_or_b32_e32 v14, 48, v14
	v_lshlrev_b32_e32 v4, 3, v4
	s_or_b32 s21, s21, s95
	v_ashrrev_i32_e32 v19, 31, v18
	v_ashrrev_i32_e32 v21, 31, v20
	v_ashrrev_i32_e32 v15, 31, v14
	v_add_u32_e32 v4, s21, v4
	v_lshlrev_b64 v[18:19], 12, v[18:19]
	v_lshlrev_b64 v[20:21], 12, v[20:21]
	v_lshlrev_b64 v[14:15], 12, v[14:15]
	v_ashrrev_i32_e32 v5, 31, v4
	v_lshl_add_u64 v[16:17], s[10:11], 0, v[16:17]
	v_lshl_add_u64 v[18:19], s[10:11], 0, v[18:19]
	v_lshl_add_u64 v[20:21], s[10:11], 0, v[20:21]
	v_lshl_add_u64 v[14:15], s[10:11], 0, v[14:15]
	v_lshl_add_u64 v[16:17], v[16:17], 0, v[4:5]
	v_lshl_add_u64 v[18:19], v[18:19], 0, v[4:5]
	v_lshl_add_u64 v[20:21], v[20:21], 0, v[4:5]
	v_lshl_add_u64 v[4:5], v[14:15], 0, v[4:5]
	global_load_dwordx2 v[166:167], v[16:17], off
	global_load_dwordx2 v[164:165], v[18:19], off
	global_load_dwordx2 v[162:163], v[20:21], off
	global_load_dwordx2 v[160:161], v[4:5], off
	v_add_co_u32_e32 v4, vcc, s91, v16
	s_mov_b32 s21, 0x90000
	s_nop 0
	v_addc_co_u32_e32 v5, vcc, 0, v17, vcc
	v_add_co_u32_e32 v14, vcc, s21, v16
	s_mov_b32 s21, 0xb0000
	s_nop 0
	v_addc_co_u32_e32 v15, vcc, 0, v17, vcc
	v_add_co_u32_e32 v18, vcc, s86, v16
	s_add_i32 s28, s27, 0x12000
	s_nop 0
	v_addc_co_u32_e32 v19, vcc, 0, v17, vcc
	v_add_co_u32_e32 v16, vcc, s21, v16
	s_add_i32 s21, s27, 0x10000
	s_mov_b32 m0, s21
	s_add_u32 s42, s2, s16
	v_addc_co_u32_e32 v17, vcc, 0, v17, vcc
	global_load_dwordx2 v[158:159], v[4:5], off
	global_load_dwordx2 v[156:157], v[14:15], off
	global_load_dwordx2 v[146:147], v[18:19], off
	global_load_dwordx2 v[144:145], v[16:17], off
	s_addc_u32 s43, s3, s17
	global_load_lds_dwordx4 v70, s[44:45]
	s_mov_b32 m0, s28
	s_add_i32 s29, s27, 0x2000
	global_load_lds_dwordx4 v74, s[44:45]
	s_mov_b32 m0, s27
	s_add_u32 s16, s42, 0x50000
	global_load_lds_dwordx4 v68, s[42:43]
	s_mov_b32 m0, s29
	s_addc_u32 s17, s43, 0
	s_add_i32 s31, s27, 0x4000
	global_load_lds_dwordx4 v72, s[42:43]
	s_mov_b32 m0, s31
	s_add_i32 s48, s27, 0x6000
	global_load_lds_dwordx4 v68, s[16:17]
	s_mov_b32 m0, s48
	v_mov_b32_e32 v251, 1
	global_load_lds_dwordx4 v72, s[16:17]
	v_readlane_b32 s16, v254, 2
	v_readlane_b32 s17, v254, 3
	s_andn2_b64 vcc, exec, s[16:17]
	s_nop 0
	v_cndmask_b32_e64 v3, 0, 1, s[16:17]
	v_cmp_ne_u32_e64 s[38:39], 1, v3
	s_cbranch_vccnz .LBB0_1174
	s_barrier

; __device__ __forceinline__ unsigned cvt_pk_bf16(float lo, float hi) { f32x2 v = {lo, hi}; bf16x2_t b = __builtin_convertvector(v, bf16x2_t); return __builtin_bit_cast(unsigned, b); }
;     __device__ __forceinline__ void operator()(const f32x4 (&acc)[2][2][4][2], f32x4 (&tot)[2][4][2], const u32x2 (&pf)[8], const g8::Unit& u, int wr, int wc, int fr, int fq) const {
;         const int br = u.tag & 3, row0 = u.pm * 256 + wr * 64 + fr, col0 = u.pn * 256 + (u.tag >> 2) * 128 + wc * 32 + 8 * fq;
; #pragma unroll
;         for (int ai = 0; ai < 2; ++ai)
; #pragma unroll
;             for (int m = 0; m < 4; ++m) { const int row = row0 + ai * 128 + m * 16;
;                 const u32x2 g = pf[ai * 4 + m];
;                 const f32x4 g0 = {(float)(g.x & 0xffu), (float)((g.x >> 8) & 0xffu), (float)((g.x >> 16) & 0xffu), (float)(g.x >> 24)};
;                 const f32x4 g1 = {(float)(g.y & 0xffu), (float)((g.y >> 8) & 0xffu), (float)((g.y >> 16) & 0xffu), (float)(g.y >> 24)};
;                 const f32x4 t0 = g0 * acc[ai][0][m][0], t1 = g1 * acc[ai][0][m][1];
;                 if (br == 0) { tot[ai][m][0] = t0; tot[ai][m][1] = t1; } else { tot[ai][m][0] += t0; tot[ai][m][1] += t1; }
;                 if (br == 3) { const f32x4 s0 = tot[ai][m][0] * (1.f / 255.f), s1 = tot[ai][m][1] * (1.f / 255.f);
;                     u32x4 w; w.x = cvt_pk_bf16(s0[0], s0[1]); w.y = cvt_pk_bf16(s0[2], s0[3]); w.z = cvt_pk_bf16(s1[0], s1[1]); w.w = cvt_pk_bf16(s1[2], s1[3]);
;                     *(u32x4*)(MG + (size_t)row * 1024 + col0) = w; } }
;     }
.LBB0_1193:
	s_mov_b32 s42, -1
	s_lshl_b32 s43, s61, 5
	s_and_b32 s43, s43, 0xffffff80
	v_mbcnt_lo_u32_b32 v1, s42, 0
	v_mbcnt_hi_u32_b32 v1, s42, v1
	v_and_b32_e32 v228, 60, v1
	v_and_b32_e32 v229, 3, v1
	v_lshrrev_b32_e32 v230, 4, v1
	v_lshl_or_b32 v228, v229, 6, v228
	v_and_b32_e32 v229, 15, v1
	v_lshlrev_b32_e32 v229, 4, v229
	v_lshl_or_b32 v229, v230, 2, v229
	s_lshl_b32 s42, s60, 8
	s_or_b32 s43, s43, s95
	s_and_b32 s44, s61, 3
	v_and_b32_e32 v149, 3, v1
	s_add_i32 s43, s43, s42
	s_waitcnt vmcnt(8)
	ds_bpermute_b32 v166, v229, v166
	ds_bpermute_b32 v167, v229, v167
	ds_bpermute_b32 v164, v229, v164
	ds_bpermute_b32 v165, v229, v165
	ds_bpermute_b32 v162, v229, v162
	ds_bpermute_b32 v163, v229, v163
	ds_bpermute_b32 v160, v229, v160
	ds_bpermute_b32 v161, v229, v161
	ds_bpermute_b32 v158, v229, v158
	ds_bpermute_b32 v159, v229, v159
	ds_bpermute_b32 v156, v229, v156
	ds_bpermute_b32 v157, v229, v157
	ds_bpermute_b32 v146, v229, v146
	ds_bpermute_b32 v147, v229, v147
	ds_bpermute_b32 v144, v229, v144
	ds_bpermute_b32 v145, v229, v145
	s_waitcnt lgkmcnt(0)
	v_cvt_f32_ubyte3_e32 v151, v167
	v_cvt_f32_ubyte2_e32 v150, v167
	v_lshlrev_b32_e32 v149, 3, v149
	v_cvt_f32_ubyte1_e32 v153, v166
	v_cvt_f32_ubyte0_e32 v152, v166
	v_pk_fma_f32 v[142:143], v[62:63], v[150:151], v[142:143]
	v_cvt_f32_ubyte3_e32 v173, v166
	v_cvt_f32_ubyte2_e32 v172, v166
	v_cvt_f32_ubyte1_e32 v155, v167
	v_cvt_f32_ubyte0_e32 v154, v167
	v_add_u32_e32 v168, s43, v149
	v_lshrrev_b32_e32 v1, 2, v1
	v_or_b32_e32 v1, s9, v1
	s_cmp_eq_u32 s44, 3
	v_pk_fma_f32 v[140:141], v[66:67], v[172:173], v[140:141]
	v_pk_fma_f32 v[138:139], v[64:65], v[152:153], v[138:139]
	v_pk_fma_f32 v[130:131], v[60:61], v[154:155], v[130:131]
	v_lshl_add_u32 v170, s4, 8, v1
	s_cselect_b64 s[46:47], -1, 0
	s_cmp_lg_u32 s44, 3
	v_ashrrev_i32_e32 v169, 31, v168
	s_cbranch_scc1 .LBB0_1195
	s_mov_b32 s4, 0x3b808081
	v_pk_mul_f32 v[62:63], v[140:141], s[4:5] op_sel_hi:[1,0]
	v_pk_mul_f32 v[60:61], v[138:139], s[4:5] op_sel_hi:[1,0]
	v_pk_mul_f32 v[64:65], v[142:143], s[4:5] op_sel_hi:[1,0]
	v_ashrrev_i32_e32 v171, 31, v170
	v_cvt_pk_bf16_f32 v60, v60, v61
	v_cvt_pk_bf16_f32 v61, v62, v63
	v_cvt_pk_bf16_f32 v63, v64, v65
	v_lshlrev_b64 v[64:65], 11, v[170:171]
	v_pk_mul_f32 v[66:67], v[130:131], s[4:5] op_sel_hi:[1,0]
	v_lshl_add_u64 v[64:65], s[14:15], 0, v[64:65]
	v_cvt_pk_bf16_f32 v62, v66, v67
	v_lshl_add_u64 v[64:65], v[168:169], 1, v[64:65]
	v_mov_b64_e32 v[142:143], 0
	v_mov_b64_e32 v[140:141], 0
	v_mov_b64_e32 v[138:139], 0
	v_mov_b64_e32 v[130:131], 0
	ds_bpermute_b32 v60, v228, v60
	ds_bpermute_b32 v61, v228, v61
	ds_bpermute_b32 v62, v228, v62
	ds_bpermute_b32 v63, v228, v63
	s_waitcnt lgkmcnt(0)
	global_store_dwordx4 v[64:65], v[60:63], off
.LBB0_1195:
	s_nop 1
	v_cvt_f32_ubyte1_e32 v61, v164
	v_cvt_f32_ubyte0_e32 v60, v164
	v_cvt_f32_ubyte3_e32 v63, v164
	v_cvt_f32_ubyte2_e32 v62, v164
	v_cvt_f32_ubyte1_e32 v65, v165
	v_cvt_f32_ubyte0_e32 v64, v165
	v_cvt_f32_ubyte3_e32 v67, v165
	v_cvt_f32_ubyte2_e32 v66, v165
	v_pk_fma_f32 v[136:137], v[58:59], v[62:63], v[136:137]
	v_pk_fma_f32 v[134:135], v[56:57], v[60:61], v[134:135]
	v_pk_fma_f32 v[126:127], v[54:55], v[66:67], v[126:127]
	v_pk_fma_f32 v[122:123], v[52:53], v[64:65], v[122:123]
	v_cndmask_b32_e64 v1, 0, 1, s[46:47]
	v_cmp_ne_u32_e64 s[44:45], 1, v1
	s_andn2_b64 vcc, exec, s[46:47]
	s_cbranch_vccnz .LBB0_1197
	v_or_b32_e32 v56, 16, v170
	v_ashrrev_i32_e32 v57, 31, v56
	s_mov_b32 s4, 0x3b808081
	v_lshlrev_b64 v[56:57], 11, v[56:57]
	v_pk_mul_f32 v[54:55], v[136:137], s[4:5] op_sel_hi:[1,0]
	v_pk_mul_f32 v[52:53], v[134:135], s[4:5] op_sel_hi:[1,0]
	v_pk_mul_f32 v[58:59], v[126:127], s[4:5] op_sel_hi:[1,0]
	v_pk_mul_f32 v[60:61], v[122:123], s[4:5] op_sel_hi:[1,0]
	v_lshl_add_u64 v[56:57], s[14:15], 0, v[56:57]
	v_cvt_pk_bf16_f32 v52, v52, v53
	v_cvt_pk_bf16_f32 v53, v54, v55
	v_cvt_pk_bf16_f32 v54, v60, v61
	v_cvt_pk_bf16_f32 v55, v58, v59
	v_lshl_add_u64 v[56:57], v[168:169], 1, v[56:57]
	v_mov_b64_e32 v[136:137], 0
	v_mov_b64_e32 v[134:135], 0
	v_mov_b64_e32 v[126:127], 0
	v_mov_b64_e32 v[122:123], 0
	ds_bpermute_b32 v52, v228, v52
	ds_bpermute_b32 v53, v228, v53
	ds_bpermute_b32 v54, v228, v54
	ds_bpermute_b32 v55, v228, v55
	s_waitcnt lgkmcnt(0)
	global_store_dwordx4 v[56:57], v[52:55], off
.LBB0_1197:
	s_nop 1
	v_cvt_f32_ubyte1_e32 v53, v162
	v_cvt_f32_ubyte0_e32 v52, v162
	v_cvt_f32_ubyte3_e32 v55, v162
	v_cvt_f32_ubyte2_e32 v54, v162
	v_cvt_f32_ubyte1_e32 v57, v163
	v_cvt_f32_ubyte0_e32 v56, v163
	v_cvt_f32_ubyte3_e32 v59, v163
	v_cvt_f32_ubyte2_e32 v58, v163
	v_pk_fma_f32 v[132:133], v[50:51], v[54:55], v[132:133]
	v_pk_fma_f32 v[128:129], v[48:49], v[52:53], v[128:129]
	v_pk_fma_f32 v[118:119], v[46:47], v[58:59], v[118:119]
	v_pk_fma_f32 v[114:115], v[44:45], v[56:57], v[114:115]
	s_and_b64 vcc, exec, s[44:45]
	s_cbranch_vccnz .LBB0_1199
	v_or_b32_e32 v48, 32, v170
	v_ashrrev_i32_e32 v49, 31, v48
	s_mov_b32 s4, 0x3b808081
	v_lshlrev_b64 v[48:49], 11, v[48:49]
	v_pk_mul_f32 v[46:47], v[132:133], s[4:5] op_sel_hi:[1,0]
	v_pk_mul_f32 v[44:45], v[128:129], s[4:5] op_sel_hi:[1,0]
	v_pk_mul_f32 v[50:51], v[118:119], s[4:5] op_sel_hi:[1,0]
	v_pk_mul_f32 v[52:53], v[114:115], s[4:5] op_sel_hi:[1,0]
	v_lshl_add_u64 v[48:49], s[14:15], 0, v[48:49]
	v_cvt_pk_bf16_f32 v44, v44, v45
	v_cvt_pk_bf16_f32 v45, v46, v47
	v_cvt_pk_bf16_f32 v46, v52, v53
	v_cvt_pk_bf16_f32 v47, v50, v51
	v_lshl_add_u64 v[48:49], v[168:169], 1, v[48:49]
	v_mov_b64_e32 v[132:133], 0
	v_mov_b64_e32 v[128:129], 0
	v_mov_b64_e32 v[118:119], 0
	v_mov_b64_e32 v[114:115], 0
	ds_bpermute_b32 v44, v228, v44
	ds_bpermute_b32 v45, v228, v45
	ds_bpermute_b32 v46, v228, v46
	ds_bpermute_b32 v47, v228, v47
	s_waitcnt lgkmcnt(0)
	global_store_dwordx4 v[48:49], v[44:47], off
; __device__ __forceinline__ unsigned cvt_pk_bf16(float lo, float hi) { f32x2 v = {lo, hi}; bf16x2_t b = __builtin_convertvector(v, bf16x2_t); return __builtin_bit_cast(unsigned, b); }
;     __device__ __forceinline__ void operator()(const f32x4 (&acc)[2][2][4][2], f32x4 (&tot)[2][4][2], const u32x2 (&pf)[8], const g8::Unit& u, int wr, int wc, int fr, int fq) const {
;         const int br = u.tag & 3, row0 = u.pm * 256 + wr * 64 + fr, col0 = u.pn * 256 + (u.tag >> 2) * 128 + wc * 32 + 8 * fq;
; #pragma unroll
;         for (int ai = 0; ai < 2; ++ai)
; #pragma unroll
;             for (int m = 0; m < 4; ++m) { const int row = row0 + ai * 128 + m * 16;
;                 const u32x2 g = pf[ai * 4 + m];
;                 const f32x4 g0 = {(float)(g.x & 0xffu), (float)((g.x >> 8) & 0xffu), (float)((g.x >> 16) & 0xffu), (float)(g.x >> 24)};
;                 const f32x4 g1 = {(float)(g.y & 0xffu), (float)((g.y >> 8) & 0xffu), (float)((g.y >> 16) & 0xffu), (float)(g.y >> 24)};
;                 const f32x4 t0 = g0 * acc[ai][0][m][0], t1 = g1 * acc[ai][0][m][1];
;                 if (br == 0) { tot[ai][m][0] = t0; tot[ai][m][1] = t1; } else { tot[ai][m][0] += t0; tot[ai][m][1] += t1; }
;                 if (br == 3) { const f32x4 s0 = tot[ai][m][0] * (1.f / 255.f), s1 = tot[ai][m][1] * (1.f / 255.f);
;                     u32x4 w; w.x = cvt_pk_bf16(s0[0], s0[1]); w.y = cvt_pk_bf16(s0[2], s0[3]); w.z = cvt_pk_bf16(s1[0], s1[1]); w.w = cvt_pk_bf16(s1[2], s1[3]);
;                     *(u32x4*)(MG + (size_t)row * 1024 + col0) = w; } }
;     }
.LBB0_1199:
	s_nop 1
	v_cvt_f32_ubyte1_e32 v45, v160
	v_cvt_f32_ubyte0_e32 v44, v160
	v_cvt_f32_ubyte3_e32 v47, v160
	v_cvt_f32_ubyte2_e32 v46, v160
	v_cvt_f32_ubyte1_e32 v49, v161
	v_cvt_f32_ubyte0_e32 v48, v161
	v_cvt_f32_ubyte3_e32 v51, v161
	v_cvt_f32_ubyte2_e32 v50, v161
	v_pk_fma_f32 v[124:125], v[42:43], v[46:47], v[124:125]
	v_pk_fma_f32 v[120:121], v[40:41], v[44:45], v[120:121]
	v_pk_fma_f32 v[110:111], v[38:39], v[50:51], v[110:111]
	v_pk_fma_f32 v[106:107], v[36:37], v[48:49], v[106:107]
	s_and_b64 vcc, exec, s[44:45]
	s_cbranch_vccnz .LBB0_1201
	v_or_b32_e32 v40, 48, v170
	v_ashrrev_i32_e32 v41, 31, v40
	s_mov_b32 s4, 0x3b808081
	v_lshlrev_b64 v[40:41], 11, v[40:41]
	v_pk_mul_f32 v[38:39], v[124:125], s[4:5] op_sel_hi:[1,0]
	v_pk_mul_f32 v[36:37], v[120:121], s[4:5] op_sel_hi:[1,0]
	v_pk_mul_f32 v[42:43], v[110:111], s[4:5] op_sel_hi:[1,0]
	v_pk_mul_f32 v[44:45], v[106:107], s[4:5] op_sel_hi:[1,0]
	v_lshl_add_u64 v[40:41], s[14:15], 0, v[40:41]
	v_cvt_pk_bf16_f32 v36, v36, v37
	v_cvt_pk_bf16_f32 v37, v38, v39
	v_cvt_pk_bf16_f32 v38, v44, v45
	v_cvt_pk_bf16_f32 v39, v42, v43
	v_lshl_add_u64 v[40:41], v[168:169], 1, v[40:41]
	v_mov_b64_e32 v[124:125], 0
	v_mov_b64_e32 v[120:121], 0
	v_mov_b64_e32 v[110:111], 0
	v_mov_b64_e32 v[106:107], 0
	ds_bpermute_b32 v36, v228, v36
	ds_bpermute_b32 v37, v228, v37
	ds_bpermute_b32 v38, v228, v38
	ds_bpermute_b32 v39, v228, v39
	s_waitcnt lgkmcnt(0)
	global_store_dwordx4 v[40:41], v[36:39], off
.LBB0_1201:
	s_nop 1
	v_cvt_f32_ubyte1_e32 v37, v158
	v_cvt_f32_ubyte0_e32 v36, v158
	v_cvt_f32_ubyte3_e32 v39, v158
	v_cvt_f32_ubyte2_e32 v38, v158
	v_cvt_f32_ubyte1_e32 v41, v159
	v_cvt_f32_ubyte0_e32 v40, v159
	v_cvt_f32_ubyte3_e32 v43, v159
	v_cvt_f32_ubyte2_e32 v42, v159
	v_pk_fma_f32 v[116:117], v[34:35], v[38:39], v[116:117]
	v_pk_fma_f32 v[112:113], v[32:33], v[36:37], v[112:113]
	v_pk_fma_f32 v[102:103], v[28:29], v[42:43], v[102:103]
	v_pk_fma_f32 v[98:99], v[26:27], v[40:41], v[98:99]
	s_and_b64 vcc, exec, s[44:45]
	s_cbranch_vccnz .LBB0_1203
	s_mov_b32 s4, 0x3b808081
	v_pk_mul_f32 v[28:29], v[116:117], s[4:5] op_sel_hi:[1,0]
	v_pk_mul_f32 v[26:27], v[112:113], s[4:5] op_sel_hi:[1,0]
	v_pk_mul_f32 v[32:33], v[102:103], s[4:5] op_sel_hi:[1,0]
	v_ashrrev_i32_e32 v171, 31, v170
	v_cvt_pk_bf16_f32 v26, v26, v27
	v_cvt_pk_bf16_f32 v27, v28, v29
	v_cvt_pk_bf16_f32 v29, v32, v33
	v_lshlrev_b64 v[32:33], 11, v[170:171]
	v_lshl_add_u64 v[32:33], s[14:15], 0, v[32:33]
	v_lshl_add_u64 v[32:33], v[168:169], 1, v[32:33]
	v_pk_mul_f32 v[34:35], v[98:99], s[4:5] op_sel_hi:[1,0]
	v_add_co_u32_e32 v32, vcc, 0x40000, v32
	v_cvt_pk_bf16_f32 v28, v34, v35
	s_nop 0
	v_addc_co_u32_e32 v33, vcc, 0, v33, vcc
	v_mov_b64_e32 v[116:117], 0
	v_mov_b64_e32 v[112:113], 0
	v_mov_b64_e32 v[102:103], 0
	v_mov_b64_e32 v[98:99], 0
	ds_bpermute_b32 v26, v228, v26
	ds_bpermute_b32 v27, v228, v27
	ds_bpermute_b32 v28, v228, v28
	ds_bpermute_b32 v29, v228, v29
	s_waitcnt lgkmcnt(0)
	global_store_dwordx4 v[32:33], v[26:29], off
.LBB0_1203:
	s_nop 1
	v_cvt_f32_ubyte1_e32 v27, v156
	v_cvt_f32_ubyte0_e32 v26, v156
	v_cvt_f32_ubyte3_e32 v29, v156
	v_cvt_f32_ubyte2_e32 v28, v156
	v_cvt_f32_ubyte1_e32 v33, v157
	v_cvt_f32_ubyte0_e32 v32, v157
	v_cvt_f32_ubyte3_e32 v35, v157
	v_cvt_f32_ubyte2_e32 v34, v157
	v_pk_fma_f32 v[108:109], v[24:25], v[28:29], v[108:109]
	v_pk_fma_f32 v[104:105], v[22:23], v[26:27], v[104:105]
	v_pk_fma_f32 v[94:95], v[20:21], v[34:35], v[94:95]
	v_pk_fma_f32 v[90:91], v[18:19], v[32:33], v[90:91]
	s_and_b64 vcc, exec, s[44:45]
	s_cbranch_vccnz .LBB0_1205
	s_mov_b32 s4, 0x3b808081
	v_pk_mul_f32 v[20:21], v[108:109], s[4:5] op_sel_hi:[1,0]
	v_pk_mul_f32 v[18:19], v[104:105], s[4:5] op_sel_hi:[1,0]
	v_pk_mul_f32 v[22:23], v[94:95], s[4:5] op_sel_hi:[1,0]
	v_ashrrev_i32_e32 v171, 31, v170
	v_cvt_pk_bf16_f32 v18, v18, v19
	v_cvt_pk_bf16_f32 v19, v20, v21
	v_cvt_pk_bf16_f32 v21, v22, v23
	v_lshlrev_b64 v[22:23], 11, v[170:171]
	v_lshl_add_u64 v[22:23], s[14:15], 0, v[22:23]
	v_lshl_add_u64 v[22:23], v[168:169], 1, v[22:23]
	v_pk_mul_f32 v[24:25], v[90:91], s[4:5] op_sel_hi:[1,0]
	v_add_co_u32_e32 v22, vcc, 0x48000, v22
	v_cvt_pk_bf16_f32 v20, v24, v25
	s_nop 0
	v_addc_co_u32_e32 v23, vcc, 0, v23, vcc
	v_mov_b64_e32 v[108:109], 0
	v_mov_b64_e32 v[104:105], 0
	v_mov_b64_e32 v[94:95], 0
	v_mov_b64_e32 v[90:91], 0
	ds_bpermute_b32 v18, v228, v18
	ds_bpermute_b32 v19, v228, v19
	ds_bpermute_b32 v20, v228, v20
	ds_bpermute_b32 v21, v228, v21
	s_waitcnt lgkmcnt(0)
	global_store_dwordx4 v[22:23], v[18:21], off
; __device__ __forceinline__ unsigned cvt_pk_bf16(float lo, float hi) { f32x2 v = {lo, hi}; bf16x2_t b = __builtin_convertvector(v, bf16x2_t); return __builtin_bit_cast(unsigned, b); }
;     __device__ __forceinline__ void pre(u32x2 (&pf)[8], const g8::Unit& u, int wr, int wc, int ln) const {
;         const int fr = ln & 15, fq = ln >> 4, br = u.tag & 3, row0 = u.pm * 256 + wr * 64 + fr, col0 = u.pn * 256 + (u.tag >> 2) * 128 + wc * 32 + 8 * fq;
; #pragma unroll
;         for (int ai = 0; ai < 2; ++ai)
; #pragma unroll
;             for (int m = 0; m < 4; ++m) pf[ai * 4 + m] = *(const u32x2*)(GT + (size_t)(row0 + ai * 128 + m * 16) * 4096 + br * 1024 + col0);
;     }
;     __device__ __forceinline__ void operator()(const f32x4 (&acc)[2][2][4][2], f32x4 (&tot)[2][4][2], const u32x2 (&pf)[8], const g8::Unit& u, int wr, int wc, int fr, int fq) const {
;         const int br = u.tag & 3, row0 = u.pm * 256 + wr * 64 + fr, col0 = u.pn * 256 + (u.tag >> 2) * 128 + wc * 32 + 8 * fq;
; #pragma unroll
;         for (int ai = 0; ai < 2; ++ai)
; #pragma unroll
;             for (int m = 0; m < 4; ++m) { const int row = row0 + ai * 128 + m * 16;
;                 const u32x2 g = pf[ai * 4 + m];
;                 const f32x4 g0 = {(float)(g.x & 0xffu), (float)((g.x >> 8) & 0xffu), (float)((g.x >> 16) & 0xffu), (float)(g.x >> 24)};
;                 const f32x4 g1 = {(float)(g.y & 0xffu), (float)((g.y >> 8) & 0xffu), (float)((g.y >> 16) & 0xffu), (float)(g.y >> 24)};
;                 const f32x4 t0 = g0 * acc[ai][0][m][0], t1 = g1 * acc[ai][0][m][1];
;                 if (br == 0) { tot[ai][m][0] = t0; tot[ai][m][1] = t1; } else { tot[ai][m][0] += t0; tot[ai][m][1] += t1; }
;                 if (br == 3) { const f32x4 s0 = tot[ai][m][0] * (1.f / 255.f), s1 = tot[ai][m][1] * (1.f / 255.f);
;                     u32x4 w; w.x = cvt_pk_bf16(s0[0], s0[1]); w.y = cvt_pk_bf16(s0[2], s0[3]); w.z = cvt_pk_bf16(s1[0], s1[1]); w.w = cvt_pk_bf16(s1[2], s1[3]);
;                     *(u32x4*)(MG + (size_t)row * 1024 + col0) = w; } }
;     }
.LBB0_1205:
	s_nop 1
	v_cvt_f32_ubyte1_e32 v19, v146
	v_cvt_f32_ubyte0_e32 v18, v146
	v_cvt_f32_ubyte3_e32 v21, v146
	v_cvt_f32_ubyte2_e32 v20, v146
	v_cvt_f32_ubyte1_e32 v23, v147
	v_cvt_f32_ubyte0_e32 v22, v147
	v_cvt_f32_ubyte3_e32 v25, v147
	v_cvt_f32_ubyte2_e32 v24, v147
	v_pk_fma_f32 v[100:101], v[16:17], v[20:21], v[100:101]
	v_pk_fma_f32 v[96:97], v[14:15], v[18:19], v[96:97]
	v_pk_fma_f32 v[86:87], v[12:13], v[24:25], v[86:87]
	v_pk_fma_f32 v[84:85], v[10:11], v[22:23], v[84:85]
	s_and_b64 vcc, exec, s[44:45]
	s_cbranch_vccnz .LBB0_1207
	s_mov_b32 s4, 0x3b808081
	v_pk_mul_f32 v[12:13], v[100:101], s[4:5] op_sel_hi:[1,0]
	v_pk_mul_f32 v[10:11], v[96:97], s[4:5] op_sel_hi:[1,0]
	v_pk_mul_f32 v[14:15], v[86:87], s[4:5] op_sel_hi:[1,0]
	v_ashrrev_i32_e32 v171, 31, v170
	v_cvt_pk_bf16_f32 v10, v10, v11
	v_cvt_pk_bf16_f32 v11, v12, v13
	v_cvt_pk_bf16_f32 v13, v14, v15
	v_lshlrev_b64 v[14:15], 11, v[170:171]
	v_lshl_add_u64 v[14:15], s[14:15], 0, v[14:15]
	v_lshl_add_u64 v[14:15], v[168:169], 1, v[14:15]
	v_pk_mul_f32 v[16:17], v[84:85], s[4:5] op_sel_hi:[1,0]
	v_add_co_u32_e32 v14, vcc, 0x50000, v14
	v_cvt_pk_bf16_f32 v12, v16, v17
	s_nop 0
	v_addc_co_u32_e32 v15, vcc, 0, v15, vcc
	v_mov_b64_e32 v[100:101], 0
	v_mov_b64_e32 v[96:97], 0
	v_mov_b64_e32 v[86:87], 0
	v_mov_b64_e32 v[84:85], 0
	ds_bpermute_b32 v10, v228, v10
	ds_bpermute_b32 v11, v228, v11
	ds_bpermute_b32 v12, v228, v12
	ds_bpermute_b32 v13, v228, v13
	s_waitcnt lgkmcnt(0)
	global_store_dwordx4 v[14:15], v[10:13], off
.LBB0_1207:
	s_nop 1
	v_cvt_f32_ubyte1_e32 v11, v144
	v_cvt_f32_ubyte0_e32 v10, v144
	v_cvt_f32_ubyte3_e32 v13, v144
	v_cvt_f32_ubyte2_e32 v12, v144
	v_cvt_f32_ubyte1_e32 v15, v145
	v_cvt_f32_ubyte0_e32 v14, v145
	v_cvt_f32_ubyte3_e32 v17, v145
	v_cvt_f32_ubyte2_e32 v16, v145
	v_pk_fma_f32 v[92:93], v[8:9], v[12:13], v[92:93]
	v_pk_fma_f32 v[88:89], v[6:7], v[10:11], v[88:89]
	v_pk_fma_f32 v[82:83], v[4:5], v[16:17], v[82:83]
	v_pk_fma_f32 v[80:81], v[2:3], v[14:15], v[80:81]
	s_and_b64 vcc, exec, s[44:45]
	s_cbranch_vccnz .LBB0_1209
	s_mov_b32 s4, 0x3b808081
	v_pk_mul_f32 v[4:5], v[92:93], s[4:5] op_sel_hi:[1,0]
	v_pk_mul_f32 v[2:3], v[88:89], s[4:5] op_sel_hi:[1,0]
	v_pk_mul_f32 v[6:7], v[82:83], s[4:5] op_sel_hi:[1,0]
	v_ashrrev_i32_e32 v171, 31, v170
	v_cvt_pk_bf16_f32 v2, v2, v3
	v_cvt_pk_bf16_f32 v3, v4, v5
	v_cvt_pk_bf16_f32 v5, v6, v7
	v_lshlrev_b64 v[6:7], 11, v[170:171]
	v_lshl_add_u64 v[6:7], s[14:15], 0, v[6:7]
	v_lshl_add_u64 v[6:7], v[168:169], 1, v[6:7]
	v_pk_mul_f32 v[8:9], v[80:81], s[4:5] op_sel_hi:[1,0]
	v_add_co_u32_e32 v6, vcc, 0x58000, v6
	v_cvt_pk_bf16_f32 v4, v8, v9
	s_nop 0
	v_addc_co_u32_e32 v7, vcc, 0, v7, vcc
	v_mov_b64_e32 v[92:93], 0
	v_mov_b64_e32 v[88:89], 0
	v_mov_b64_e32 v[82:83], 0
	v_mov_b64_e32 v[80:81], 0
	ds_bpermute_b32 v2, v228, v2
	ds_bpermute_b32 v3, v228, v3
	ds_bpermute_b32 v4, v228, v4
	ds_bpermute_b32 v5, v228, v5
	s_waitcnt lgkmcnt(0)
	global_store_dwordx4 v[6:7], v[2:5], off
.LBB0_1209:
	s_andn2_b64 vcc, exec, s[40:41]
	s_mov_b64 s[40:41], -1
	s_cbranch_vccnz .LBB0_1176
	s_mov_b32 s4, -1
	s_lshl_b32 s40, s57, 5
	v_mbcnt_lo_u32_b32 v1, s4, 0
	v_mbcnt_hi_u32_b32 v1, s4, v1
	v_and_b32_e32 v2, 3, v1
	v_lshrrev_b32_e32 v1, 2, v1
	v_or_b32_e32 v1, s9, v1
	v_lshl_add_u32 v4, s55, 8, v1
	v_ashrrev_i32_e32 v5, 31, v4
	s_and_b32 s40, s40, 0xffffff80
	v_lshlrev_b64 v[6:7], 12, v[4:5]
	v_or_b32_e32 v8, 16, v4
	v_or_b32_e32 v10, 32, v4
	v_or_b32_e32 v4, 48, v4
	s_lshl_b32 s4, s54, 8
	s_or_b32 s40, s40, s95
	v_ashrrev_i32_e32 v9, 31, v8
	v_ashrrev_i32_e32 v11, 31, v10
	v_ashrrev_i32_e32 v5, 31, v4
	v_lshlrev_b32_e32 v2, 3, v2
	s_add_i32 s40, s40, s4
	s_lshl_b32 s4, s57, 10
	v_lshlrev_b64 v[8:9], 12, v[8:9]
	v_lshlrev_b64 v[10:11], 12, v[10:11]
	v_lshlrev_b64 v[4:5], 12, v[4:5]
	v_add_u32_e32 v2, s40, v2
	s_and_b32 s4, s4, 0xc00
	v_lshl_add_u64 v[6:7], s[10:11], 0, v[6:7]
	v_lshl_add_u64 v[8:9], s[10:11], 0, v[8:9]
	v_lshl_add_u64 v[10:11], s[10:11], 0, v[10:11]
	v_lshl_add_u64 v[4:5], s[10:11], 0, v[4:5]
	v_ashrrev_i32_e32 v3, 31, v2
	v_lshl_add_u64 v[6:7], v[6:7], 0, s[4:5]
	v_lshl_add_u64 v[8:9], v[8:9], 0, s[4:5]
	v_lshl_add_u64 v[10:11], v[10:11], 0, s[4:5]
	v_lshl_add_u64 v[4:5], v[4:5], 0, s[4:5]
	v_lshl_add_u64 v[6:7], v[6:7], 0, v[2:3]
	v_lshl_add_u64 v[8:9], v[8:9], 0, v[2:3]
	v_lshl_add_u64 v[10:11], v[10:11], 0, v[2:3]
	v_lshl_add_u64 v[2:3], v[4:5], 0, v[2:3]
	global_load_dwordx2 v[166:167], v[6:7], off
	global_load_dwordx2 v[164:165], v[8:9], off
	global_load_dwordx2 v[162:163], v[10:11], off
	global_load_dwordx2 v[160:161], v[2:3], off
	v_add_co_u32_e32 v2, vcc, 0x80000, v6
	s_nop 1
	v_addc_co_u32_e32 v3, vcc, 0, v7, vcc
	v_add_co_u32_e32 v4, vcc, 0x90000, v6
	s_nop 1
	v_addc_co_u32_e32 v5, vcc, 0, v7, vcc
	v_add_co_u32_e32 v8, vcc, 0xa0000, v6
	s_nop 1
	v_addc_co_u32_e32 v9, vcc, 0, v7, vcc
	v_add_co_u32_e32 v6, vcc, 0xb0000, v6
	s_nop 1
	v_addc_co_u32_e32 v7, vcc, 0, v7, vcc
	global_load_dwordx2 v[158:159], v[2:3], off
	global_load_dwordx2 v[156:157], v[4:5], off
	global_load_dwordx2 v[146:147], v[8:9], off
	global_load_dwordx2 v[144:145], v[6:7], off
	s_and_b64 vcc, exec, s[38:39]
	s_cbranch_vccnz .LBB0_1175
	s_barrier
	s_branch .LBB0_1175

; __device__ __forceinline__ unsigned pk_fp8x4(float a, float b, float c_, float d) { int p = __builtin_amdgcn_cvt_pk_fp8_f32(a, b, 0, false); p = __builtin_amdgcn_cvt_pk_fp8_f32(c_, d, p, true); return (unsigned)p; }
;     __device__ __forceinline__ void operator()(const f32x4 (&acc)[2][2][4][2], const g8::Unit& u, int wr, int wc, int fr, int fq) const {
;         const int row0 = u.pm * 256 + wr * 64 + fr, col0 = u.pn * 256 + wc * 32 + 8 * fq;
; #pragma unroll
;         for (int ai = 0; ai < 2; ++ai)
; #pragma unroll
;             for (int m = 0; m < 4; ++m) { unsigned char* rp = O + (size_t)(row0 + ai * 128 + m * 16) * 1024 + col0;
; #pragma unroll
;                 for (int bj = 0; bj < 2; ++bj) { const f32x4 v0 = acc[ai][bj][m][0] * 0.0625f, v1 = acc[ai][bj][m][1] * 0.0625f;
;                     *(u32x2*)(rp + bj * 128) = (u32x2){pk_fp8x4(v0[0], v0[1], v0[2], v0[3]), pk_fp8x4(v1[0], v1[1], v1[2], v1[3])}; } }
;     }
.LBB0_1731:
	v_pk_mul_f32 v[8:9], v[144:145], s[8:9] op_sel_hi:[1,0]
	v_pk_mul_f32 v[12:13], v[140:141], s[8:9] op_sel_hi:[1,0]
	v_mov_b32_e32 v14, v31
	v_mov_b32_e32 v15, v31
	s_mov_b32 s45, -1
	v_cvt_pk_fp8_f32 v14, v8, v9
	v_cvt_pk_fp8_f32 v15, v12, v13
	s_lshl_b32 s44, s44, 8
	v_mbcnt_lo_u32_b32 v0, s45, 0
	v_mbcnt_hi_u32_b32 v0, s45, v0
	s_add_i32 s44, s44, s9
	v_and_b32_e32 v149, 60, v0
	v_and_b32_e32 v150, 3, v0
	v_lshrrev_b32_e32 v4, 2, v0
	v_lshl_or_b32 v149, v150, 6, v149
	v_or_b32_e32 v4, s44, v4
	s_lshl_b32 s44, s69, 8
	v_and_b32_e32 v0, 3, v0
	v_pk_mul_f32 v[6:7], v[146:147], s[8:9] op_sel_hi:[1,0]
	v_pk_mul_f32 v[10:11], v[142:143], s[8:9] op_sel_hi:[1,0]
	s_or_b32 s44, s44, s95
	v_lshlrev_b32_e32 v0, 3, v0
	v_ashrrev_i32_e32 v5, 31, v4
	v_cvt_pk_fp8_f32 v14, v6, v7 op_sel:[0,0,1]
	v_cvt_pk_fp8_f32 v15, v10, v11 op_sel:[0,0,1]
	v_add_u32_e32 v2, s44, v0
	v_lshlrev_b64 v[0:1], 10, v[4:5]
	v_ashrrev_i32_e32 v3, 31, v2
	v_lshl_add_u64 v[0:1], s[14:15], 0, v[0:1]
	v_lshl_add_u64 v[0:1], v[0:1], 0, v[2:3]
	ds_bpermute_b32 v14, v149, v14
	ds_bpermute_b32 v15, v149, v15
	s_waitcnt lgkmcnt(0)
	global_store_dwordx2 v[0:1], v[14:15], off
	v_pk_mul_f32 v[8:9], v[136:137], s[8:9] op_sel_hi:[1,0]
	v_pk_mul_f32 v[12:13], v[132:133], s[8:9] op_sel_hi:[1,0]
	v_mov_b32_e32 v14, v31
	v_mov_b32_e32 v15, v31
	v_cvt_pk_fp8_f32 v14, v8, v9
	v_cvt_pk_fp8_f32 v15, v12, v13
	v_pk_mul_f32 v[6:7], v[138:139], s[8:9] op_sel_hi:[1,0]
	v_pk_mul_f32 v[10:11], v[134:135], s[8:9] op_sel_hi:[1,0]
	v_cvt_pk_fp8_f32 v14, v6, v7 op_sel:[0,0,1]
	v_cvt_pk_fp8_f32 v15, v10, v11 op_sel:[0,0,1]
	v_pk_mul_f32 v[10:11], v[128:129], s[8:9] op_sel_hi:[1,0]
	v_pk_mul_f32 v[8:9], v[130:131], s[8:9] op_sel_hi:[1,0]
	v_pk_mul_f32 v[12:13], v[126:127], s[8:9] op_sel_hi:[1,0]
	ds_bpermute_b32 v14, v149, v14
	ds_bpermute_b32 v15, v149, v15
	s_waitcnt lgkmcnt(0)
	global_store_dwordx2 v[0:1], v[14:15], off offset:128
	v_pk_mul_f32 v[14:15], v[124:125], s[8:9] op_sel_hi:[1,0]
	v_mov_b32_e32 v124, v31
	v_mov_b32_e32 v125, v31
	v_cvt_pk_fp8_f32 v124, v10, v11
	v_cvt_pk_fp8_f32 v125, v14, v15
	v_pk_mul_f32 v[10:11], v[120:121], s[8:9] op_sel_hi:[1,0]
	v_pk_mul_f32 v[14:15], v[116:117], s[8:9] op_sel_hi:[1,0]
	v_mov_b32_e32 v116, v31
	v_mov_b32_e32 v117, v31
	v_cvt_pk_fp8_f32 v116, v10, v11
	v_cvt_pk_fp8_f32 v117, v14, v15
	v_or_b32_e32 v6, 16, v4
	v_cvt_pk_fp8_f32 v124, v8, v9 op_sel:[0,0,1]
	v_cvt_pk_fp8_f32 v125, v12, v13 op_sel:[0,0,1]
	v_pk_mul_f32 v[8:9], v[122:123], s[8:9] op_sel_hi:[1,0]
	v_pk_mul_f32 v[12:13], v[118:119], s[8:9] op_sel_hi:[1,0]
	v_pk_mul_f32 v[10:11], v[112:113], s[8:9] op_sel_hi:[1,0]
	v_pk_mul_f32 v[14:15], v[108:109], s[8:9] op_sel_hi:[1,0]
	v_mov_b32_e32 v108, v31
	v_mov_b32_e32 v109, v31
	v_ashrrev_i32_e32 v7, 31, v6
	v_cvt_pk_fp8_f32 v116, v8, v9 op_sel:[0,0,1]
	v_cvt_pk_fp8_f32 v117, v12, v13 op_sel:[0,0,1]
	v_cvt_pk_fp8_f32 v108, v10, v11
	v_cvt_pk_fp8_f32 v109, v14, v15
	v_pk_mul_f32 v[10:11], v[104:105], s[8:9] op_sel_hi:[1,0]
	v_pk_mul_f32 v[14:15], v[100:101], s[8:9] op_sel_hi:[1,0]
	v_mov_b32_e32 v100, v31
	v_mov_b32_e32 v101, v31
	v_lshlrev_b64 v[6:7], 10, v[6:7]
	v_cvt_pk_fp8_f32 v100, v10, v11
	v_cvt_pk_fp8_f32 v101, v14, v15
	v_lshl_add_u64 v[6:7], s[14:15], 0, v[6:7]
	v_lshl_add_u64 v[6:7], v[6:7], 0, v[2:3]
	v_pk_mul_f32 v[8:9], v[114:115], s[8:9] op_sel_hi:[1,0]
	v_pk_mul_f32 v[12:13], v[110:111], s[8:9] op_sel_hi:[1,0]
	ds_bpermute_b32 v124, v149, v124
	ds_bpermute_b32 v125, v149, v125
	s_waitcnt lgkmcnt(0)
	global_store_dwordx2 v[6:7], v[124:125], off
	ds_bpermute_b32 v116, v149, v116
	ds_bpermute_b32 v117, v149, v117
	s_waitcnt lgkmcnt(0)
	global_store_dwordx2 v[6:7], v[116:117], off offset:128
	v_or_b32_e32 v6, 32, v4
	v_cvt_pk_fp8_f32 v108, v8, v9 op_sel:[0,0,1]
	v_cvt_pk_fp8_f32 v109, v12, v13 op_sel:[0,0,1]
	v_pk_mul_f32 v[8:9], v[106:107], s[8:9] op_sel_hi:[1,0]
	v_pk_mul_f32 v[12:13], v[102:103], s[8:9] op_sel_hi:[1,0]
	v_ashrrev_i32_e32 v7, 31, v6
	v_cvt_pk_fp8_f32 v100, v8, v9 op_sel:[0,0,1]
	v_cvt_pk_fp8_f32 v101, v12, v13 op_sel:[0,0,1]
	v_lshlrev_b64 v[6:7], 10, v[6:7]
	v_lshl_add_u64 v[6:7], s[14:15], 0, v[6:7]
	v_lshl_add_u64 v[6:7], v[6:7], 0, v[2:3]
	ds_bpermute_b32 v108, v149, v108
	ds_bpermute_b32 v109, v149, v109
	s_waitcnt lgkmcnt(0)
	global_store_dwordx2 v[6:7], v[108:109], off
	ds_bpermute_b32 v100, v149, v100
	ds_bpermute_b32 v101, v149, v101
	s_waitcnt lgkmcnt(0)
	global_store_dwordx2 v[6:7], v[100:101], off offset:128
	v_or_b32_e32 v4, 48, v4
	v_pk_mul_f32 v[6:7], v[96:97], s[8:9] op_sel_hi:[1,0]
	v_pk_mul_f32 v[10:11], v[92:93], s[8:9] op_sel_hi:[1,0]
	v_mov_b32_e32 v12, v31
	v_mov_b32_e32 v13, v31
	v_ashrrev_i32_e32 v5, 31, v4
	v_cvt_pk_fp8_f32 v12, v6, v7
	v_cvt_pk_fp8_f32 v13, v10, v11
	v_lshlrev_b64 v[4:5], 10, v[4:5]
	v_lshl_add_u64 v[4:5], s[14:15], 0, v[4:5]
	v_lshl_add_u64 v[2:3], v[4:5], 0, v[2:3]
	v_pk_mul_f32 v[4:5], v[98:99], s[8:9] op_sel_hi:[1,0]
	v_pk_mul_f32 v[8:9], v[94:95], s[8:9] op_sel_hi:[1,0]
	v_cvt_pk_fp8_f32 v12, v4, v5 op_sel:[0,0,1]
	v_cvt_pk_fp8_f32 v13, v8, v9 op_sel:[0,0,1]
	v_pk_mul_f32 v[6:7], v[88:89], s[8:9] op_sel_hi:[1,0]
	v_pk_mul_f32 v[10:11], v[84:85], s[8:9] op_sel_hi:[1,0]
	v_pk_mul_f32 v[4:5], v[90:91], s[8:9] op_sel_hi:[1,0]
	ds_bpermute_b32 v12, v149, v12
	ds_bpermute_b32 v13, v149, v13
	s_waitcnt lgkmcnt(0)
; __device__ __forceinline__ unsigned pk_fp8x4(float a, float b, float c_, float d) { int p = __builtin_amdgcn_cvt_pk_fp8_f32(a, b, 0, false); p = __builtin_amdgcn_cvt_pk_fp8_f32(c_, d, p, true); return (unsigned)p; }
;     __device__ __forceinline__ void operator()(const f32x4 (&acc)[2][2][4][2], const g8::Unit& u, int wr, int wc, int fr, int fq) const {
;         const int row0 = u.pm * 256 + wr * 64 + fr, col0 = u.pn * 256 + wc * 32 + 8 * fq;
; #pragma unroll
;         for (int ai = 0; ai < 2; ++ai)
; #pragma unroll
;             for (int m = 0; m < 4; ++m) { unsigned char* rp = O + (size_t)(row0 + ai * 128 + m * 16) * 1024 + col0;
; #pragma unroll
;                 for (int bj = 0; bj < 2; ++bj) { const f32x4 v0 = acc[ai][bj][m][0] * 0.0625f, v1 = acc[ai][bj][m][1] * 0.0625f;
;                     *(u32x2*)(rp + bj * 128) = (u32x2){pk_fp8x4(v0[0], v0[1], v0[2], v0[3]), pk_fp8x4(v1[0], v1[1], v1[2], v1[3])}; } }
;     }
	global_store_dwordx2 v[2:3], v[12:13], off
	v_mov_b32_e32 v12, v31
	v_mov_b32_e32 v13, v31
	v_cvt_pk_fp8_f32 v12, v6, v7
	v_cvt_pk_fp8_f32 v13, v10, v11
	v_pk_mul_f32 v[8:9], v[86:87], s[8:9] op_sel_hi:[1,0]
	v_pk_mul_f32 v[6:7], v[80:81], s[8:9] op_sel_hi:[1,0]
	v_cvt_pk_fp8_f32 v12, v4, v5 op_sel:[0,0,1]
	v_cvt_pk_fp8_f32 v13, v8, v9 op_sel:[0,0,1]
	v_pk_mul_f32 v[10:11], v[76:77], s[8:9] op_sel_hi:[1,0]
	v_pk_mul_f32 v[4:5], v[82:83], s[8:9] op_sel_hi:[1,0]
	v_pk_mul_f32 v[8:9], v[78:79], s[8:9] op_sel_hi:[1,0]
	ds_bpermute_b32 v12, v149, v12
	ds_bpermute_b32 v13, v149, v13
	s_waitcnt lgkmcnt(0)
	global_store_dwordx2 v[2:3], v[12:13], off offset:128
	v_mov_b32_e32 v12, v31
	v_mov_b32_e32 v13, v31
	v_cvt_pk_fp8_f32 v12, v6, v7
	v_cvt_pk_fp8_f32 v13, v10, v11
	s_mov_b64 s[44:45], 0x20000
	v_lshl_add_u64 v[2:3], v[0:1], 0, s[44:45]
	v_cvt_pk_fp8_f32 v12, v4, v5 op_sel:[0,0,1]
	v_cvt_pk_fp8_f32 v13, v8, v9 op_sel:[0,0,1]
	s_mov_b32 s44, 0x20000
	v_add_co_u32_e32 v4, vcc, s44, v0
	v_pk_mul_f32 v[6:7], v[72:73], s[8:9] op_sel_hi:[1,0]
	s_nop 0
	v_addc_co_u32_e32 v5, vcc, 0, v1, vcc
	ds_bpermute_b32 v12, v149, v12
	ds_bpermute_b32 v13, v149, v13
	s_waitcnt lgkmcnt(0)
	global_store_dwordx2 v[4:5], v[12:13], off
	v_pk_mul_f32 v[10:11], v[68:69], s[8:9] op_sel_hi:[1,0]
	v_mov_b32_e32 v12, v31
	v_mov_b32_e32 v13, v31
	v_cvt_pk_fp8_f32 v12, v6, v7
	v_cvt_pk_fp8_f32 v13, v10, v11
	v_pk_mul_f32 v[4:5], v[74:75], s[8:9] op_sel_hi:[1,0]
	v_pk_mul_f32 v[8:9], v[70:71], s[8:9] op_sel_hi:[1,0]
	v_cvt_pk_fp8_f32 v12, v4, v5 op_sel:[0,0,1]
	v_cvt_pk_fp8_f32 v13, v8, v9 op_sel:[0,0,1]
	v_pk_mul_f32 v[6:7], v[64:65], s[8:9] op_sel_hi:[1,0]
	v_pk_mul_f32 v[10:11], v[60:61], s[8:9] op_sel_hi:[1,0]
	v_pk_mul_f32 v[4:5], v[66:67], s[8:9] op_sel_hi:[1,0]
	ds_bpermute_b32 v12, v149, v12
	ds_bpermute_b32 v13, v149, v13
	s_waitcnt lgkmcnt(0)
	global_store_dwordx2 v[2:3], v[12:13], off offset:128
	v_mov_b32_e32 v12, v31
	v_mov_b32_e32 v13, v31
	v_cvt_pk_fp8_f32 v12, v6, v7
	v_cvt_pk_fp8_f32 v13, v10, v11
	v_pk_mul_f32 v[8:9], v[62:63], s[8:9] op_sel_hi:[1,0]
	s_mov_b64 s[44:45], 0x24000
	v_cvt_pk_fp8_f32 v12, v4, v5 op_sel:[0,0,1]
	v_cvt_pk_fp8_f32 v13, v8, v9 op_sel:[0,0,1]
	v_lshl_add_u64 v[2:3], v[0:1], 0, s[44:45]
	s_mov_b32 s44, 0x24000
	v_add_co_u32_e32 v4, vcc, s44, v0
	v_pk_mul_f32 v[6:7], v[56:57], s[8:9] op_sel_hi:[1,0]
	s_nop 0
	v_addc_co_u32_e32 v5, vcc, 0, v1, vcc
	ds_bpermute_b32 v12, v149, v12
	ds_bpermute_b32 v13, v149, v13
	s_waitcnt lgkmcnt(0)
	global_store_dwordx2 v[4:5], v[12:13], off
	v_pk_mul_f32 v[10:11], v[52:53], s[8:9] op_sel_hi:[1,0]
	v_mov_b32_e32 v12, v31
	v_mov_b32_e32 v13, v31
	v_cvt_pk_fp8_f32 v12, v6, v7
	v_cvt_pk_fp8_f32 v13, v10, v11
	v_pk_mul_f32 v[4:5], v[58:59], s[8:9] op_sel_hi:[1,0]
	v_pk_mul_f32 v[8:9], v[54:55], s[8:9] op_sel_hi:[1,0]
	v_cvt_pk_fp8_f32 v12, v4, v5 op_sel:[0,0,1]
	v_cvt_pk_fp8_f32 v13, v8, v9 op_sel:[0,0,1]
	v_pk_mul_f32 v[6:7], v[48:49], s[8:9] op_sel_hi:[1,0]
	v_pk_mul_f32 v[10:11], v[44:45], s[8:9] op_sel_hi:[1,0]
	v_pk_mul_f32 v[4:5], v[50:51], s[8:9] op_sel_hi:[1,0]
	ds_bpermute_b32 v12, v149, v12
	ds_bpermute_b32 v13, v149, v13
	s_waitcnt lgkmcnt(0)
	global_store_dwordx2 v[2:3], v[12:13], off offset:128
	v_mov_b32_e32 v12, v31
	v_mov_b32_e32 v13, v31
	v_cvt_pk_fp8_f32 v12, v6, v7
	v_cvt_pk_fp8_f32 v13, v10, v11
	v_pk_mul_f32 v[8:9], v[46:47], s[8:9] op_sel_hi:[1,0]
	s_mov_b64 s[44:45], 0x28000
	v_cvt_pk_fp8_f32 v12, v4, v5 op_sel:[0,0,1]
	v_cvt_pk_fp8_f32 v13, v8, v9 op_sel:[0,0,1]
	v_lshl_add_u64 v[2:3], v[0:1], 0, s[44:45]
	s_mov_b32 s44, 0x28000
	v_add_co_u32_e32 v4, vcc, s44, v0
	v_pk_mul_f32 v[6:7], v[40:41], s[8:9] op_sel_hi:[1,0]
	s_nop 0
	v_addc_co_u32_e32 v5, vcc, 0, v1, vcc
	ds_bpermute_b32 v12, v149, v12
	ds_bpermute_b32 v13, v149, v13
	s_waitcnt lgkmcnt(0)
	global_store_dwordx2 v[4:5], v[12:13], off
	v_pk_mul_f32 v[10:11], v[36:37], s[8:9] op_sel_hi:[1,0]
	v_mov_b32_e32 v12, v31
	v_mov_b32_e32 v13, v31
	v_cvt_pk_fp8_f32 v12, v6, v7
	v_cvt_pk_fp8_f32 v13, v10, v11
	v_pk_mul_f32 v[4:5], v[42:43], s[8:9] op_sel_hi:[1,0]
	v_pk_mul_f32 v[8:9], v[38:39], s[8:9] op_sel_hi:[1,0]
	v_cvt_pk_fp8_f32 v12, v4, v5 op_sel:[0,0,1]
	v_cvt_pk_fp8_f32 v13, v8, v9 op_sel:[0,0,1]
	v_pk_mul_f32 v[6:7], v[32:33], s[8:9] op_sel_hi:[1,0]
	v_pk_mul_f32 v[10:11], v[26:27], s[8:9] op_sel_hi:[1,0]
	v_pk_mul_f32 v[4:5], v[34:35], s[8:9] op_sel_hi:[1,0]
	ds_bpermute_b32 v12, v149, v12
	ds_bpermute_b32 v13, v149, v13
	s_waitcnt lgkmcnt(0)
	global_store_dwordx2 v[2:3], v[12:13], off offset:128
	v_mov_b32_e32 v12, v31
	v_mov_b32_e32 v13, v31
	v_cvt_pk_fp8_f32 v12, v6, v7
	v_cvt_pk_fp8_f32 v13, v10, v11
	v_pk_mul_f32 v[8:9], v[28:29], s[8:9] op_sel_hi:[1,0]
	s_mov_b64 s[44:45], 0x2c000
	v_cvt_pk_fp8_f32 v12, v4, v5 op_sel:[0,0,1]
	v_cvt_pk_fp8_f32 v13, v8, v9 op_sel:[0,0,1]
	v_pk_mul_f32 v[4:5], v[22:23], s[8:9] op_sel_hi:[1,0]
	v_pk_mul_f32 v[8:9], v[16:17], s[8:9] op_sel_hi:[1,0]
	v_mov_b32_e32 v10, v31
	v_mov_b32_e32 v11, v31
	v_lshl_add_u64 v[2:3], v[0:1], 0, s[44:45]
	s_mov_b32 s44, 0x2c000
	v_cvt_pk_fp8_f32 v10, v4, v5
	v_cvt_pk_fp8_f32 v11, v8, v9
	v_add_co_u32_e32 v0, vcc, s44, v0
	v_pk_mul_f32 v[6:7], v[18:19], s[8:9] op_sel_hi:[1,0]
	s_nop 0
	v_addc_co_u32_e32 v1, vcc, 0, v1, vcc
	ds_bpermute_b32 v12, v149, v12
	ds_bpermute_b32 v13, v149, v13
	s_waitcnt lgkmcnt(0)
	global_store_dwordx2 v[0:1], v[12:13], off
	v_pk_mul_f32 v[0:1], v[24:25], s[8:9] op_sel_hi:[1,0]
	v_cvt_pk_fp8_f32 v11, v6, v7 op_sel:[0,0,1]
	v_cvt_pk_fp8_f32 v10, v0, v1 op_sel:[0,0,1]
	s_mov_b64 s[44:45], -1
	s_andn2_b64 vcc, exec, s[42:43]
	ds_bpermute_b32 v10, v149, v10
	ds_bpermute_b32 v11, v149, v11
	s_waitcnt lgkmcnt(0)
	global_store_dwordx2 v[2:3], v[10:11], off offset:128
	s_cbranch_vccnz .LBB0_1723
	s_and_b64 vcc, exec, s[38:39]
	s_cbranch_vccnz .LBB0_1722
	s_barrier
	s_branch .LBB0_1722
